# node0 x-row loads hoisted ahead of the staging barrier; U3 work packed into the first 768 blocks (4 tiles per block, 53 waves take a second tile) so the grid runs in one residency round
# speedup vs baseline: 1.1323x; 1.0083x over previous
_Z14k_bcount_node0ItEvPKiPiS2_PKfS4_S4_S4_PK15HIP_vector_typeIjLj4EEPtPT_SB_:
	s_cmpk_gt_u32 s2, 0xf4
	s_mov_b64 s[4:5], -1
	s_cbranch_scc0 .LBB5_8
	s_load_dwordx2 s[8:9], s[0:1], 0x20
	s_load_dwordx2 s[6:7], s[0:1], 0x38
	s_load_dwordx2 s[20:21], s[0:1], 0x18
	s_load_dword s22, s[0:1], 0x58
	v_mov_b32_e32 v3, 0
	v_lshlrev_b32_e32 v2, 4, v0
	v_cmp_gt_u32_e64 s[4:5], 16, v0
	s_waitcnt lgkmcnt(0)
	s_add_i32 s22, s22, 0xffffff0b
	s_add_i32 s23, s2, 0xffffff0b
	v_lshrrev_b32_e32 v150, 6, v0
	v_mul_lo_u32 v150, s22, v150
	v_add_u32_e32 v150, s23, v150
	v_min_u32_e32 v150, 0xc34, v150
	v_and_b32_e32 v151, 31, v0
	v_lshl_or_b32 v150, v150, 5, v151
	v_mul_u32_u24_e32 v150, 0xc4, v150
	global_load_dwordx4 v[100:103], v150, s[20:21]
	global_load_dwordx4 v[104:107], v150, s[20:21] offset:16
	global_load_dwordx4 v[108:111], v150, s[20:21] offset:32
	global_load_dwordx4 v[112:115], v150, s[20:21] offset:48
	global_load_dwordx4 v[116:119], v150, s[20:21] offset:64
	global_load_dwordx4 v[120:123], v150, s[20:21] offset:80
	global_load_dwordx4 v[124:127], v150, s[20:21] offset:96
	global_load_dwordx4 v[128:131], v150, s[20:21] offset:112
	global_load_dwordx4 v[132:135], v150, s[20:21] offset:128
	global_load_dwordx4 v[136:139], v150, s[20:21] offset:144
	global_load_dwordx4 v[140:143], v150, s[20:21] offset:160
	global_load_dwordx4 v[144:147], v150, s[20:21] offset:176
	global_load_dword v148, v150, s[20:21] offset:192
	v_lshl_add_u64 v[4:5], s[8:9], 0, v[2:3]
	v_mov_b32_e32 v6, v3
	v_mov_b32_e32 v7, v3
	v_mov_b32_e32 v8, v3
	v_mov_b32_e32 v9, v3
	s_and_saveexec_b64 s[8:9], s[4:5]
	s_cbranch_execz .LBB5_3
	v_add_co_u32_e32 v6, vcc, 0x3000, v4
	s_nop 1
	v_addc_co_u32_e32 v7, vcc, 0, v5, vcc
	global_load_dwordx4 v[6:9], v[6:7], off
.LBB5_3:
	s_or_b64 exec, exec, s[8:9]
	v_lshl_add_u64 v[38:39], s[6:7], 0, v[2:3]
	v_add_co_u32_e32 v30, vcc, 0x1000, v38
	v_or_b32_e32 v1, 0x4000, v2
	s_nop 0
	v_addc_co_u32_e32 v31, vcc, 0, v39, vcc
	v_add_co_u32_e32 v32, vcc, 0x2000, v38
	global_load_dwordx4 v[10:13], v2, s[6:7]
	s_nop 0
	v_addc_co_u32_e32 v33, vcc, 0, v39, vcc
	v_add_co_u32_e32 v34, vcc, 0x3000, v38
	s_nop 1
	v_addc_co_u32_e32 v35, vcc, 0, v39, vcc
	v_add_co_u32_e32 v40, vcc, 0x5000, v38
	global_load_dwordx4 v[14:17], v[32:33], off
	global_load_dwordx4 v[18:21], v[34:35], off
	global_load_dwordx4 v[22:25], v[30:31], off
	global_load_dwordx4 v[26:29], v1, s[6:7]
	v_addc_co_u32_e32 v41, vcc, 0, v39, vcc
	v_add_co_u32_e32 v42, vcc, 0x6000, v38
	s_nop 1
	v_addc_co_u32_e32 v43, vcc, 0, v39, vcc
	v_add_co_u32_e32 v46, vcc, 0x7000, v38
	global_load_dwordx4 v[30:33], v[40:41], off
	global_load_dwordx4 v[34:37], v[42:43], off
	v_addc_co_u32_e32 v47, vcc, 0, v39, vcc
	v_add_co_u32_e32 v54, vcc, 0x1000, v4
	global_load_dwordx4 v[38:41], v[46:47], off
	global_load_dwordx4 v[42:45], v[4:5], off
	v_addc_co_u32_e32 v55, vcc, 0, v5, vcc
	v_add_co_u32_e32 v4, vcc, 0x2000, v4
	s_nop 1
	v_addc_co_u32_e32 v5, vcc, 0, v5, vcc
	global_load_dwordx4 v[46:49], v[54:55], off
	global_load_dwordx4 v[50:53], v[4:5], off
	s_load_dword s3, s[0:1], 0x58
	s_waitcnt vmcnt(10)
	ds_write_b128 v2, v[10:13]
	s_waitcnt vmcnt(7)
	ds_write_b128 v2, v[22:25] offset:4096
	s_waitcnt vmcnt(6)
	ds_write_b128 v2, v[26:29] offset:16384
	ds_write_b128 v2, v[14:17] offset:8192
	ds_write_b128 v2, v[18:21] offset:12288
	s_waitcnt vmcnt(5)
	ds_write_b128 v2, v[30:33] offset:20480
	s_waitcnt vmcnt(4)
	ds_write_b128 v2, v[34:37] offset:24576
	s_waitcnt vmcnt(3)
	ds_write_b128 v2, v[38:41] offset:28672
	s_waitcnt vmcnt(2)
	ds_write_b128 v2, v[42:45] offset:32768
	s_waitcnt vmcnt(1)
	ds_write_b128 v2, v[46:49] offset:36864
	s_waitcnt vmcnt(0)
	ds_write_b128 v2, v[50:53] offset:40960
	s_and_saveexec_b64 s[6:7], s[4:5]
	ds_write_b128 v2, v[6:9] offset:45056
	s_or_b64 exec, exec, s[6:7]
	s_waitcnt lgkmcnt(0)
	s_addk_i32 s3, 0xff0b
	v_lshrrev_b32_e32 v1, 6, v0
	s_add_i32 s4, s2, 0xffffff0b
	v_mul_lo_u32 v1, s3, v1
	v_add_u32_e32 v1, s4, v1
	s_movk_i32 s3, 0xc35
	v_cmp_gt_i32_e32 vcc, s3, v1
	s_barrier
	s_and_saveexec_b64 s[8:9], vcc
	s_cbranch_execz .LBB5_7
	s_load_dwordx2 s[4:5], s[0:1], 0x18
	s_load_dwordx2 s[10:11], s[0:1], 0x50
	v_lshlrev_b32_e32 v69, 5, v1
	v_and_b32_e32 v1, 31, v0
	s_movk_i32 s3, 0xc4
	v_or_b32_e32 v66, v69, v1
	s_waitcnt lgkmcnt(0)
	v_mov_b64_e32 v[2:3], s[4:5]
	v_mad_i64_i32 v[50:51], s[4:5], v66, s3, v[2:3]
	s_waitcnt vmcnt(0)
	v_mov_b32_e32 v46, v100
	v_mov_b32_e32 v47, v101
	v_mov_b32_e32 v48, v102
	v_mov_b32_e32 v49, v103
	v_mov_b32_e32 v42, v104
	v_mov_b32_e32 v43, v105
	v_mov_b32_e32 v44, v106
	v_mov_b32_e32 v45, v107
	v_mov_b32_e32 v38, v108
	v_mov_b32_e32 v39, v109
	v_mov_b32_e32 v40, v110
	v_mov_b32_e32 v41, v111
	v_mov_b32_e32 v34, v112
	v_mov_b32_e32 v35, v113
	v_mov_b32_e32 v36, v114
	v_mov_b32_e32 v37, v115
	v_mov_b32_e32 v30, v116
	v_mov_b32_e32 v31, v117
	v_mov_b32_e32 v32, v118
	v_mov_b32_e32 v33, v119
	v_mov_b32_e32 v26, v120
	v_mov_b32_e32 v27, v121
	v_mov_b32_e32 v28, v122
	v_mov_b32_e32 v29, v123
	v_mov_b32_e32 v22, v124
	v_mov_b32_e32 v23, v125
	v_mov_b32_e32 v24, v126
	v_mov_b32_e32 v25, v127
	v_mov_b32_e32 v18, v128
	v_mov_b32_e32 v19, v129
	v_mov_b32_e32 v20, v130
	v_mov_b32_e32 v21, v131
	v_mov_b32_e32 v14, v132
	v_mov_b32_e32 v15, v133
	v_mov_b32_e32 v16, v134
	v_mov_b32_e32 v17, v135
	v_mov_b32_e32 v10, v136
	v_mov_b32_e32 v11, v137
	v_mov_b32_e32 v12, v138
	v_mov_b32_e32 v13, v139
	v_mov_b32_e32 v6, v140
	v_mov_b32_e32 v7, v141
	v_mov_b32_e32 v8, v142
	v_mov_b32_e32 v9, v143
	v_mov_b32_e32 v2, v144
	v_mov_b32_e32 v3, v145
	v_mov_b32_e32 v4, v146
	v_mov_b32_e32 v5, v147
	v_mov_b32_e32 v68, v148
	s_load_dwordx4 s[4:7], s[0:1], 0x28
	v_and_b32_e32 v71, 32, v0
	v_lshlrev_b32_e32 v50, 2, v71
	v_and_b32_e32 v72, 63, v0
	s_waitcnt vmcnt(5)
	v_mov_b32_e32 v70, v49
	s_waitcnt vmcnt(0)
	s_waitcnt lgkmcnt(0)
	global_load_dwordx4 v[58:61], v50, s[4:5] offset:112
	global_load_dwordx4 v[74:77], v50, s[4:5] offset:96
	global_load_dwordx4 v[78:81], v50, s[4:5] offset:80
	global_load_dwordx4 v[82:85], v50, s[4:5] offset:64
	global_load_dwordx4 v[86:89], v50, s[4:5]
	global_load_dwordx4 v[90:93], v50, s[4:5] offset:48
	global_load_dwordx4 v[94:97], v50, s[4:5] offset:16
	global_load_dwordx4 v[98:101], v50, s[4:5] offset:32
	v_lshlrev_b32_e32 v50, 2, v0
	v_and_b32_e32 v67, 0x80, v50
	ds_read_b128 v[102:105], v67 offset:32880
	ds_read_b128 v[106:109], v67 offset:32864
	ds_read_b128 v[110:113], v67 offset:33136
	ds_read_b128 v[114:117], v67 offset:33120
	ds_read_b128 v[118:121], v67 offset:33392
	ds_read_b128 v[122:125], v67 offset:33376
	ds_read_b128 v[126:129], v67 offset:32848
	ds_read_b128 v[130:133], v67 offset:32832
	ds_read_b128 v[134:137], v67 offset:33104
	ds_read_b128 v[138:141], v67 offset:33088
	ds_read_b128 v[142:145], v67 offset:33360
	ds_read_b128 v[146:149], v67 offset:33344
	ds_read_b128 v[62:65], v67 offset:33616
	ds_read_b128 v[50:53], v67 offset:33600
	ds_read_b128 v[54:57], v67 offset:33632
	s_waitcnt vmcnt(7) lgkmcnt(14)
	v_pk_fma_f32 v[104:105], v[46:47], v[104:105], v[60:61] op_sel_hi:[0,1,1]
	s_waitcnt vmcnt(6) lgkmcnt(13)
	v_pk_fma_f32 v[108:109], v[46:47], v[108:109], v[76:77] op_sel_hi:[0,1,1]
	v_pk_fma_f32 v[106:107], v[46:47], v[106:107], v[74:75] op_sel_hi:[0,1,1]
	ds_read_b128 v[74:77], v67 offset:32768
	s_waitcnt vmcnt(5) lgkmcnt(9)
	v_pk_fma_f32 v[128:129], v[46:47], v[128:129], v[80:81] op_sel_hi:[0,1,1]
	v_pk_fma_f32 v[126:127], v[46:47], v[126:127], v[78:79] op_sel_hi:[0,1,1]
	ds_read_b128 v[78:81], v67 offset:32816
	s_waitcnt vmcnt(4) lgkmcnt(9)
	v_pk_fma_f32 v[132:133], v[46:47], v[132:133], v[84:85] op_sel_hi:[0,1,1]
	v_pk_fma_f32 v[130:131], v[46:47], v[130:131], v[82:83] op_sel_hi:[0,1,1]
	ds_read_b128 v[82:85], v67 offset:32784
	s_waitcnt vmcnt(3) lgkmcnt(2)
	v_pk_fma_f32 v[150:151], v[46:47], v[74:75], v[86:87] op_sel_hi:[0,1,1]
	v_pk_fma_f32 v[152:153], v[46:47], v[76:77], v[88:89] op_sel_hi:[0,1,1]
	ds_read_b128 v[74:77], v67 offset:32800
	s_waitcnt vmcnt(2) lgkmcnt(2)
	v_pk_fma_f32 v[154:155], v[46:47], v[80:81], v[92:93] op_sel_hi:[0,1,1]
	v_pk_fma_f32 v[156:157], v[46:47], v[78:79], v[90:91] op_sel_hi:[0,1,1]
	ds_read_b128 v[78:81], v67 offset:33072
	s_waitcnt vmcnt(1) lgkmcnt(2)
	v_pk_fma_f32 v[158:159], v[46:47], v[82:83], v[94:95] op_sel_hi:[0,1,1]
	v_pk_fma_f32 v[160:161], v[46:47], v[84:85], v[96:97] op_sel_hi:[0,1,1]
	ds_read_b128 v[82:85], v67 offset:33024
	v_pk_fma_f32 v[102:103], v[46:47], v[102:103], v[58:59] op_sel_hi:[0,1,1]
	ds_read_b128 v[58:61], v67 offset:33648
	s_waitcnt vmcnt(0) lgkmcnt(3)
	v_pk_fma_f32 v[162:163], v[46:47], v[76:77], v[100:101] op_sel_hi:[0,1,1]
	v_pk_fma_f32 v[164:165], v[46:47], v[74:75], v[98:99] op_sel_hi:[0,1,1]
	ds_read_b128 v[74:77], v67 offset:33040
	ds_read_b128 v[86:89], v67 offset:33280
	ds_read_b128 v[90:93], v67 offset:33296
	v_pk_fma_f32 v[128:129], v[46:47], v[136:137], v[128:129] op_sel:[1,0,0]
	v_pk_fma_f32 v[126:127], v[46:47], v[134:135], v[126:127] op_sel:[1,0,0]
	s_waitcnt lgkmcnt(4)
	v_pk_fma_f32 v[134:135], v[46:47], v[82:83], v[150:151] op_sel:[1,0,0]
	v_pk_fma_f32 v[136:137], v[46:47], v[84:85], v[152:153] op_sel:[1,0,0]
	ds_read_b128 v[82:85], v67 offset:33056
	v_pk_fma_f32 v[112:113], v[46:47], v[112:113], v[104:105] op_sel:[1,0,0]
	v_pk_fma_f32 v[110:111], v[46:47], v[110:111], v[102:103] op_sel:[1,0,0]
	v_pk_fma_f32 v[116:117], v[46:47], v[116:117], v[108:109] op_sel:[1,0,0]
	v_pk_fma_f32 v[114:115], v[46:47], v[114:115], v[106:107] op_sel:[1,0,0]
	ds_read_b128 v[94:97], v67 offset:33536
	ds_read_b128 v[98:101], v67 offset:33552
	v_pk_fma_f32 v[132:133], v[46:47], v[140:141], v[132:133] op_sel:[1,0,0]
	v_pk_fma_f32 v[130:131], v[46:47], v[138:139], v[130:131] op_sel:[1,0,0]
	v_pk_fma_f32 v[138:139], v[46:47], v[80:81], v[154:155] op_sel:[1,0,0]
	v_pk_fma_f32 v[140:141], v[46:47], v[78:79], v[156:157] op_sel:[1,0,0]
	s_waitcnt lgkmcnt(5)
	v_pk_fma_f32 v[150:151], v[46:47], v[74:75], v[158:159] op_sel:[1,0,0]
	v_pk_fma_f32 v[152:153], v[46:47], v[76:77], v[160:161] op_sel:[1,0,0]
	ds_read_b128 v[74:77], v67 offset:33328
	s_waitcnt lgkmcnt(3)
	v_pk_fma_f32 v[154:155], v[46:47], v[84:85], v[162:163] op_sel:[1,0,0]
	v_pk_fma_f32 v[46:47], v[46:47], v[82:83], v[164:165] op_sel:[1,0,0]
	ds_read_b128 v[82:85], v67 offset:33312
	ds_read_b128 v[106:109], v67 offset:33584
	ds_read_b128 v[102:105], v67 offset:33792
	ds_read_b128 v[78:81], v67 offset:33808
	v_pk_fma_f32 v[156:157], v[48:49], v[120:121], v[112:113] op_sel_hi:[0,1,1]
	v_pk_fma_f32 v[158:159], v[48:49], v[118:119], v[110:111] op_sel_hi:[0,1,1]
	ds_read_b128 v[110:113], v67 offset:33568
	v_pk_fma_f32 v[128:129], v[48:49], v[144:145], v[128:129] op_sel_hi:[0,1,1]
	v_pk_fma_f32 v[126:127], v[48:49], v[142:143], v[126:127] op_sel_hi:[0,1,1]
	v_pk_fma_f32 v[124:125], v[48:49], v[124:125], v[116:117] op_sel_hi:[0,1,1]
	v_pk_fma_f32 v[122:123], v[48:49], v[122:123], v[114:115] op_sel_hi:[0,1,1]
	ds_read_b128 v[114:117], v67 offset:33824
	ds_read_b128 v[118:121], v67 offset:33840
	v_pk_fma_f32 v[134:135], v[48:49], v[86:87], v[134:135] op_sel_hi:[0,1,1]
	v_pk_fma_f32 v[136:137], v[48:49], v[88:89], v[136:137] op_sel_hi:[0,1,1]
	ds_read_b128 v[86:89], v67 offset:33856
	v_pk_fma_f32 v[142:143], v[48:49], v[90:91], v[150:151] op_sel_hi:[0,1,1]
	v_pk_fma_f32 v[144:145], v[48:49], v[92:93], v[152:153] op_sel_hi:[0,1,1]
	v_pk_fma_f32 v[150:151], v[70:71], v[62:63], v[126:127] op_sel_hi:[0,1,1]
	v_pk_fma_f32 v[152:153], v[70:71], v[64:65], v[128:129] op_sel_hi:[0,1,1]
	ds_read_b128 v[62:65], v67 offset:34048
	ds_read_b128 v[126:129], v67 offset:34304
	v_pk_fma_f32 v[130:131], v[48:49], v[146:147], v[130:131] op_sel_hi:[0,1,1]
	s_waitcnt lgkmcnt(10)
	v_pk_fma_f32 v[138:139], v[48:49], v[76:77], v[138:139] op_sel_hi:[0,1,1]
	v_pk_fma_f32 v[140:141], v[48:49], v[74:75], v[140:141] op_sel_hi:[0,1,1]
	s_waitcnt lgkmcnt(9)
	v_pk_fma_f32 v[146:147], v[48:49], v[84:85], v[154:155] op_sel_hi:[0,1,1]
	v_pk_fma_f32 v[154:155], v[70:71], v[58:59], v[158:159] op_sel_hi:[0,1,1]
	v_pk_fma_f32 v[156:157], v[70:71], v[60:61], v[156:157] op_sel_hi:[0,1,1]
	v_pk_fma_f32 v[58:59], v[70:71], v[94:95], v[134:135] op_sel_hi:[0,1,1]
	v_pk_fma_f32 v[60:61], v[70:71], v[96:97], v[136:137] op_sel_hi:[0,1,1]
	ds_read_b128 v[94:97], v67 offset:34560
	v_pk_fma_f32 v[132:133], v[48:49], v[148:149], v[132:133] op_sel_hi:[0,1,1]
	v_pk_fma_f32 v[148:149], v[48:49], v[82:83], v[46:47] op_sel_hi:[0,1,1]
	s_waitcnt lgkmcnt(9)
	v_pk_fma_f32 v[134:135], v[70:71], v[108:109], v[138:139] op_sel_hi:[0,1,1]
	v_pk_fma_f32 v[136:137], v[70:71], v[106:107], v[140:141] op_sel_hi:[0,1,1]
	v_pk_fma_f32 v[138:139], v[70:71], v[98:99], v[142:143] op_sel_hi:[0,1,1]
	v_pk_fma_f32 v[140:141], v[70:71], v[100:101], v[144:145] op_sel_hi:[0,1,1]
	ds_read_b128 v[98:101], v67 offset:34816
	v_pk_fma_f32 v[50:51], v[70:71], v[50:51], v[130:131] op_sel_hi:[0,1,1]
	s_waitcnt lgkmcnt(7)
	v_pk_fma_f32 v[142:143], v[70:71], v[112:113], v[146:147] op_sel_hi:[0,1,1]
	v_pk_fma_f32 v[144:145], v[70:71], v[110:111], v[148:149] op_sel_hi:[0,1,1]
	v_pk_fma_f32 v[146:147], v[42:43], v[102:103], v[58:59] op_sel_hi:[0,1,1]
	v_pk_fma_f32 v[148:149], v[42:43], v[104:105], v[60:61] op_sel_hi:[0,1,1]
	ds_read_b128 v[102:105], v67 offset:35072
	ds_read_b128 v[74:77], v67 offset:33872
	v_pk_fma_f32 v[54:55], v[70:71], v[54:55], v[122:123] op_sel_hi:[0,1,1]
	v_pk_fma_f32 v[56:57], v[70:71], v[56:57], v[124:125] op_sel_hi:[0,1,1]
	ds_read_b128 v[122:125], v67 offset:34064
	s_waitcnt lgkmcnt(9)
	v_pk_fma_f32 v[144:145], v[42:43], v[114:115], v[144:145] op_sel_hi:[0,1,1]
	v_pk_fma_f32 v[142:143], v[42:43], v[116:117], v[142:143] op_sel_hi:[0,1,1]
	ds_read_b128 v[114:117], v67 offset:35328
	s_waitcnt lgkmcnt(8)
	v_pk_fma_f32 v[158:159], v[42:43], v[86:87], v[50:51] op_sel_hi:[0,1,1]
	s_waitcnt lgkmcnt(7)
	v_pk_fma_f32 v[50:51], v[42:43], v[62:63], v[146:147] op_sel:[1,0,0]
	v_pk_fma_f32 v[62:63], v[42:43], v[64:65], v[148:149] op_sel:[1,0,0]
	v_mov_b32_e32 v48, v45
	v_pk_fma_f32 v[52:53], v[70:71], v[52:53], v[132:133] op_sel_hi:[0,1,1]
	ds_read_b128 v[130:133], v67 offset:34320
	s_waitcnt lgkmcnt(7)
	v_pk_fma_f32 v[62:63], v[44:45], v[128:129], v[62:63] op_sel_hi:[0,1,1]
	ds_read_b128 v[106:109], v67 offset:34576
	s_waitcnt lgkmcnt(7)
	v_pk_fma_f32 v[62:63], v[48:49], v[96:97], v[62:63] op_sel_hi:[0,1,1]
	ds_read_b128 v[110:113], v67 offset:34832
	s_waitcnt lgkmcnt(7)
	v_pk_fma_f32 v[62:63], v[38:39], v[100:101], v[62:63] op_sel_hi:[0,1,1]
	v_pk_fma_f32 v[138:139], v[42:43], v[78:79], v[138:139] op_sel_hi:[0,1,1]
	v_pk_fma_f32 v[140:141], v[42:43], v[80:81], v[140:141] op_sel_hi:[0,1,1]
	ds_read_b128 v[78:81], v67 offset:35088
	s_waitcnt lgkmcnt(7)
	v_pk_fma_f32 v[62:63], v[38:39], v[104:105], v[62:63] op_sel:[1,0,0]
	v_pk_fma_f32 v[136:137], v[42:43], v[118:119], v[136:137] op_sel_hi:[0,1,1]
	v_pk_fma_f32 v[134:135], v[42:43], v[120:121], v[134:135] op_sel_hi:[0,1,1]
	ds_read_b128 v[118:121], v67 offset:35344
	s_waitcnt lgkmcnt(5)
	v_pk_fma_f32 v[128:129], v[40:41], v[116:117], v[62:63] op_sel_hi:[0,1,1]
	v_pk_fma_f32 v[62:63], v[42:43], v[122:123], v[138:139] op_sel:[1,0,0]
	ds_read_b128 v[90:93], v67 offset:33888
	ds_read_b128 v[82:85], v67 offset:33904
	s_waitcnt lgkmcnt(6)
	v_pk_fma_f32 v[62:63], v[44:45], v[130:131], v[62:63] op_sel_hi:[0,1,1]
	s_waitcnt lgkmcnt(5)
	v_pk_fma_f32 v[62:63], v[48:49], v[106:107], v[62:63] op_sel_hi:[0,1,1]
	s_waitcnt lgkmcnt(4)
	v_pk_fma_f32 v[62:63], v[38:39], v[110:111], v[62:63] op_sel_hi:[0,1,1]
	s_waitcnt lgkmcnt(3)
	v_pk_fma_f32 v[62:63], v[38:39], v[78:79], v[62:63] op_sel:[1,0,0]
	v_pk_fma_f32 v[150:151], v[42:43], v[74:75], v[150:151] op_sel_hi:[0,1,1]
	s_waitcnt lgkmcnt(2)
	v_pk_fma_f32 v[118:119], v[40:41], v[118:119], v[62:63] op_sel_hi:[0,1,1]
	v_pk_fma_f32 v[62:63], v[42:43], v[124:125], v[140:141] op_sel:[1,0,0]
	v_pk_fma_f32 v[60:61], v[42:43], v[76:77], v[152:153] op_sel_hi:[0,1,1]
	v_pk_fma_f32 v[62:63], v[44:45], v[132:133], v[62:63] op_sel_hi:[0,1,1]
	v_pk_fma_f32 v[62:63], v[48:49], v[108:109], v[62:63] op_sel_hi:[0,1,1]
	v_pk_fma_f32 v[74:75], v[38:39], v[112:113], v[62:63] op_sel_hi:[0,1,1]
	ds_read_b128 v[62:65], v67 offset:34080
	v_pk_fma_f32 v[74:75], v[38:39], v[80:81], v[74:75] op_sel:[1,0,0]
	v_pk_fma_f32 v[160:161], v[42:43], v[88:89], v[52:53] op_sel_hi:[0,1,1]
	v_pk_fma_f32 v[120:121], v[40:41], v[120:121], v[74:75] op_sel_hi:[0,1,1]
	ds_read_b128 v[74:77], v67 offset:34336
	ds_read_b128 v[78:81], v67 offset:34096
	s_waitcnt lgkmcnt(4)
	v_pk_fma_f32 v[58:59], v[42:43], v[90:91], v[54:55] op_sel_hi:[0,1,1]
	s_waitcnt lgkmcnt(3)
	v_pk_fma_f32 v[54:55], v[42:43], v[82:83], v[154:155] op_sel_hi:[0,1,1]
	v_pk_fma_f32 v[52:53], v[42:43], v[84:85], v[156:157] op_sel_hi:[0,1,1]
	v_pk_fma_f32 v[50:51], v[44:45], v[126:127], v[50:51] op_sel_hi:[0,1,1]
	ds_read_b128 v[82:85], v67 offset:34592
	ds_read_b128 v[86:89], v67 offset:34352
	v_pk_fma_f32 v[56:57], v[42:43], v[92:93], v[56:57] op_sel_hi:[0,1,1]
	v_pk_fma_f32 v[50:51], v[48:49], v[94:95], v[50:51] op_sel_hi:[0,1,1]
	ds_read_b128 v[90:93], v67 offset:34848
	ds_read_b128 v[94:97], v67 offset:34608
	v_pk_fma_f32 v[50:51], v[38:39], v[98:99], v[50:51] op_sel_hi:[0,1,1]
	s_waitcnt lgkmcnt(6)
	v_pk_fma_f32 v[62:63], v[42:43], v[62:63], v[144:145] op_sel:[1,0,0]
	v_pk_fma_f32 v[50:51], v[38:39], v[102:103], v[50:51] op_sel:[1,0,0]
	s_waitcnt lgkmcnt(5)
	v_pk_fma_f32 v[62:63], v[44:45], v[74:75], v[62:63] op_sel_hi:[0,1,1]
	ds_read_b128 v[98:101], v67 offset:35104
	ds_read_b128 v[102:105], v67 offset:35360
	ds_read_b128 v[106:109], v67 offset:34864
	s_waitcnt lgkmcnt(6)
	v_pk_fma_f32 v[62:63], v[48:49], v[82:83], v[62:63] op_sel_hi:[0,1,1]
	s_waitcnt lgkmcnt(4)
	v_pk_fma_f32 v[62:63], v[38:39], v[90:91], v[62:63] op_sel_hi:[0,1,1]
	s_waitcnt lgkmcnt(2)
	v_pk_fma_f32 v[62:63], v[38:39], v[98:99], v[62:63] op_sel:[1,0,0]
	v_mov_b32_e32 v46, v41
	s_waitcnt lgkmcnt(1)
	v_pk_fma_f32 v[82:83], v[40:41], v[102:103], v[62:63] op_sel_hi:[0,1,1]
	v_pk_fma_f32 v[62:63], v[42:43], v[64:65], v[142:143] op_sel:[1,0,0]
	v_pk_fma_f32 v[126:127], v[40:41], v[114:115], v[50:51] op_sel_hi:[0,1,1]
	v_pk_fma_f32 v[62:63], v[44:45], v[76:77], v[62:63] op_sel_hi:[0,1,1]
	v_pk_fma_f32 v[74:75], v[48:49], v[84:85], v[62:63] op_sel_hi:[0,1,1]
	ds_read_b128 v[62:65], v67 offset:35584
	v_pk_fma_f32 v[84:85], v[38:39], v[92:93], v[74:75] op_sel_hi:[0,1,1]
	ds_read_b128 v[74:77], v67 offset:35600
	ds_read_b128 v[110:113], v67 offset:35120
	ds_read_b128 v[114:117], v67 offset:35376
	s_waitcnt lgkmcnt(3)
	v_pk_fma_f32 v[126:127], v[46:47], v[62:63], v[126:127] op_sel_hi:[0,1,1]
	v_pk_fma_f32 v[62:63], v[42:43], v[78:79], v[136:137] op_sel:[1,0,0]
	v_pk_fma_f32 v[128:129], v[46:47], v[64:65], v[128:129] op_sel_hi:[0,1,1]
	v_pk_fma_f32 v[62:63], v[44:45], v[86:87], v[62:63] op_sel_hi:[0,1,1]
	s_waitcnt lgkmcnt(2)
	v_pk_fma_f32 v[130:131], v[46:47], v[74:75], v[118:119] op_sel_hi:[0,1,1]
	v_pk_fma_f32 v[74:75], v[48:49], v[94:95], v[62:63] op_sel_hi:[0,1,1]
	ds_read_b128 v[62:65], v67 offset:35616
	v_pk_fma_f32 v[132:133], v[46:47], v[76:77], v[120:121] op_sel_hi:[0,1,1]
	v_pk_fma_f32 v[78:79], v[38:39], v[106:107], v[74:75] op_sel_hi:[0,1,1]
	ds_read_b128 v[74:77], v67 offset:35632
	v_pk_fma_f32 v[84:85], v[38:39], v[100:101], v[84:85] op_sel:[1,0,0]
	s_waitcnt lgkmcnt(1)
	v_pk_fma_f32 v[136:137], v[46:47], v[62:63], v[82:83] op_sel_hi:[0,1,1]
	v_pk_fma_f32 v[62:63], v[42:43], v[80:81], v[134:135] op_sel:[1,0,0]
	v_pk_fma_f32 v[78:79], v[38:39], v[110:111], v[78:79] op_sel:[1,0,0]
	v_pk_fma_f32 v[62:63], v[44:45], v[88:89], v[62:63] op_sel_hi:[0,1,1]
	v_pk_fma_f32 v[62:63], v[48:49], v[96:97], v[62:63] op_sel_hi:[0,1,1]
	v_pk_fma_f32 v[84:85], v[40:41], v[104:105], v[84:85] op_sel_hi:[0,1,1]
	v_pk_fma_f32 v[78:79], v[40:41], v[114:115], v[78:79] op_sel_hi:[0,1,1]
	v_pk_fma_f32 v[62:63], v[38:39], v[108:109], v[62:63] op_sel_hi:[0,1,1]
	v_pk_fma_f32 v[138:139], v[46:47], v[64:65], v[84:85] op_sel_hi:[0,1,1]
	s_waitcnt lgkmcnt(0)
	v_pk_fma_f32 v[140:141], v[46:47], v[74:75], v[78:79] op_sel_hi:[0,1,1]
	v_pk_fma_f32 v[74:75], v[38:39], v[112:113], v[62:63] op_sel:[1,0,0]
	ds_read_b128 v[62:65], v67 offset:34112
	v_pk_fma_f32 v[74:75], v[40:41], v[116:117], v[74:75] op_sel_hi:[0,1,1]
	v_pk_fma_f32 v[134:135], v[46:47], v[76:77], v[74:75] op_sel_hi:[0,1,1]
	ds_read_b128 v[74:77], v67 offset:34368
	ds_read_b128 v[78:81], v67 offset:34128
	ds_read_b128 v[82:85], v67 offset:34624
	ds_read_b128 v[86:89], v67 offset:34384
	ds_read_b128 v[90:93], v67 offset:34880
	ds_read_b128 v[94:97], v67 offset:34640
	s_waitcnt lgkmcnt(6)
	v_pk_fma_f32 v[62:63], v[42:43], v[62:63], v[158:159] op_sel:[1,0,0]
	ds_read_b128 v[98:101], v67 offset:35136
	ds_read_b128 v[102:105], v67 offset:34896
	s_waitcnt lgkmcnt(7)
	v_pk_fma_f32 v[62:63], v[44:45], v[74:75], v[62:63] op_sel_hi:[0,1,1]
	s_waitcnt lgkmcnt(5)
	v_pk_fma_f32 v[62:63], v[48:49], v[82:83], v[62:63] op_sel_hi:[0,1,1]
	ds_read_b128 v[106:109], v67 offset:35392
	ds_read_b128 v[110:113], v67 offset:35648
	ds_read_b128 v[114:117], v67 offset:35152
	s_waitcnt lgkmcnt(6)
	v_pk_fma_f32 v[62:63], v[38:39], v[90:91], v[62:63] op_sel_hi:[0,1,1]
	s_waitcnt lgkmcnt(4)
	v_pk_fma_f32 v[62:63], v[38:39], v[98:99], v[62:63] op_sel:[1,0,0]
	ds_read_b128 v[118:121], v67 offset:35408
	s_waitcnt lgkmcnt(3)
	v_pk_fma_f32 v[62:63], v[40:41], v[106:107], v[62:63] op_sel_hi:[0,1,1]
	s_waitcnt lgkmcnt(2)
	v_pk_fma_f32 v[90:91], v[46:47], v[110:111], v[62:63] op_sel_hi:[0,1,1]
	v_pk_fma_f32 v[62:63], v[42:43], v[64:65], v[160:161] op_sel:[1,0,0]
	v_pk_fma_f32 v[60:61], v[42:43], v[80:81], v[60:61] op_sel:[1,0,0]
	v_pk_fma_f32 v[62:63], v[44:45], v[76:77], v[62:63] op_sel_hi:[0,1,1]
	v_pk_fma_f32 v[62:63], v[48:49], v[84:85], v[62:63] op_sel_hi:[0,1,1]
	v_pk_fma_f32 v[74:75], v[38:39], v[92:93], v[62:63] op_sel_hi:[0,1,1]
	v_pk_fma_f32 v[74:75], v[38:39], v[100:101], v[74:75] op_sel:[1,0,0]
	ds_read_b128 v[62:65], v67 offset:35840
	v_pk_fma_f32 v[82:83], v[40:41], v[108:109], v[74:75] op_sel_hi:[0,1,1]
	ds_read_b128 v[74:77], v67 offset:35856
	v_pk_fma_f32 v[92:93], v[46:47], v[112:113], v[82:83] op_sel_hi:[0,1,1]
	ds_read_b128 v[82:85], v67 offset:35872
	s_waitcnt lgkmcnt(2)
	v_pk_fma_f32 v[126:127], v[34:35], v[62:63], v[126:127] op_sel_hi:[0,1,1]
	v_pk_fma_f32 v[128:129], v[34:35], v[64:65], v[128:129] op_sel_hi:[0,1,1]
	s_waitcnt lgkmcnt(1)
	v_pk_fma_f32 v[130:131], v[34:35], v[74:75], v[130:131] op_sel_hi:[0,1,1]
	v_pk_fma_f32 v[74:75], v[42:43], v[78:79], v[150:151] op_sel:[1,0,0]
	v_pk_fma_f32 v[132:133], v[34:35], v[76:77], v[132:133] op_sel_hi:[0,1,1]
	v_pk_fma_f32 v[74:75], v[44:45], v[86:87], v[74:75] op_sel_hi:[0,1,1]
	v_pk_fma_f32 v[74:75], v[48:49], v[94:95], v[74:75] op_sel_hi:[0,1,1]
	v_pk_fma_f32 v[74:75], v[38:39], v[102:103], v[74:75] op_sel_hi:[0,1,1]
	v_pk_fma_f32 v[74:75], v[38:39], v[114:115], v[74:75] op_sel:[1,0,0]
	ds_read_b128 v[62:65], v67 offset:35888
	v_pk_fma_f32 v[78:79], v[40:41], v[118:119], v[74:75] op_sel_hi:[0,1,1]
	ds_read_b128 v[74:77], v67 offset:35904
	ds_read_b128 v[122:125], v67 offset:35664
	v_pk_fma_f32 v[60:61], v[44:45], v[88:89], v[60:61] op_sel_hi:[0,1,1]
	s_waitcnt lgkmcnt(3)
	v_pk_fma_f32 v[136:137], v[34:35], v[82:83], v[136:137] op_sel_hi:[0,1,1]
	v_pk_fma_f32 v[138:139], v[34:35], v[84:85], v[138:139] op_sel_hi:[0,1,1]
	ds_read_b128 v[82:85], v67 offset:35920
	v_pk_fma_f32 v[60:61], v[48:49], v[96:97], v[60:61] op_sel_hi:[0,1,1]
	v_pk_fma_f32 v[60:61], v[38:39], v[104:105], v[60:61] op_sel_hi:[0,1,1]
	v_pk_fma_f32 v[60:61], v[38:39], v[116:117], v[60:61] op_sel:[1,0,0]
	s_waitcnt lgkmcnt(3)
	v_pk_fma_f32 v[140:141], v[34:35], v[62:63], v[140:141] op_sel_hi:[0,1,1]
	v_pk_fma_f32 v[64:65], v[34:35], v[64:65], v[134:135] op_sel_hi:[0,1,1]
	s_waitcnt lgkmcnt(2)
	v_pk_fma_f32 v[134:135], v[34:35], v[74:75], v[90:91] op_sel_hi:[0,1,1]
	v_pk_fma_f32 v[74:75], v[40:41], v[120:121], v[60:61] op_sel_hi:[0,1,1]
	ds_read_b128 v[60:63], v67 offset:34144
	s_waitcnt lgkmcnt(2)
	v_pk_fma_f32 v[78:79], v[46:47], v[122:123], v[78:79] op_sel_hi:[0,1,1]
	v_pk_fma_f32 v[74:75], v[46:47], v[124:125], v[74:75] op_sel_hi:[0,1,1]
	v_pk_fma_f32 v[142:143], v[34:35], v[76:77], v[92:93] op_sel_hi:[0,1,1]
	s_waitcnt lgkmcnt(1)
	v_pk_fma_f32 v[144:145], v[34:35], v[82:83], v[78:79] op_sel_hi:[0,1,1]
	v_pk_fma_f32 v[146:147], v[34:35], v[84:85], v[74:75] op_sel_hi:[0,1,1]
	ds_read_b128 v[74:77], v67 offset:34400
	ds_read_b128 v[78:81], v67 offset:34160
	s_waitcnt lgkmcnt(2)
	v_pk_fma_f32 v[86:87], v[42:43], v[60:61], v[58:59] op_sel:[1,0,0]
	ds_read_b128 v[58:61], v67 offset:34656
	ds_read_b128 v[82:85], v67 offset:34416
	v_pk_fma_f32 v[56:57], v[42:43], v[62:63], v[56:57] op_sel:[1,0,0]
	s_waitcnt lgkmcnt(3)
	v_pk_fma_f32 v[74:75], v[44:45], v[74:75], v[86:87] op_sel_hi:[0,1,1]
	ds_read_b128 v[86:89], v67 offset:34912
	ds_read_b128 v[90:93], v67 offset:34672
	ds_read_b128 v[94:97], v67 offset:35168
	ds_read_b128 v[98:101], v67 offset:34928
	ds_read_b128 v[102:105], v67 offset:35424
	ds_read_b128 v[106:109], v67 offset:35184
	ds_read_b128 v[110:113], v67 offset:36096
	ds_read_b128 v[114:117], v67 offset:35680
	ds_read_b128 v[118:121], v67 offset:35440
	s_waitcnt lgkmcnt(10)
	v_pk_fma_f32 v[58:59], v[48:49], v[58:59], v[74:75] op_sel_hi:[0,1,1]
	s_waitcnt lgkmcnt(8)
	v_pk_fma_f32 v[58:59], v[38:39], v[86:87], v[58:59] op_sel_hi:[0,1,1]
	ds_read_b128 v[122:125], v67 offset:36112
	s_waitcnt lgkmcnt(7)
	v_pk_fma_f32 v[58:59], v[38:39], v[94:95], v[58:59] op_sel:[1,0,0]
	s_waitcnt lgkmcnt(3)
	v_pk_fma_f32 v[86:87], v[34:35], v[110:111], v[126:127] op_sel:[1,0,0]
	v_pk_fma_f32 v[94:95], v[34:35], v[112:113], v[128:129] op_sel:[1,0,0]
	ds_read_b128 v[110:113], v67 offset:36128
	ds_read_b128 v[126:129], v67 offset:35696
	v_pk_fma_f32 v[58:59], v[40:41], v[102:103], v[58:59] op_sel_hi:[0,1,1]
	s_waitcnt lgkmcnt(2)
	v_pk_fma_f32 v[102:103], v[34:35], v[122:123], v[130:131] op_sel:[1,0,0]
	v_pk_fma_f32 v[130:131], v[34:35], v[124:125], v[132:133] op_sel:[1,0,0]
	ds_read_b128 v[122:125], v67 offset:36144
	s_waitcnt lgkmcnt(2)
	v_pk_fma_f32 v[132:133], v[34:35], v[110:111], v[136:137] op_sel:[1,0,0]
	v_pk_fma_f32 v[136:137], v[34:35], v[112:113], v[138:139] op_sel:[1,0,0]
	ds_read_b128 v[110:113], v67 offset:35936
	v_pk_fma_f32 v[56:57], v[44:45], v[76:77], v[56:57] op_sel_hi:[0,1,1]
	v_pk_fma_f32 v[56:57], v[48:49], v[60:61], v[56:57] op_sel_hi:[0,1,1]
	v_pk_fma_f32 v[56:57], v[38:39], v[88:89], v[56:57] op_sel_hi:[0,1,1]
	v_pk_fma_f32 v[60:61], v[38:39], v[96:97], v[56:57] op_sel:[1,0,0]
	v_pk_fma_f32 v[58:59], v[46:47], v[114:115], v[58:59] op_sel_hi:[0,1,1]
	v_pk_fma_f32 v[60:61], v[40:41], v[104:105], v[60:61] op_sel_hi:[0,1,1]
	v_pk_fma_f32 v[74:75], v[46:47], v[116:117], v[60:61] op_sel_hi:[0,1,1]
	ds_read_b128 v[60:63], v67 offset:36176
	s_waitcnt lgkmcnt(2)
	v_pk_fma_f32 v[114:115], v[34:35], v[122:123], v[140:141] op_sel:[1,0,0]
	v_pk_fma_f32 v[64:65], v[34:35], v[124:125], v[64:65] op_sel:[1,0,0]
	ds_read_b128 v[122:125], v67 offset:35952
	s_waitcnt lgkmcnt(2)
	v_pk_fma_f32 v[110:111], v[34:35], v[110:111], v[58:59] op_sel_hi:[0,1,1]
	ds_read_b128 v[56:59], v67 offset:36160
	v_pk_fma_f32 v[54:55], v[42:43], v[78:79], v[54:55] op_sel:[1,0,0]
	v_pk_fma_f32 v[42:43], v[42:43], v[80:81], v[52:53] op_sel:[1,0,0]
	v_pk_fma_f32 v[54:55], v[44:45], v[82:83], v[54:55] op_sel_hi:[0,1,1]
	v_pk_fma_f32 v[42:43], v[44:45], v[84:85], v[42:43] op_sel_hi:[0,1,1]
	v_pk_fma_f32 v[54:55], v[48:49], v[90:91], v[54:55] op_sel_hi:[0,1,1]
	v_pk_fma_f32 v[42:43], v[48:49], v[92:93], v[42:43] op_sel_hi:[0,1,1]
	v_pk_fma_f32 v[88:89], v[34:35], v[112:113], v[74:75] op_sel_hi:[0,1,1]
	ds_read_b128 v[74:77], v67 offset:36192
	s_waitcnt lgkmcnt(1)
	v_pk_fma_f32 v[96:97], v[34:35], v[56:57], v[134:135] op_sel:[1,0,0]
	v_pk_fma_f32 v[104:105], v[34:35], v[58:59], v[142:143] op_sel:[1,0,0]
	v_pk_fma_f32 v[112:113], v[34:35], v[60:61], v[144:145] op_sel:[1,0,0]
	v_pk_fma_f32 v[116:117], v[34:35], v[62:63], v[146:147] op_sel:[1,0,0]
	ds_read_b128 v[56:59], v67 offset:36208
	ds_read_b128 v[60:63], v67 offset:36352
	v_pk_fma_f32 v[54:55], v[38:39], v[98:99], v[54:55] op_sel_hi:[0,1,1]
	v_pk_fma_f32 v[42:43], v[38:39], v[100:101], v[42:43] op_sel_hi:[0,1,1]
	v_pk_fma_f32 v[54:55], v[38:39], v[106:107], v[54:55] op_sel:[1,0,0]
	v_pk_fma_f32 v[38:39], v[38:39], v[108:109], v[42:43] op_sel:[1,0,0]
	v_pk_fma_f32 v[54:55], v[40:41], v[118:119], v[54:55] op_sel_hi:[0,1,1]
	v_pk_fma_f32 v[38:39], v[40:41], v[120:121], v[38:39] op_sel_hi:[0,1,1]
	v_pk_fma_f32 v[54:55], v[46:47], v[126:127], v[54:55] op_sel_hi:[0,1,1]
	v_pk_fma_f32 v[42:43], v[46:47], v[128:129], v[38:39] op_sel_hi:[0,1,1]
	v_pk_fma_f32 v[54:55], v[34:35], v[122:123], v[54:55] op_sel_hi:[0,1,1]
	v_pk_fma_f32 v[42:43], v[34:35], v[124:125], v[42:43] op_sel_hi:[0,1,1]
	s_waitcnt lgkmcnt(2)
	v_pk_fma_f32 v[110:111], v[34:35], v[74:75], v[110:111] op_sel:[1,0,0]
	v_pk_fma_f32 v[88:89], v[34:35], v[76:77], v[88:89] op_sel:[1,0,0]
	s_waitcnt lgkmcnt(1)
	v_pk_fma_f32 v[78:79], v[34:35], v[56:57], v[54:55] op_sel:[1,0,0]
	s_waitcnt lgkmcnt(0)
	v_pk_fma_f32 v[82:83], v[36:37], v[60:61], v[86:87] op_sel_hi:[0,1,1]
	v_pk_fma_f32 v[86:87], v[36:37], v[62:63], v[94:95] op_sel_hi:[0,1,1]
	ds_read_b128 v[60:63], v67 offset:36400
	ds_read_b128 v[38:41], v67 offset:36416
	v_pk_fma_f32 v[34:35], v[34:35], v[58:59], v[42:43] op_sel:[1,0,0]
	ds_read_b128 v[42:45], v67 offset:36432
	ds_read_b128 v[46:49], v67 offset:36448
	ds_read_b128 v[54:57], v67 offset:36368
	ds_read_b128 v[74:77], v67 offset:36384
	s_waitcnt lgkmcnt(5)
	v_pk_fma_f32 v[62:63], v[36:37], v[62:63], v[64:65] op_sel_hi:[0,1,1]
	s_waitcnt lgkmcnt(4)
	v_pk_fma_f32 v[64:65], v[36:37], v[38:39], v[96:97] op_sel_hi:[0,1,1]
	v_pk_fma_f32 v[80:81], v[36:37], v[40:41], v[104:105] op_sel_hi:[0,1,1]
	s_waitcnt lgkmcnt(3)
	v_pk_fma_f32 v[84:85], v[36:37], v[42:43], v[112:113] op_sel_hi:[0,1,1]
	ds_read_b128 v[38:41], v67 offset:36464
	v_pk_fma_f32 v[90:91], v[36:37], v[44:45], v[116:117] op_sel_hi:[0,1,1]
	s_waitcnt lgkmcnt(3)
	v_pk_fma_f32 v[92:93], v[36:37], v[46:47], v[110:111] op_sel_hi:[0,1,1]
	ds_read_b128 v[42:45], v67 offset:36608
	v_pk_fma_f32 v[88:89], v[36:37], v[48:49], v[88:89] op_sel_hi:[0,1,1]
	ds_read_b128 v[46:49], v67 offset:36624
	v_mov_b32_e32 v50, v37
	s_waitcnt lgkmcnt(4)
	v_pk_fma_f32 v[54:55], v[36:37], v[54:55], v[102:103] op_sel_hi:[0,1,1]
	s_waitcnt lgkmcnt(2)
	v_pk_fma_f32 v[78:79], v[36:37], v[38:39], v[78:79] op_sel_hi:[0,1,1]
	v_pk_fma_f32 v[94:95], v[36:37], v[40:41], v[34:35] op_sel_hi:[0,1,1]
	s_waitcnt lgkmcnt(1)
	v_pk_fma_f32 v[34:35], v[50:51], v[42:43], v[82:83] op_sel_hi:[0,1,1]
	ds_read_b128 v[40:43], v67 offset:36640
	s_waitcnt lgkmcnt(1)
	v_pk_fma_f32 v[38:39], v[50:51], v[46:47], v[54:55] op_sel_hi:[0,1,1]
	ds_read_b128 v[52:55], v67 offset:36656
	v_pk_fma_f32 v[56:57], v[36:37], v[56:57], v[130:131] op_sel_hi:[0,1,1]
	v_pk_fma_f32 v[74:75], v[36:37], v[74:75], v[132:133] op_sel_hi:[0,1,1]
	v_pk_fma_f32 v[76:77], v[36:37], v[76:77], v[136:137] op_sel_hi:[0,1,1]
	v_pk_fma_f32 v[60:61], v[36:37], v[60:61], v[114:115] op_sel_hi:[0,1,1]
	v_pk_fma_f32 v[36:37], v[50:51], v[44:45], v[86:87] op_sel_hi:[0,1,1]
	v_pk_fma_f32 v[44:45], v[50:51], v[48:49], v[56:57] op_sel_hi:[0,1,1]
	ds_read_b128 v[56:59], v67 offset:36672
	s_waitcnt lgkmcnt(2)
	v_pk_fma_f32 v[46:47], v[50:51], v[40:41], v[74:75] op_sel_hi:[0,1,1]
	v_pk_fma_f32 v[48:49], v[50:51], v[42:43], v[76:77] op_sel_hi:[0,1,1]
	s_waitcnt lgkmcnt(1)
	v_pk_fma_f32 v[52:53], v[50:51], v[52:53], v[60:61] op_sel_hi:[0,1,1]
	v_pk_fma_f32 v[54:55], v[50:51], v[54:55], v[62:63] op_sel_hi:[0,1,1]
	ds_read_b128 v[40:43], v67 offset:36688
	ds_read_b128 v[60:63], v67 offset:36704
	s_waitcnt lgkmcnt(2)
	v_pk_fma_f32 v[110:111], v[50:51], v[56:57], v[64:65] op_sel_hi:[0,1,1]
	v_pk_fma_f32 v[112:113], v[50:51], v[58:59], v[80:81] op_sel_hi:[0,1,1]
	ds_read_b128 v[56:59], v67 offset:36720
	s_waitcnt lgkmcnt(2)
	v_pk_fma_f32 v[114:115], v[50:51], v[40:41], v[84:85] op_sel_hi:[0,1,1]
	s_waitcnt lgkmcnt(1)
	v_pk_fma_f32 v[118:119], v[50:51], v[60:61], v[92:93] op_sel_hi:[0,1,1]
	v_pk_fma_f32 v[120:121], v[50:51], v[62:63], v[88:89] op_sel_hi:[0,1,1]
	ds_read_b128 v[60:63], v67 offset:36976
	s_waitcnt lgkmcnt(1)
	v_pk_fma_f32 v[122:123], v[50:51], v[56:57], v[78:79] op_sel_hi:[0,1,1]
	v_pk_fma_f32 v[40:41], v[50:51], v[58:59], v[94:95] op_sel_hi:[0,1,1]
	ds_read_b128 v[56:59], v67 offset:37232
	ds_read_b128 v[74:77], v67 offset:37488
	ds_read_b128 v[78:81], v67 offset:36960
	ds_read_b128 v[86:89], v67 offset:37744
	s_waitcnt lgkmcnt(4)
	v_pk_fma_f32 v[40:41], v[30:31], v[62:63], v[40:41] op_sel_hi:[0,1,1]
	s_waitcnt lgkmcnt(3)
	v_pk_fma_f32 v[40:41], v[30:31], v[58:59], v[40:41] op_sel:[1,0,0]
	v_pk_fma_f32 v[58:59], v[30:31], v[60:61], v[122:123] op_sel_hi:[0,1,1]
	v_pk_fma_f32 v[116:117], v[50:51], v[42:43], v[90:91] op_sel_hi:[0,1,1]
	ds_read_b128 v[62:65], v67 offset:37216
	ds_read_b128 v[82:85], v67 offset:37472
	ds_read_b128 v[90:93], v67 offset:38000
	ds_read_b128 v[94:97], v67 offset:38256
	ds_read_b128 v[98:101], v67 offset:37728
	v_pk_fma_f32 v[56:57], v[30:31], v[56:57], v[58:59] op_sel:[1,0,0]
	s_waitcnt lgkmcnt(7)
	v_pk_fma_f32 v[42:43], v[32:33], v[76:77], v[40:41] op_sel_hi:[0,1,1]
	v_mov_b32_e32 v40, v33
	v_pk_fma_f32 v[56:57], v[32:33], v[74:75], v[56:57] op_sel_hi:[0,1,1]
	s_waitcnt lgkmcnt(5)
	v_pk_fma_f32 v[56:57], v[40:41], v[86:87], v[56:57] op_sel_hi:[0,1,1]
	ds_read_b128 v[102:105], v67 offset:37984
	ds_read_b128 v[106:109], v67 offset:38240
	s_waitcnt lgkmcnt(4)
	v_pk_fma_f32 v[56:57], v[26:27], v[90:91], v[56:57] op_sel_hi:[0,1,1]
	s_waitcnt lgkmcnt(3)
	v_pk_fma_f32 v[122:123], v[26:27], v[94:95], v[56:57] op_sel:[1,0,0]
	v_pk_fma_f32 v[56:57], v[30:31], v[80:81], v[120:121] op_sel_hi:[0,1,1]
	v_pk_fma_f32 v[56:57], v[30:31], v[64:65], v[56:57] op_sel:[1,0,0]
	v_pk_fma_f32 v[42:43], v[40:41], v[88:89], v[42:43] op_sel_hi:[0,1,1]
	v_pk_fma_f32 v[56:57], v[32:33], v[84:85], v[56:57] op_sel_hi:[0,1,1]
	s_waitcnt lgkmcnt(2)
	v_pk_fma_f32 v[56:57], v[40:41], v[100:101], v[56:57] op_sel_hi:[0,1,1]
	s_waitcnt lgkmcnt(1)
	v_pk_fma_f32 v[56:57], v[26:27], v[104:105], v[56:57] op_sel_hi:[0,1,1]
	s_waitcnt lgkmcnt(0)
	v_pk_fma_f32 v[120:121], v[26:27], v[108:109], v[56:57] op_sel:[1,0,0]
	v_pk_fma_f32 v[56:57], v[30:31], v[78:79], v[118:119] op_sel_hi:[0,1,1]
	v_pk_fma_f32 v[56:57], v[30:31], v[62:63], v[56:57] op_sel:[1,0,0]
	v_pk_fma_f32 v[42:43], v[26:27], v[92:93], v[42:43] op_sel_hi:[0,1,1]
	v_pk_fma_f32 v[56:57], v[32:33], v[82:83], v[56:57] op_sel_hi:[0,1,1]
	v_pk_fma_f32 v[60:61], v[40:41], v[98:99], v[56:57] op_sel_hi:[0,1,1]
	ds_read_b128 v[56:59], v67 offset:36944
	v_pk_fma_f32 v[60:61], v[26:27], v[102:103], v[60:61] op_sel_hi:[0,1,1]
	v_pk_fma_f32 v[118:119], v[26:27], v[106:107], v[60:61] op_sel:[1,0,0]
	ds_read_b128 v[60:63], v67 offset:37200
	ds_read_b128 v[74:77], v67 offset:36928
	ds_read_b128 v[78:81], v67 offset:37456
	ds_read_b128 v[82:85], v67 offset:37184
	s_waitcnt lgkmcnt(4)
	v_pk_fma_f32 v[58:59], v[30:31], v[58:59], v[116:117] op_sel_hi:[0,1,1]
	v_pk_fma_f32 v[50:51], v[26:27], v[96:97], v[42:43] op_sel:[1,0,0]
	s_waitcnt lgkmcnt(3)
	v_pk_fma_f32 v[58:59], v[30:31], v[62:63], v[58:59] op_sel:[1,0,0]
	ds_read_b128 v[62:65], v67 offset:37712
	ds_read_b128 v[86:89], v67 offset:37440
	ds_read_b128 v[90:93], v67 offset:37968
	ds_read_b128 v[94:97], v67 offset:38224
	ds_read_b128 v[98:101], v67 offset:37696
	s_waitcnt lgkmcnt(6)
	v_pk_fma_f32 v[58:59], v[32:33], v[80:81], v[58:59] op_sel_hi:[0,1,1]
	v_pk_fma_f32 v[56:57], v[30:31], v[56:57], v[114:115] op_sel_hi:[0,1,1]
	s_waitcnt lgkmcnt(4)
	v_pk_fma_f32 v[58:59], v[40:41], v[64:65], v[58:59] op_sel_hi:[0,1,1]
	s_waitcnt lgkmcnt(2)
	v_pk_fma_f32 v[58:59], v[26:27], v[92:93], v[58:59] op_sel_hi:[0,1,1]
	v_pk_fma_f32 v[56:57], v[30:31], v[60:61], v[56:57] op_sel:[1,0,0]
	s_waitcnt lgkmcnt(1)
	v_pk_fma_f32 v[64:65], v[26:27], v[96:97], v[58:59] op_sel:[1,0,0]
	v_pk_fma_f32 v[60:61], v[32:33], v[78:79], v[56:57] op_sel_hi:[0,1,1]
	ds_read_b128 v[56:59], v67 offset:38480
	v_pk_fma_f32 v[60:61], v[40:41], v[62:63], v[60:61] op_sel_hi:[0,1,1]
	v_pk_fma_f32 v[60:61], v[26:27], v[90:91], v[60:61] op_sel_hi:[0,1,1]
	v_pk_fma_f32 v[78:79], v[26:27], v[94:95], v[60:61] op_sel:[1,0,0]
	ds_read_b128 v[102:105], v67 offset:37952
	s_waitcnt lgkmcnt(1)
	v_pk_fma_f32 v[124:125], v[28:29], v[56:57], v[78:79] op_sel_hi:[0,1,1]
	v_pk_fma_f32 v[56:57], v[30:31], v[76:77], v[112:113] op_sel_hi:[0,1,1]
	v_pk_fma_f32 v[56:57], v[30:31], v[84:85], v[56:57] op_sel:[1,0,0]
	v_pk_fma_f32 v[126:127], v[28:29], v[58:59], v[64:65] op_sel_hi:[0,1,1]
	v_pk_fma_f32 v[56:57], v[32:33], v[88:89], v[56:57] op_sel_hi:[0,1,1]
	v_pk_fma_f32 v[64:65], v[40:41], v[100:101], v[56:57] op_sel_hi:[0,1,1]
	ds_read_b128 v[56:59], v67 offset:38496
	ds_read_b128 v[76:79], v67 offset:38512
	ds_read_b128 v[106:109], v67 offset:38208
	ds_read_b128 v[60:63], v67 offset:38464
	v_mov_b32_e32 v42, v29
	s_waitcnt lgkmcnt(3)
	v_pk_fma_f32 v[118:119], v[28:29], v[56:57], v[118:119] op_sel_hi:[0,1,1]
	s_waitcnt lgkmcnt(2)
	v_pk_fma_f32 v[130:131], v[28:29], v[78:79], v[50:51] op_sel_hi:[0,1,1]
	v_pk_fma_f32 v[50:51], v[30:31], v[74:75], v[110:111] op_sel_hi:[0,1,1]
	v_pk_fma_f32 v[50:51], v[30:31], v[82:83], v[50:51] op_sel:[1,0,0]
	v_pk_fma_f32 v[120:121], v[28:29], v[58:59], v[120:121] op_sel_hi:[0,1,1]
	v_pk_fma_f32 v[50:51], v[32:33], v[86:87], v[50:51] op_sel_hi:[0,1,1]
	v_pk_fma_f32 v[50:51], v[40:41], v[98:99], v[50:51] op_sel_hi:[0,1,1]
	ds_read_b128 v[56:59], v67 offset:36912
	v_pk_fma_f32 v[64:65], v[26:27], v[104:105], v[64:65] op_sel_hi:[0,1,1]
	v_pk_fma_f32 v[50:51], v[26:27], v[102:103], v[50:51] op_sel_hi:[0,1,1]
	s_waitcnt lgkmcnt(2)
	v_pk_fma_f32 v[64:65], v[26:27], v[108:109], v[64:65] op_sel:[1,0,0]
	v_pk_fma_f32 v[50:51], v[26:27], v[106:107], v[50:51] op_sel:[1,0,0]
	s_waitcnt lgkmcnt(1)
	v_pk_fma_f32 v[128:129], v[28:29], v[62:63], v[64:65] op_sel_hi:[0,1,1]
	v_pk_fma_f32 v[122:123], v[28:29], v[76:77], v[122:123] op_sel_hi:[0,1,1]
	v_pk_fma_f32 v[132:133], v[28:29], v[60:61], v[50:51] op_sel_hi:[0,1,1]
	ds_read_b128 v[60:63], v67 offset:37168
	ds_read_b128 v[74:77], v67 offset:36896
	s_waitcnt lgkmcnt(2)
	v_pk_fma_f32 v[50:51], v[30:31], v[58:59], v[54:55] op_sel_hi:[0,1,1]
	ds_read_b128 v[78:81], v67 offset:37424
	ds_read_b128 v[82:85], v67 offset:37152
	s_waitcnt lgkmcnt(3)
	v_pk_fma_f32 v[50:51], v[30:31], v[62:63], v[50:51] op_sel:[1,0,0]
	ds_read_b128 v[62:65], v67 offset:37680
	ds_read_b128 v[86:89], v67 offset:37408
	ds_read_b128 v[90:93], v67 offset:37936
	ds_read_b128 v[94:97], v67 offset:37664
	s_waitcnt lgkmcnt(5)
	v_pk_fma_f32 v[50:51], v[32:33], v[80:81], v[50:51] op_sel_hi:[0,1,1]
	ds_read_b128 v[98:101], v67 offset:38192
	ds_read_b128 v[102:105], v67 offset:38448
	ds_read_b128 v[106:109], v67 offset:37920
	s_waitcnt lgkmcnt(6)
	v_pk_fma_f32 v[50:51], v[40:41], v[64:65], v[50:51] op_sel_hi:[0,1,1]
	s_waitcnt lgkmcnt(4)
	v_pk_fma_f32 v[50:51], v[26:27], v[92:93], v[50:51] op_sel_hi:[0,1,1]
	s_waitcnt lgkmcnt(2)
	v_pk_fma_f32 v[50:51], v[26:27], v[100:101], v[50:51] op_sel:[1,0,0]
	ds_read_b128 v[110:113], v67 offset:38176
	ds_read_b128 v[114:117], v67 offset:38432
	s_waitcnt lgkmcnt(3)
	v_pk_fma_f32 v[64:65], v[28:29], v[104:105], v[50:51] op_sel_hi:[0,1,1]
	v_pk_fma_f32 v[50:51], v[30:31], v[56:57], v[52:53] op_sel_hi:[0,1,1]
	v_pk_fma_f32 v[50:51], v[30:31], v[60:61], v[50:51] op_sel:[1,0,0]
	v_pk_fma_f32 v[48:49], v[30:31], v[76:77], v[48:49] op_sel_hi:[0,1,1]
	v_pk_fma_f32 v[50:51], v[32:33], v[78:79], v[50:51] op_sel_hi:[0,1,1]
	v_pk_fma_f32 v[50:51], v[40:41], v[62:63], v[50:51] op_sel_hi:[0,1,1]
	v_pk_fma_f32 v[54:55], v[26:27], v[90:91], v[50:51] op_sel_hi:[0,1,1]
	ds_read_b128 v[50:53], v67 offset:38704
	v_pk_fma_f32 v[54:55], v[26:27], v[98:99], v[54:55] op_sel:[1,0,0]
	v_pk_fma_f32 v[48:49], v[30:31], v[84:85], v[48:49] op_sel:[1,0,0]
	v_pk_fma_f32 v[62:63], v[28:29], v[102:103], v[54:55] op_sel_hi:[0,1,1]
	ds_read_b128 v[54:57], v67 offset:38720
	ds_read_b128 v[58:61], v67 offset:38688
	v_pk_fma_f32 v[48:49], v[32:33], v[88:89], v[48:49] op_sel_hi:[0,1,1]
	v_pk_fma_f32 v[48:49], v[40:41], v[96:97], v[48:49] op_sel_hi:[0,1,1]
	s_waitcnt lgkmcnt(2)
	v_pk_fma_f32 v[134:135], v[42:43], v[50:51], v[62:63] op_sel_hi:[0,1,1]
	v_pk_fma_f32 v[136:137], v[42:43], v[52:53], v[64:65] op_sel_hi:[0,1,1]
	ds_read_b128 v[50:53], v67 offset:38736
	v_pk_fma_f32 v[48:49], v[26:27], v[108:109], v[48:49] op_sel_hi:[0,1,1]
	v_pk_fma_f32 v[46:47], v[30:31], v[74:75], v[46:47] op_sel_hi:[0,1,1]
	v_pk_fma_f32 v[48:49], v[26:27], v[112:113], v[48:49] op_sel:[1,0,0]
	v_pk_fma_f32 v[46:47], v[30:31], v[82:83], v[46:47] op_sel:[1,0,0]
	s_waitcnt lgkmcnt(2)
	v_pk_fma_f32 v[132:133], v[42:43], v[54:55], v[132:133] op_sel_hi:[0,1,1]
	v_pk_fma_f32 v[138:139], v[42:43], v[56:57], v[128:129] op_sel_hi:[0,1,1]
	v_pk_fma_f32 v[48:49], v[28:29], v[116:117], v[48:49] op_sel_hi:[0,1,1]
	ds_read_b128 v[54:57], v67 offset:38752
	v_pk_fma_f32 v[46:47], v[32:33], v[86:87], v[46:47] op_sel_hi:[0,1,1]
	s_waitcnt lgkmcnt(2)
	v_pk_fma_f32 v[140:141], v[42:43], v[60:61], v[48:49] op_sel_hi:[0,1,1]
	ds_read_b128 v[60:63], v67 offset:38768
	v_pk_fma_f32 v[46:47], v[40:41], v[94:95], v[46:47] op_sel_hi:[0,1,1]
	v_pk_fma_f32 v[46:47], v[26:27], v[106:107], v[46:47] op_sel_hi:[0,1,1]
	s_waitcnt lgkmcnt(2)
	v_pk_fma_f32 v[142:143], v[42:43], v[50:51], v[124:125] op_sel_hi:[0,1,1]
	v_pk_fma_f32 v[50:51], v[26:27], v[110:111], v[46:47] op_sel:[1,0,0]
	ds_read_b128 v[46:49], v67 offset:36880
	v_pk_fma_f32 v[50:51], v[28:29], v[114:115], v[50:51] op_sel_hi:[0,1,1]
	v_pk_fma_f32 v[144:145], v[42:43], v[52:53], v[126:127] op_sel_hi:[0,1,1]
	s_waitcnt lgkmcnt(2)
	v_pk_fma_f32 v[146:147], v[42:43], v[54:55], v[118:119] op_sel_hi:[0,1,1]
	v_pk_fma_f32 v[148:149], v[42:43], v[56:57], v[120:121] op_sel_hi:[0,1,1]
	v_pk_fma_f32 v[152:153], v[42:43], v[58:59], v[50:51] op_sel_hi:[0,1,1]
	ds_read_b128 v[50:53], v67 offset:37136
	ds_read_b128 v[54:57], v67 offset:36864
	s_waitcnt lgkmcnt(3)
	v_pk_fma_f32 v[150:151], v[42:43], v[60:61], v[122:123] op_sel_hi:[0,1,1]
	v_pk_fma_f32 v[130:131], v[42:43], v[62:63], v[130:131] op_sel_hi:[0,1,1]
	ds_read_b128 v[58:61], v67 offset:37392
	ds_read_b128 v[62:65], v67 offset:37120
	ds_read_b128 v[74:77], v67 offset:37648
	ds_read_b128 v[78:81], v67 offset:37376
	s_waitcnt lgkmcnt(6)
	v_pk_fma_f32 v[44:45], v[30:31], v[48:49], v[44:45] op_sel_hi:[0,1,1]
	ds_read_b128 v[82:85], v67 offset:37904
	ds_read_b128 v[86:89], v67 offset:37632
	s_waitcnt lgkmcnt(7)
	v_pk_fma_f32 v[44:45], v[30:31], v[52:53], v[44:45] op_sel:[1,0,0]
	ds_read_b128 v[90:93], v67 offset:38160
	ds_read_b128 v[94:97], v67 offset:37888
	s_waitcnt lgkmcnt(7)
	v_pk_fma_f32 v[44:45], v[32:33], v[60:61], v[44:45] op_sel_hi:[0,1,1]
	ds_read_b128 v[98:101], v67 offset:38416
	ds_read_b128 v[102:105], v67 offset:38144
	s_waitcnt lgkmcnt(7)
	v_pk_fma_f32 v[44:45], v[40:41], v[76:77], v[44:45] op_sel_hi:[0,1,1]
	ds_read_b128 v[106:109], v67 offset:38672
	ds_read_b128 v[110:113], v67 offset:38400
	s_waitcnt lgkmcnt(7)
	v_pk_fma_f32 v[44:45], v[26:27], v[84:85], v[44:45] op_sel_hi:[0,1,1]
	s_waitcnt lgkmcnt(5)
	v_pk_fma_f32 v[44:45], v[26:27], v[92:93], v[44:45] op_sel:[1,0,0]
	ds_read_b128 v[114:117], v67 offset:38944
	ds_read_b128 v[118:121], v67 offset:38928
	ds_read_b128 v[122:125], v67 offset:38656
	ds_read_b128 v[126:129], v67 offset:38960
	v_pk_fma_f32 v[38:39], v[30:31], v[46:47], v[38:39] op_sel_hi:[0,1,1]
	s_waitcnt lgkmcnt(7)
	v_pk_fma_f32 v[44:45], v[28:29], v[100:101], v[44:45] op_sel_hi:[0,1,1]
	v_pk_fma_f32 v[38:39], v[30:31], v[50:51], v[38:39] op_sel:[1,0,0]
	s_waitcnt lgkmcnt(5)
	v_pk_fma_f32 v[44:45], v[42:43], v[108:109], v[44:45] op_sel_hi:[0,1,1]
	v_pk_fma_f32 v[38:39], v[32:33], v[58:59], v[38:39] op_sel_hi:[0,1,1]
	v_pk_fma_f32 v[36:37], v[30:31], v[56:57], v[36:37] op_sel_hi:[0,1,1]
	s_waitcnt lgkmcnt(2)
	v_pk_fma_f32 v[100:101], v[22:23], v[120:121], v[44:45] op_sel_hi:[0,1,1]
	ds_read_b128 v[44:47], v67 offset:38992
	ds_read_b128 v[48:51], v67 offset:39008
	v_pk_fma_f32 v[38:39], v[40:41], v[74:75], v[38:39] op_sel_hi:[0,1,1]
	v_pk_fma_f32 v[36:37], v[30:31], v[64:65], v[36:37] op_sel:[1,0,0]
	v_pk_fma_f32 v[38:39], v[26:27], v[82:83], v[38:39] op_sel_hi:[0,1,1]
	v_pk_fma_f32 v[36:37], v[32:33], v[80:81], v[36:37] op_sel_hi:[0,1,1]
	v_pk_fma_f32 v[34:35], v[30:31], v[54:55], v[34:35] op_sel_hi:[0,1,1]
	v_pk_fma_f32 v[38:39], v[26:27], v[90:91], v[38:39] op_sel:[1,0,0]
	v_pk_fma_f32 v[36:37], v[40:41], v[88:89], v[36:37] op_sel_hi:[0,1,1]
	v_pk_fma_f32 v[30:31], v[30:31], v[62:63], v[34:35] op_sel:[1,0,0]
	v_pk_fma_f32 v[38:39], v[28:29], v[98:99], v[38:39] op_sel_hi:[0,1,1]
	v_pk_fma_f32 v[36:37], v[26:27], v[96:97], v[36:37] op_sel_hi:[0,1,1]
	v_pk_fma_f32 v[30:31], v[32:33], v[78:79], v[30:31] op_sel_hi:[0,1,1]
	v_pk_fma_f32 v[52:53], v[22:23], v[114:115], v[152:153] op_sel_hi:[0,1,1]
	v_pk_fma_f32 v[76:77], v[22:23], v[116:117], v[140:141] op_sel_hi:[0,1,1]
	ds_read_b128 v[114:117], v67 offset:38976
	s_waitcnt lgkmcnt(3)
	v_pk_fma_f32 v[84:85], v[22:23], v[126:127], v[134:135] op_sel_hi:[0,1,1]
	v_pk_fma_f32 v[92:93], v[22:23], v[128:129], v[136:137] op_sel_hi:[0,1,1]
	ds_read_b128 v[126:129], v67 offset:38912
	v_pk_fma_f32 v[38:39], v[42:43], v[106:107], v[38:39] op_sel_hi:[0,1,1]
	v_pk_fma_f32 v[36:37], v[26:27], v[104:105], v[36:37] op_sel:[1,0,0]
	v_pk_fma_f32 v[30:31], v[40:41], v[86:87], v[30:31] op_sel_hi:[0,1,1]
	v_pk_fma_f32 v[74:75], v[22:23], v[118:119], v[38:39] op_sel_hi:[0,1,1]
	ds_read_b128 v[58:61], v67 offset:39024
	s_waitcnt lgkmcnt(4)
	v_pk_fma_f32 v[90:91], v[22:23], v[44:45], v[142:143] op_sel_hi:[0,1,1]
	v_pk_fma_f32 v[98:99], v[22:23], v[46:47], v[144:145] op_sel_hi:[0,1,1]
	s_waitcnt lgkmcnt(3)
	v_pk_fma_f32 v[106:107], v[22:23], v[48:49], v[146:147] op_sel_hi:[0,1,1]
	v_pk_fma_f32 v[48:49], v[28:29], v[112:113], v[36:37] op_sel_hi:[0,1,1]
	ds_read_b128 v[36:39], v67 offset:39168
	ds_read_b128 v[44:47], v67 offset:39184
	v_pk_fma_f32 v[30:31], v[26:27], v[94:95], v[30:31] op_sel_hi:[0,1,1]
	v_pk_fma_f32 v[26:27], v[26:27], v[102:103], v[30:31] op_sel:[1,0,0]
	v_pk_fma_f32 v[48:49], v[42:43], v[124:125], v[48:49] op_sel_hi:[0,1,1]
	v_pk_fma_f32 v[26:27], v[28:29], v[110:111], v[26:27] op_sel_hi:[0,1,1]
	v_pk_fma_f32 v[26:27], v[42:43], v[122:123], v[26:27] op_sel_hi:[0,1,1]
	s_waitcnt lgkmcnt(3)
	v_pk_fma_f32 v[56:57], v[22:23], v[128:129], v[48:49] op_sel_hi:[0,1,1]
	v_pk_fma_f32 v[30:31], v[22:23], v[126:127], v[26:27] op_sel_hi:[0,1,1]
	v_pk_fma_f32 v[108:109], v[22:23], v[114:115], v[132:133] op_sel_hi:[0,1,1]
	v_pk_fma_f32 v[114:115], v[22:23], v[50:51], v[148:149] op_sel_hi:[0,1,1]
	ds_read_b128 v[48:51], v67 offset:39200
	s_waitcnt lgkmcnt(2)
	v_pk_fma_f32 v[38:39], v[22:23], v[38:39], v[56:57] op_sel:[1,0,0]
	s_waitcnt lgkmcnt(1)
	v_pk_fma_f32 v[56:57], v[22:23], v[44:45], v[74:75] op_sel:[1,0,0]
	v_pk_fma_f32 v[64:65], v[22:23], v[46:47], v[100:101] op_sel:[1,0,0]
	ds_read_b128 v[44:47], v67 offset:39216
	ds_read_b128 v[26:29], v67 offset:39232
	v_pk_fma_f32 v[40:41], v[22:23], v[36:37], v[30:31] op_sel:[1,0,0]
	ds_read_b128 v[30:33], v67 offset:39248
	ds_read_b128 v[34:37], v67 offset:39264
	v_pk_fma_f32 v[82:83], v[22:23], v[116:117], v[138:139] op_sel_hi:[0,1,1]
	s_waitcnt lgkmcnt(4)
	v_pk_fma_f32 v[48:49], v[22:23], v[48:49], v[52:53] op_sel:[1,0,0]
	v_pk_fma_f32 v[50:51], v[22:23], v[50:51], v[76:77] op_sel:[1,0,0]
	s_waitcnt lgkmcnt(3)
	v_pk_fma_f32 v[42:43], v[22:23], v[44:45], v[84:85] op_sel:[1,0,0]
	v_pk_fma_f32 v[44:45], v[22:23], v[46:47], v[92:93] op_sel:[1,0,0]
	s_waitcnt lgkmcnt(2)
	v_pk_fma_f32 v[46:47], v[22:23], v[26:27], v[108:109] op_sel:[1,0,0]
	v_pk_fma_f32 v[52:53], v[22:23], v[28:29], v[82:83] op_sel:[1,0,0]
	s_waitcnt lgkmcnt(1)
	v_pk_fma_f32 v[54:55], v[22:23], v[30:31], v[90:91] op_sel:[1,0,0]
	ds_read_b128 v[26:29], v67 offset:39280
	v_pk_fma_f32 v[62:63], v[22:23], v[32:33], v[98:99] op_sel:[1,0,0]
	s_waitcnt lgkmcnt(1)
	v_pk_fma_f32 v[74:75], v[22:23], v[34:35], v[106:107] op_sel:[1,0,0]
	ds_read_b128 v[30:33], v67 offset:39424
	v_pk_fma_f32 v[76:77], v[22:23], v[36:37], v[114:115] op_sel:[1,0,0]
	ds_read_b128 v[34:37], v67 offset:39440
	v_pk_fma_f32 v[58:59], v[22:23], v[58:59], v[150:151] op_sel_hi:[0,1,1]
	v_pk_fma_f32 v[60:61], v[22:23], v[60:61], v[130:131] op_sel_hi:[0,1,1]
	s_waitcnt lgkmcnt(2)
	v_pk_fma_f32 v[58:59], v[22:23], v[26:27], v[58:59] op_sel:[1,0,0]
	v_pk_fma_f32 v[22:23], v[22:23], v[28:29], v[60:61] op_sel:[1,0,0]
	s_waitcnt lgkmcnt(1)
	v_pk_fma_f32 v[60:61], v[24:25], v[30:31], v[40:41] op_sel_hi:[0,1,1]
	ds_read_b128 v[26:29], v67 offset:39456
	v_pk_fma_f32 v[102:103], v[24:25], v[32:33], v[38:39] op_sel_hi:[0,1,1]
	s_waitcnt lgkmcnt(1)
	v_pk_fma_f32 v[104:105], v[24:25], v[34:35], v[56:57] op_sel_hi:[0,1,1]
	ds_read_b128 v[30:33], v67 offset:39472
	v_pk_fma_f32 v[64:65], v[24:25], v[36:37], v[64:65] op_sel_hi:[0,1,1]
	ds_read_b128 v[34:37], v67 offset:39488
	s_waitcnt lgkmcnt(2)
	v_pk_fma_f32 v[106:107], v[24:25], v[26:27], v[48:49] op_sel_hi:[0,1,1]
	v_pk_fma_f32 v[108:109], v[24:25], v[28:29], v[50:51] op_sel_hi:[0,1,1]
	s_waitcnt lgkmcnt(1)
	v_pk_fma_f32 v[110:111], v[24:25], v[30:31], v[42:43] op_sel_hi:[0,1,1]
	v_pk_fma_f32 v[112:113], v[24:25], v[32:33], v[44:45] op_sel_hi:[0,1,1]
	ds_read_b128 v[26:29], v67 offset:39504
	s_waitcnt lgkmcnt(1)
	v_pk_fma_f32 v[42:43], v[24:25], v[34:35], v[46:47] op_sel_hi:[0,1,1]
	ds_read_b128 v[30:33], v67 offset:39520
	ds_read_b128 v[44:47], v67 offset:39536
	ds_read_b128 v[48:51], v67 offset:39680
	v_pk_fma_f32 v[40:41], v[24:25], v[36:37], v[52:53] op_sel_hi:[0,1,1]
	s_waitcnt lgkmcnt(3)
	v_pk_fma_f32 v[38:39], v[24:25], v[26:27], v[54:55] op_sel_hi:[0,1,1]
	v_pk_fma_f32 v[36:37], v[24:25], v[28:29], v[62:63] op_sel_hi:[0,1,1]
	s_waitcnt lgkmcnt(1)
	v_pk_fma_f32 v[26:27], v[24:25], v[44:45], v[58:59] op_sel_hi:[0,1,1]
	v_pk_fma_f32 v[22:23], v[24:25], v[46:47], v[22:23] op_sel_hi:[0,1,1]
	ds_read_b128 v[44:47], v67 offset:39936
	ds_read_b128 v[52:55], v67 offset:39696
	v_pk_fma_f32 v[34:35], v[24:25], v[30:31], v[74:75] op_sel_hi:[0,1,1]
	v_pk_fma_f32 v[28:29], v[24:25], v[32:33], v[76:77] op_sel_hi:[0,1,1]
	v_mov_b32_e32 v24, v25
	s_waitcnt lgkmcnt(2)
	v_pk_fma_f32 v[30:31], v[24:25], v[48:49], v[60:61] op_sel_hi:[0,1,1]
	ds_read_b128 v[56:59], v67 offset:40192
	ds_read_b128 v[60:63], v67 offset:39952
	ds_read_b128 v[74:77], v67 offset:40448
	ds_read_b128 v[78:81], v67 offset:40208
	s_waitcnt lgkmcnt(5)
	v_pk_fma_f32 v[30:31], v[18:19], v[44:45], v[30:31] op_sel_hi:[0,1,1]
	ds_read_b128 v[82:85], v67 offset:40704
	ds_read_b128 v[86:89], v67 offset:40464
	ds_read_b128 v[90:93], v67 offset:40960
	ds_read_b128 v[94:97], v67 offset:40720
	v_pk_fma_f32 v[44:45], v[24:25], v[50:51], v[102:103] op_sel_hi:[0,1,1]
	v_pk_fma_f32 v[44:45], v[18:19], v[46:47], v[44:45] op_sel_hi:[0,1,1]
	s_waitcnt lgkmcnt(7)
	v_pk_fma_f32 v[30:31], v[18:19], v[56:57], v[30:31] op_sel:[1,0,0]
	v_pk_fma_f32 v[44:45], v[18:19], v[58:59], v[44:45] op_sel:[1,0,0]
	s_waitcnt lgkmcnt(5)
	v_pk_fma_f32 v[32:33], v[20:21], v[74:75], v[30:31] op_sel_hi:[0,1,1]
	v_mov_b32_e32 v30, v21
	v_pk_fma_f32 v[44:45], v[20:21], v[76:77], v[44:45] op_sel_hi:[0,1,1]
	s_waitcnt lgkmcnt(3)
	v_pk_fma_f32 v[44:45], v[30:31], v[84:85], v[44:45] op_sel_hi:[0,1,1]
	ds_read_b128 v[98:101], v67 offset:40976
	s_waitcnt lgkmcnt(2)
	v_pk_fma_f32 v[102:103], v[14:15], v[92:93], v[44:45] op_sel_hi:[0,1,1]
	v_pk_fma_f32 v[44:45], v[24:25], v[52:53], v[104:105] op_sel_hi:[0,1,1]
	v_pk_fma_f32 v[44:45], v[18:19], v[60:61], v[44:45] op_sel_hi:[0,1,1]
	v_pk_fma_f32 v[44:45], v[18:19], v[78:79], v[44:45] op_sel:[1,0,0]
	v_pk_fma_f32 v[32:33], v[30:31], v[82:83], v[32:33] op_sel_hi:[0,1,1]
	v_pk_fma_f32 v[44:45], v[20:21], v[86:87], v[44:45] op_sel_hi:[0,1,1]
	s_waitcnt lgkmcnt(1)
	v_pk_fma_f32 v[44:45], v[30:31], v[94:95], v[44:45] op_sel_hi:[0,1,1]
	s_waitcnt lgkmcnt(0)
	v_pk_fma_f32 v[104:105], v[14:15], v[98:99], v[44:45] op_sel_hi:[0,1,1]
	v_pk_fma_f32 v[44:45], v[24:25], v[54:55], v[64:65] op_sel_hi:[0,1,1]
	v_pk_fma_f32 v[44:45], v[18:19], v[62:63], v[44:45] op_sel_hi:[0,1,1]
	v_pk_fma_f32 v[44:45], v[18:19], v[80:81], v[44:45] op_sel:[1,0,0]
	v_pk_fma_f32 v[114:115], v[14:15], v[90:91], v[32:33] op_sel_hi:[0,1,1]
	v_pk_fma_f32 v[48:49], v[20:21], v[88:89], v[44:45] op_sel_hi:[0,1,1]
	ds_read_b128 v[44:47], v67 offset:39712
	v_pk_fma_f32 v[48:49], v[30:31], v[96:97], v[48:49] op_sel_hi:[0,1,1]
	v_pk_fma_f32 v[64:65], v[14:15], v[100:101], v[48:49] op_sel_hi:[0,1,1]
	ds_read_b128 v[48:51], v67 offset:39968
	ds_read_b128 v[52:55], v67 offset:39728
	ds_read_b128 v[56:59], v67 offset:40224
	ds_read_b128 v[60:63], v67 offset:39984
	ds_read_b128 v[74:77], v67 offset:40480
	ds_read_b128 v[78:81], v67 offset:40240
	s_waitcnt lgkmcnt(6)
	v_pk_fma_f32 v[44:45], v[24:25], v[44:45], v[106:107] op_sel_hi:[0,1,1]
	s_waitcnt lgkmcnt(5)
	v_pk_fma_f32 v[44:45], v[18:19], v[48:49], v[44:45] op_sel_hi:[0,1,1]
	ds_read_b128 v[82:85], v67 offset:40736
	ds_read_b128 v[86:89], v67 offset:40992
	ds_read_b128 v[90:93], v67 offset:40496
	s_waitcnt lgkmcnt(6)
	v_pk_fma_f32 v[44:45], v[18:19], v[56:57], v[44:45] op_sel:[1,0,0]
	ds_read_b128 v[94:97], v67 offset:40752
	ds_read_b128 v[98:101], v67 offset:41008
	s_waitcnt lgkmcnt(6)
	v_pk_fma_f32 v[44:45], v[20:21], v[74:75], v[44:45] op_sel_hi:[0,1,1]
	s_waitcnt lgkmcnt(4)
	v_pk_fma_f32 v[44:45], v[30:31], v[82:83], v[44:45] op_sel_hi:[0,1,1]
	s_waitcnt lgkmcnt(3)
	v_pk_fma_f32 v[56:57], v[14:15], v[86:87], v[44:45] op_sel_hi:[0,1,1]
	v_pk_fma_f32 v[44:45], v[24:25], v[46:47], v[108:109] op_sel_hi:[0,1,1]
	v_pk_fma_f32 v[44:45], v[18:19], v[50:51], v[44:45] op_sel_hi:[0,1,1]
	v_pk_fma_f32 v[48:49], v[18:19], v[58:59], v[44:45] op_sel:[1,0,0]
	ds_read_b128 v[44:47], v67 offset:41216
	v_pk_fma_f32 v[58:59], v[20:21], v[76:77], v[48:49] op_sel_hi:[0,1,1]
	ds_read_b128 v[48:51], v67 offset:41232
	v_pk_fma_f32 v[58:59], v[30:31], v[84:85], v[58:59] op_sel_hi:[0,1,1]
	v_pk_fma_f32 v[58:59], v[14:15], v[88:89], v[58:59] op_sel_hi:[0,1,1]
	s_waitcnt lgkmcnt(1)
	v_pk_fma_f32 v[106:107], v[14:15], v[44:45], v[114:115] op_sel:[1,0,0]
	v_pk_fma_f32 v[44:45], v[24:25], v[52:53], v[110:111] op_sel_hi:[0,1,1]
	v_pk_fma_f32 v[44:45], v[18:19], v[60:61], v[44:45] op_sel_hi:[0,1,1]
	v_pk_fma_f32 v[108:109], v[14:15], v[46:47], v[102:103] op_sel:[1,0,0]
	s_waitcnt lgkmcnt(0)
	v_pk_fma_f32 v[114:115], v[14:15], v[48:49], v[104:105] op_sel:[1,0,0]
	v_pk_fma_f32 v[48:49], v[18:19], v[78:79], v[44:45] op_sel:[1,0,0]
	ds_read_b128 v[44:47], v67 offset:41248
	v_pk_fma_f32 v[64:65], v[14:15], v[50:51], v[64:65] op_sel:[1,0,0]
	v_pk_fma_f32 v[52:53], v[20:21], v[90:91], v[48:49] op_sel_hi:[0,1,1]
	ds_read_b128 v[48:51], v67 offset:41264
	v_pk_fma_f32 v[52:53], v[30:31], v[94:95], v[52:53] op_sel_hi:[0,1,1]
	s_waitcnt lgkmcnt(1)
	v_pk_fma_f32 v[110:111], v[14:15], v[44:45], v[56:57] op_sel:[1,0,0]
	v_pk_fma_f32 v[44:45], v[24:25], v[54:55], v[112:113] op_sel_hi:[0,1,1]
	v_pk_fma_f32 v[44:45], v[18:19], v[62:63], v[44:45] op_sel_hi:[0,1,1]
	v_pk_fma_f32 v[44:45], v[18:19], v[80:81], v[44:45] op_sel:[1,0,0]
	v_pk_fma_f32 v[52:53], v[14:15], v[98:99], v[52:53] op_sel_hi:[0,1,1]
	v_pk_fma_f32 v[44:45], v[20:21], v[92:93], v[44:45] op_sel_hi:[0,1,1]
	v_pk_fma_f32 v[116:117], v[14:15], v[46:47], v[58:59] op_sel:[1,0,0]
	s_waitcnt lgkmcnt(0)
	v_pk_fma_f32 v[118:119], v[14:15], v[48:49], v[52:53] op_sel:[1,0,0]
	v_pk_fma_f32 v[48:49], v[30:31], v[96:97], v[44:45] op_sel_hi:[0,1,1]
	ds_read_b128 v[44:47], v67 offset:39744
	v_pk_fma_f32 v[48:49], v[14:15], v[100:101], v[48:49] op_sel_hi:[0,1,1]
	v_pk_fma_f32 v[112:113], v[14:15], v[50:51], v[48:49] op_sel:[1,0,0]
	ds_read_b128 v[48:51], v67 offset:40000
	ds_read_b128 v[52:55], v67 offset:39760
	v_mov_b32_e32 v32, v17
	s_waitcnt lgkmcnt(2)
	v_pk_fma_f32 v[60:61], v[24:25], v[44:45], v[42:43] op_sel_hi:[0,1,1]
	ds_read_b128 v[42:45], v67 offset:40256
	ds_read_b128 v[56:59], v67 offset:40016
	s_waitcnt lgkmcnt(3)
	v_pk_fma_f32 v[48:49], v[18:19], v[48:49], v[60:61] op_sel_hi:[0,1,1]
	ds_read_b128 v[60:63], v67 offset:40512
	ds_read_b128 v[74:77], v67 offset:40272
	ds_read_b128 v[78:81], v67 offset:40768
	ds_read_b128 v[82:85], v67 offset:40528
	v_pk_fma_f32 v[40:41], v[24:25], v[46:47], v[40:41] op_sel_hi:[0,1,1]
	v_pk_fma_f32 v[40:41], v[18:19], v[50:51], v[40:41] op_sel_hi:[0,1,1]
	s_waitcnt lgkmcnt(5)
	v_pk_fma_f32 v[42:43], v[18:19], v[42:43], v[48:49] op_sel:[1,0,0]
	ds_read_b128 v[86:89], v67 offset:41024
	ds_read_b128 v[90:93], v67 offset:41280
	ds_read_b128 v[94:97], v67 offset:40784
	v_pk_fma_f32 v[40:41], v[18:19], v[44:45], v[40:41] op_sel:[1,0,0]
	s_waitcnt lgkmcnt(6)
	v_pk_fma_f32 v[42:43], v[20:21], v[60:61], v[42:43] op_sel_hi:[0,1,1]
	v_pk_fma_f32 v[44:45], v[20:21], v[62:63], v[40:41] op_sel_hi:[0,1,1]
	s_waitcnt lgkmcnt(4)
	v_pk_fma_f32 v[42:43], v[30:31], v[78:79], v[42:43] op_sel_hi:[0,1,1]
	v_pk_fma_f32 v[44:45], v[30:31], v[80:81], v[44:45] op_sel_hi:[0,1,1]
	s_waitcnt lgkmcnt(2)
	v_pk_fma_f32 v[42:43], v[14:15], v[86:87], v[42:43] op_sel_hi:[0,1,1]
	v_pk_fma_f32 v[48:49], v[14:15], v[88:89], v[44:45] op_sel_hi:[0,1,1]
	s_waitcnt lgkmcnt(1)
	v_pk_fma_f32 v[60:61], v[14:15], v[90:91], v[42:43] op_sel:[1,0,0]
	ds_read_b128 v[40:43], v67 offset:41472
	v_pk_fma_f32 v[62:63], v[14:15], v[92:93], v[48:49] op_sel:[1,0,0]
	ds_read_b128 v[48:51], v67 offset:41504
	ds_read_b128 v[98:101], v67 offset:41040
	ds_read_b128 v[102:105], v67 offset:41296
	v_pk_fma_f32 v[38:39], v[24:25], v[52:53], v[38:39] op_sel_hi:[0,1,1]
	v_pk_fma_f32 v[38:39], v[18:19], v[56:57], v[38:39] op_sel_hi:[0,1,1]
	ds_read_b128 v[44:47], v67 offset:41488
	s_waitcnt lgkmcnt(4)
	v_pk_fma_f32 v[120:121], v[16:17], v[40:41], v[106:107] op_sel_hi:[0,1,1]
	v_pk_fma_f32 v[122:123], v[16:17], v[42:43], v[108:109] op_sel_hi:[0,1,1]
	ds_read_b128 v[40:43], v67 offset:41520
	s_waitcnt lgkmcnt(4)
	v_pk_fma_f32 v[126:127], v[16:17], v[48:49], v[110:111] op_sel_hi:[0,1,1]
	v_pk_fma_f32 v[128:129], v[16:17], v[50:51], v[116:117] op_sel_hi:[0,1,1]
	v_pk_fma_f32 v[38:39], v[18:19], v[74:75], v[38:39] op_sel:[1,0,0]
	ds_read_b128 v[48:51], v67 offset:41552
	v_pk_fma_f32 v[36:37], v[24:25], v[54:55], v[36:37] op_sel_hi:[0,1,1]
	v_pk_fma_f32 v[38:39], v[20:21], v[82:83], v[38:39] op_sel_hi:[0,1,1]
	v_pk_fma_f32 v[36:37], v[18:19], v[58:59], v[36:37] op_sel_hi:[0,1,1]
	v_pk_fma_f32 v[38:39], v[30:31], v[94:95], v[38:39] op_sel_hi:[0,1,1]
	v_pk_fma_f32 v[36:37], v[18:19], v[76:77], v[36:37] op_sel:[1,0,0]
	s_waitcnt lgkmcnt(4)
	v_pk_fma_f32 v[38:39], v[14:15], v[98:99], v[38:39] op_sel_hi:[0,1,1]
	v_pk_fma_f32 v[36:37], v[20:21], v[84:85], v[36:37] op_sel_hi:[0,1,1]
	s_waitcnt lgkmcnt(3)
	v_pk_fma_f32 v[38:39], v[14:15], v[102:103], v[38:39] op_sel:[1,0,0]
	v_pk_fma_f32 v[36:37], v[30:31], v[96:97], v[36:37] op_sel_hi:[0,1,1]
	s_waitcnt lgkmcnt(1)
	v_pk_fma_f32 v[118:119], v[16:17], v[40:41], v[118:119] op_sel_hi:[0,1,1]
	s_waitcnt lgkmcnt(0)
	v_pk_fma_f32 v[136:137], v[16:17], v[48:49], v[38:39] op_sel_hi:[0,1,1]
	v_pk_fma_f32 v[40:41], v[14:15], v[100:101], v[36:37] op_sel_hi:[0,1,1]
	ds_read_b128 v[36:39], v67 offset:39776
	v_pk_fma_f32 v[124:125], v[16:17], v[44:45], v[114:115] op_sel_hi:[0,1,1]
	v_pk_fma_f32 v[64:65], v[16:17], v[46:47], v[64:65] op_sel_hi:[0,1,1]
	ds_read_b128 v[44:47], v67 offset:41536
	v_pk_fma_f32 v[40:41], v[14:15], v[104:105], v[40:41] op_sel:[1,0,0]
	v_pk_fma_f32 v[130:131], v[16:17], v[42:43], v[112:113] op_sel_hi:[0,1,1]
	v_pk_fma_f32 v[138:139], v[16:17], v[50:51], v[40:41] op_sel_hi:[0,1,1]
	s_waitcnt lgkmcnt(1)
	v_pk_fma_f32 v[52:53], v[24:25], v[36:37], v[34:35] op_sel_hi:[0,1,1]
	s_waitcnt lgkmcnt(0)
	v_pk_fma_f32 v[132:133], v[16:17], v[44:45], v[60:61] op_sel_hi:[0,1,1]
	v_pk_fma_f32 v[134:135], v[16:17], v[46:47], v[62:63] op_sel_hi:[0,1,1]
	ds_read_b128 v[40:43], v67 offset:40032
	ds_read_b128 v[44:47], v67 offset:39792
	ds_read_b128 v[34:37], v67 offset:40288
	ds_read_b128 v[48:51], v67 offset:40048
	v_pk_fma_f32 v[28:29], v[24:25], v[38:39], v[28:29] op_sel_hi:[0,1,1]
	s_waitcnt lgkmcnt(3)
	v_pk_fma_f32 v[40:41], v[18:19], v[40:41], v[52:53] op_sel_hi:[0,1,1]
	ds_read_b128 v[52:55], v67 offset:40544
	ds_read_b128 v[56:59], v67 offset:40304
	ds_read_b128 v[60:63], v67 offset:40800
	ds_read_b128 v[74:77], v67 offset:40560
	ds_read_b128 v[78:81], v67 offset:41056
	ds_read_b128 v[82:85], v67 offset:40816
	s_waitcnt lgkmcnt(7)
	v_pk_fma_f32 v[34:35], v[18:19], v[34:35], v[40:41] op_sel:[1,0,0]
	ds_read_b128 v[86:89], v67 offset:41312
	ds_read_b128 v[90:93], v67 offset:41072
	s_waitcnt lgkmcnt(7)
	v_pk_fma_f32 v[34:35], v[20:21], v[52:53], v[34:35] op_sel_hi:[0,1,1]
	s_waitcnt lgkmcnt(5)
	v_pk_fma_f32 v[34:35], v[30:31], v[60:61], v[34:35] op_sel_hi:[0,1,1]
	ds_read_b128 v[94:97], v67 offset:41568
	ds_read_b128 v[98:101], v67 offset:41728
	ds_read_b128 v[102:105], v67 offset:41328
	s_waitcnt lgkmcnt(6)
	v_pk_fma_f32 v[34:35], v[14:15], v[78:79], v[34:35] op_sel_hi:[0,1,1]
	v_pk_fma_f32 v[28:29], v[18:19], v[42:43], v[28:29] op_sel_hi:[0,1,1]
	s_waitcnt lgkmcnt(4)
	v_pk_fma_f32 v[34:35], v[14:15], v[86:87], v[34:35] op_sel:[1,0,0]
	v_pk_fma_f32 v[28:29], v[18:19], v[36:37], v[28:29] op_sel:[1,0,0]
	s_waitcnt lgkmcnt(2)
	v_pk_fma_f32 v[60:61], v[16:17], v[94:95], v[34:35] op_sel_hi:[0,1,1]
	v_pk_fma_f32 v[28:29], v[20:21], v[54:55], v[28:29] op_sel_hi:[0,1,1]
	ds_read_b128 v[34:37], v67 offset:41792
	ds_read_b128 v[38:41], v67 offset:41808
	ds_read_b128 v[52:55], v67 offset:41824
	v_pk_fma_f32 v[26:27], v[24:25], v[44:45], v[26:27] op_sel_hi:[0,1,1]
	v_pk_fma_f32 v[28:29], v[30:31], v[62:63], v[28:29] op_sel_hi:[0,1,1]
	v_pk_fma_f32 v[26:27], v[18:19], v[48:49], v[26:27] op_sel_hi:[0,1,1]
	v_pk_fma_f32 v[28:29], v[14:15], v[80:81], v[28:29] op_sel_hi:[0,1,1]
	v_pk_fma_f32 v[26:27], v[18:19], v[56:57], v[26:27] op_sel:[1,0,0]
	v_pk_fma_f32 v[28:29], v[14:15], v[88:89], v[28:29] op_sel:[1,0,0]
	v_pk_fma_f32 v[26:27], v[20:21], v[74:75], v[26:27] op_sel_hi:[0,1,1]
	ds_read_b128 v[106:109], v67 offset:41584
	ds_read_b128 v[110:113], v67 offset:41744
	v_pk_fma_f32 v[28:29], v[16:17], v[96:97], v[28:29] op_sel_hi:[0,1,1]
	v_pk_fma_f32 v[26:27], v[30:31], v[82:83], v[26:27] op_sel_hi:[0,1,1]
	s_waitcnt lgkmcnt(4)
	v_pk_fma_f32 v[62:63], v[32:33], v[34:35], v[132:133] op_sel_hi:[0,1,1]
	v_pk_fma_f32 v[80:81], v[32:33], v[36:37], v[134:135] op_sel_hi:[0,1,1]
	s_waitcnt lgkmcnt(3)
	v_pk_fma_f32 v[88:89], v[32:33], v[38:39], v[136:137] op_sel_hi:[0,1,1]
	ds_read_b128 v[34:37], v67 offset:41840
	s_waitcnt lgkmcnt(3)
	v_pk_fma_f32 v[54:55], v[32:33], v[54:55], v[28:29] op_sel_hi:[0,1,1]
	v_pk_fma_f32 v[38:39], v[14:15], v[90:91], v[26:27] op_sel_hi:[0,1,1]
	ds_read_b128 v[26:29], v67 offset:41984
	v_pk_fma_f32 v[22:23], v[24:25], v[46:47], v[22:23] op_sel_hi:[0,1,1]
	v_pk_fma_f32 v[38:39], v[14:15], v[102:103], v[38:39] op_sel:[1,0,0]
	v_pk_fma_f32 v[22:23], v[18:19], v[50:51], v[22:23] op_sel_hi:[0,1,1]
	v_pk_fma_f32 v[78:79], v[32:33], v[98:99], v[120:121] op_sel_hi:[0,1,1]
	ds_read_b128 v[114:117], v67 offset:41760
	v_pk_fma_f32 v[86:87], v[32:33], v[100:101], v[122:123] op_sel_hi:[0,1,1]
	ds_read_b128 v[98:101], v67 offset:41776
	s_waitcnt lgkmcnt(5)
	v_pk_fma_f32 v[38:39], v[16:17], v[106:107], v[38:39] op_sel_hi:[0,1,1]
	v_pk_fma_f32 v[18:19], v[18:19], v[58:59], v[22:23] op_sel:[1,0,0]
	v_pk_fma_f32 v[96:97], v[32:33], v[40:41], v[138:139] op_sel_hi:[0,1,1]
	s_waitcnt lgkmcnt(3)
	v_pk_fma_f32 v[34:35], v[32:33], v[34:35], v[38:39] op_sel_hi:[0,1,1]
	ds_read_b128 v[38:41], v67 offset:42000
	s_waitcnt lgkmcnt(3)
	v_pk_fma_f32 v[48:49], v[10:11], v[26:27], v[78:79] op_sel_hi:[0,1,1]
	ds_read_b128 v[42:45], v67 offset:42016
	v_pk_fma_f32 v[56:57], v[10:11], v[28:29], v[86:87] op_sel_hi:[0,1,1]
	ds_read_b128 v[26:29], v67 offset:42032
	v_pk_fma_f32 v[18:19], v[20:21], v[76:77], v[18:19] op_sel_hi:[0,1,1]
	v_pk_fma_f32 v[18:19], v[30:31], v[84:85], v[18:19] op_sel_hi:[0,1,1]
	v_pk_fma_f32 v[18:19], v[14:15], v[92:93], v[18:19] op_sel_hi:[0,1,1]
	v_pk_fma_f32 v[14:15], v[14:15], v[104:105], v[18:19] op_sel:[1,0,0]
	v_pk_fma_f32 v[64:65], v[32:33], v[112:113], v[64:65] op_sel_hi:[0,1,1]
	s_waitcnt lgkmcnt(3)
	v_pk_fma_f32 v[98:99], v[32:33], v[98:99], v[118:119] op_sel_hi:[0,1,1]
	v_pk_fma_f32 v[14:15], v[16:17], v[108:109], v[14:15] op_sel_hi:[0,1,1]
	s_waitcnt lgkmcnt(2)
	v_pk_fma_f32 v[40:41], v[10:11], v[40:41], v[64:65] op_sel_hi:[0,1,1]
	s_waitcnt lgkmcnt(0)
	v_pk_fma_f32 v[64:65], v[10:11], v[26:27], v[98:99] op_sel_hi:[0,1,1]
	ds_read_b128 v[18:21], v67 offset:42048
	v_pk_fma_f32 v[26:27], v[32:33], v[36:37], v[14:15] op_sel_hi:[0,1,1]
	ds_read_b128 v[14:17], v67 offset:42064
	ds_read_b128 v[22:25], v67 offset:42080
	v_pk_fma_f32 v[52:53], v[32:33], v[52:53], v[60:61] op_sel_hi:[0,1,1]
	s_waitcnt lgkmcnt(2)
	v_pk_fma_f32 v[46:47], v[10:11], v[18:19], v[62:63] op_sel_hi:[0,1,1]
	v_pk_fma_f32 v[50:51], v[10:11], v[20:21], v[80:81] op_sel_hi:[0,1,1]
	s_waitcnt lgkmcnt(1)
	v_pk_fma_f32 v[58:59], v[10:11], v[14:15], v[88:89] op_sel_hi:[0,1,1]
	ds_read_b128 v[18:21], v67 offset:42096
	v_pk_fma_f32 v[62:63], v[10:11], v[16:17], v[96:97] op_sel_hi:[0,1,1]
	s_waitcnt lgkmcnt(1)
	v_pk_fma_f32 v[52:53], v[10:11], v[22:23], v[52:53] op_sel_hi:[0,1,1]
	ds_read_b128 v[14:17], v67 offset:42240
	v_pk_fma_f32 v[54:55], v[10:11], v[24:25], v[54:55] op_sel_hi:[0,1,1]
	ds_read_b128 v[22:25], v67 offset:42256
	v_pk_fma_f32 v[94:95], v[32:33], v[110:111], v[124:125] op_sel_hi:[0,1,1]
	v_pk_fma_f32 v[110:111], v[32:33], v[114:115], v[126:127] op_sel_hi:[0,1,1]
	v_pk_fma_f32 v[38:39], v[10:11], v[38:39], v[94:95] op_sel_hi:[0,1,1]
	v_pk_fma_f32 v[60:61], v[10:11], v[42:43], v[110:111] op_sel_hi:[0,1,1]
	s_waitcnt lgkmcnt(2)
	v_pk_fma_f32 v[74:75], v[10:11], v[18:19], v[34:35] op_sel_hi:[0,1,1]
	v_pk_fma_f32 v[76:77], v[10:11], v[20:21], v[26:27] op_sel_hi:[0,1,1]
	s_waitcnt lgkmcnt(1)
	v_pk_fma_f32 v[34:35], v[10:11], v[14:15], v[48:49] op_sel:[1,0,0]
	ds_read_b128 v[18:21], v67 offset:42272
	s_waitcnt lgkmcnt(1)
	v_pk_fma_f32 v[42:43], v[10:11], v[22:23], v[38:39] op_sel:[1,0,0]
	v_pk_fma_f32 v[48:49], v[10:11], v[24:25], v[40:41] op_sel:[1,0,0]
	ds_read_b128 v[22:25], v67 offset:42304
	ds_read_b128 v[38:41], v67 offset:42320
	v_pk_fma_f32 v[100:101], v[32:33], v[100:101], v[130:131] op_sel_hi:[0,1,1]
	v_pk_fma_f32 v[112:113], v[32:33], v[116:117], v[128:129] op_sel_hi:[0,1,1]
	v_pk_fma_f32 v[32:33], v[10:11], v[28:29], v[100:101] op_sel_hi:[0,1,1]
	ds_read_b128 v[26:29], v67 offset:42288
	v_pk_fma_f32 v[44:45], v[10:11], v[44:45], v[112:113] op_sel_hi:[0,1,1]
	s_waitcnt lgkmcnt(3)
	v_pk_fma_f32 v[14:15], v[10:11], v[20:21], v[44:45] op_sel:[1,0,0]
	s_waitcnt lgkmcnt(2)
	v_pk_fma_f32 v[90:91], v[10:11], v[22:23], v[46:47] op_sel:[1,0,0]
	ds_read_b128 v[20:23], v67 offset:42336
	v_pk_fma_f32 v[36:37], v[10:11], v[16:17], v[56:57] op_sel:[1,0,0]
	s_waitcnt lgkmcnt(1)
	v_pk_fma_f32 v[16:17], v[10:11], v[26:27], v[64:65] op_sel:[1,0,0]
	v_pk_fma_f32 v[92:93], v[10:11], v[24:25], v[50:51] op_sel:[1,0,0]
	ds_read_b128 v[24:27], v67 offset:42352
	s_waitcnt lgkmcnt(1)
	v_pk_fma_f32 v[88:89], v[10:11], v[20:21], v[52:53] op_sel:[1,0,0]
	v_pk_fma_f32 v[96:97], v[10:11], v[22:23], v[54:55] op_sel:[1,0,0]
	ds_read_b128 v[20:23], v67 offset:42608
	v_pk_fma_f32 v[30:31], v[10:11], v[18:19], v[60:61] op_sel:[1,0,0]
	v_pk_fma_f32 v[18:19], v[10:11], v[28:29], v[32:33] op_sel:[1,0,0]
	v_pk_fma_f32 v[94:95], v[10:11], v[38:39], v[58:59] op_sel:[1,0,0]
	v_pk_fma_f32 v[86:87], v[10:11], v[40:41], v[62:63] op_sel:[1,0,0]
	s_waitcnt lgkmcnt(1)
	v_pk_fma_f32 v[98:99], v[10:11], v[24:25], v[74:75] op_sel:[1,0,0]
	v_pk_fma_f32 v[10:11], v[10:11], v[26:27], v[76:77] op_sel:[1,0,0]
	ds_read_b128 v[24:27], v67 offset:42864
	ds_read_b128 v[38:41], v67 offset:42592
	s_waitcnt lgkmcnt(2)
	v_pk_fma_f32 v[22:23], v[12:13], v[22:23], v[10:11] op_sel_hi:[0,1,1]
	v_mov_b32_e32 v10, v13
	ds_read_b128 v[44:47], v67 offset:43120
	ds_read_b128 v[52:55], v67 offset:42848
	s_waitcnt lgkmcnt(3)
	v_pk_fma_f32 v[22:23], v[10:11], v[26:27], v[22:23] op_sel_hi:[0,1,1]
	ds_read_b128 v[26:29], v67 offset:43376
	ds_read_b128 v[56:59], v67 offset:43104
	ds_read_b128 v[60:63], v67 offset:43632
	ds_read_b128 v[74:77], v67 offset:43360
	v_pk_fma_f32 v[20:21], v[12:13], v[20:21], v[98:99] op_sel_hi:[0,1,1]
	ds_read_b128 v[78:81], v67 offset:43888
	ds_read_b128 v[82:85], v67 offset:43616
	v_pk_fma_f32 v[20:21], v[10:11], v[24:25], v[20:21] op_sel_hi:[0,1,1]
	s_waitcnt lgkmcnt(7)
	v_pk_fma_f32 v[20:21], v[6:7], v[44:45], v[20:21] op_sel_hi:[0,1,1]
	v_pk_fma_f32 v[22:23], v[6:7], v[46:47], v[22:23] op_sel_hi:[0,1,1]
	s_waitcnt lgkmcnt(5)
	v_pk_fma_f32 v[20:21], v[6:7], v[26:27], v[20:21] op_sel:[1,0,0]
	v_pk_fma_f32 v[22:23], v[6:7], v[28:29], v[22:23] op_sel:[1,0,0]
	v_mov_b32_e32 v50, v9
	s_waitcnt lgkmcnt(3)
	v_pk_fma_f32 v[20:21], v[8:9], v[60:61], v[20:21] op_sel_hi:[0,1,1]
	v_pk_fma_f32 v[22:23], v[8:9], v[62:63], v[22:23] op_sel_hi:[0,1,1]
	ds_read_b128 v[62:65], v67 offset:43872
	s_waitcnt lgkmcnt(2)
	v_pk_fma_f32 v[98:99], v[50:51], v[78:79], v[20:21] op_sel_hi:[0,1,1]
	v_pk_fma_f32 v[20:21], v[12:13], v[40:41], v[96:97] op_sel_hi:[0,1,1]
	v_pk_fma_f32 v[20:21], v[10:11], v[54:55], v[20:21] op_sel_hi:[0,1,1]
	v_pk_fma_f32 v[20:21], v[6:7], v[58:59], v[20:21] op_sel_hi:[0,1,1]
	v_pk_fma_f32 v[20:21], v[6:7], v[76:77], v[20:21] op_sel:[1,0,0]
	v_pk_fma_f32 v[100:101], v[50:51], v[80:81], v[22:23] op_sel_hi:[0,1,1]
	s_waitcnt lgkmcnt(1)
	v_pk_fma_f32 v[20:21], v[8:9], v[84:85], v[20:21] op_sel_hi:[0,1,1]
	s_waitcnt lgkmcnt(0)
	v_pk_fma_f32 v[64:65], v[50:51], v[64:65], v[20:21] op_sel_hi:[0,1,1]
	v_pk_fma_f32 v[20:21], v[12:13], v[38:39], v[88:89] op_sel_hi:[0,1,1]
	v_pk_fma_f32 v[20:21], v[10:11], v[52:53], v[20:21] op_sel_hi:[0,1,1]
	v_pk_fma_f32 v[20:21], v[6:7], v[56:57], v[20:21] op_sel_hi:[0,1,1]
	v_pk_fma_f32 v[24:25], v[6:7], v[74:75], v[20:21] op_sel:[1,0,0]
	ds_read_b128 v[20:23], v67 offset:42576
	v_pk_fma_f32 v[24:25], v[8:9], v[82:83], v[24:25] op_sel_hi:[0,1,1]
	v_pk_fma_f32 v[96:97], v[50:51], v[62:63], v[24:25] op_sel_hi:[0,1,1]
	ds_read_b128 v[24:27], v67 offset:42832
	ds_read_b128 v[52:55], v67 offset:42560
	ds_read_b128 v[38:41], v67 offset:43088
	ds_read_b128 v[56:59], v67 offset:42816
	s_waitcnt lgkmcnt(4)
	v_pk_fma_f32 v[22:23], v[12:13], v[22:23], v[86:87] op_sel_hi:[0,1,1]
	v_pk_fma_f32 v[20:21], v[12:13], v[20:21], v[94:95] op_sel_hi:[0,1,1]
	s_waitcnt lgkmcnt(3)
	v_pk_fma_f32 v[22:23], v[10:11], v[26:27], v[22:23] op_sel_hi:[0,1,1]
	ds_read_b128 v[26:29], v67 offset:43344
	ds_read_b128 v[60:63], v67 offset:43072
	ds_read_b128 v[44:47], v67 offset:43600
	ds_read_b128 v[74:77], v67 offset:43856
	ds_read_b128 v[78:81], v67 offset:43328
	s_waitcnt lgkmcnt(6)
	v_pk_fma_f32 v[22:23], v[6:7], v[40:41], v[22:23] op_sel_hi:[0,1,1]
	v_pk_fma_f32 v[20:21], v[10:11], v[24:25], v[20:21] op_sel_hi:[0,1,1]
	s_waitcnt lgkmcnt(4)
	v_pk_fma_f32 v[22:23], v[6:7], v[28:29], v[22:23] op_sel:[1,0,0]
	v_pk_fma_f32 v[24:25], v[6:7], v[38:39], v[20:21] op_sel_hi:[0,1,1]
	s_waitcnt lgkmcnt(2)
	v_pk_fma_f32 v[22:23], v[8:9], v[46:47], v[22:23] op_sel_hi:[0,1,1]
	s_waitcnt lgkmcnt(1)
	v_pk_fma_f32 v[28:29], v[50:51], v[76:77], v[22:23] op_sel_hi:[0,1,1]
	ds_read_b128 v[20:23], v67 offset:44112
	v_pk_fma_f32 v[24:25], v[6:7], v[26:27], v[24:25] op_sel:[1,0,0]
	ds_read_b128 v[82:85], v67 offset:43584
	ds_read_b128 v[86:89], v67 offset:43840
	v_pk_fma_f32 v[24:25], v[8:9], v[44:45], v[24:25] op_sel_hi:[0,1,1]
	v_pk_fma_f32 v[38:39], v[50:51], v[74:75], v[24:25] op_sel_hi:[0,1,1]
	ds_read_b128 v[24:27], v67 offset:44096
	s_waitcnt lgkmcnt(3)
	v_pk_fma_f32 v[106:107], v[2:3], v[20:21], v[38:39] op_sel_hi:[0,1,1]
	v_pk_fma_f32 v[20:21], v[12:13], v[54:55], v[92:93] op_sel_hi:[0,1,1]
	v_pk_fma_f32 v[20:21], v[10:11], v[58:59], v[20:21] op_sel_hi:[0,1,1]
	v_pk_fma_f32 v[20:21], v[6:7], v[62:63], v[20:21] op_sel_hi:[0,1,1]
	v_pk_fma_f32 v[108:109], v[2:3], v[22:23], v[28:29] op_sel_hi:[0,1,1]
	v_pk_fma_f32 v[28:29], v[6:7], v[80:81], v[20:21] op_sel:[1,0,0]
	ds_read_b128 v[20:23], v67 offset:44128
	s_waitcnt lgkmcnt(3)
	v_pk_fma_f32 v[28:29], v[8:9], v[84:85], v[28:29] op_sel_hi:[0,1,1]
	s_waitcnt lgkmcnt(2)
	v_pk_fma_f32 v[28:29], v[50:51], v[88:89], v[28:29] op_sel_hi:[0,1,1]
	ds_read_b128 v[38:41], v67 offset:44144
	s_waitcnt lgkmcnt(2)
	v_pk_fma_f32 v[110:111], v[2:3], v[26:27], v[28:29] op_sel_hi:[0,1,1]
	s_waitcnt lgkmcnt(1)
	v_pk_fma_f32 v[46:47], v[2:3], v[20:21], v[96:97] op_sel_hi:[0,1,1]
	v_pk_fma_f32 v[20:21], v[12:13], v[52:53], v[90:91] op_sel_hi:[0,1,1]
	v_pk_fma_f32 v[20:21], v[10:11], v[56:57], v[20:21] op_sel_hi:[0,1,1]
	v_pk_fma_f32 v[20:21], v[6:7], v[60:61], v[20:21] op_sel_hi:[0,1,1]
	v_pk_fma_f32 v[20:21], v[6:7], v[78:79], v[20:21] op_sel:[1,0,0]
	v_pk_fma_f32 v[44:45], v[2:3], v[22:23], v[64:65] op_sel_hi:[0,1,1]
	v_pk_fma_f32 v[26:27], v[8:9], v[82:83], v[20:21] op_sel_hi:[0,1,1]
	ds_read_b128 v[20:23], v67 offset:42544
	v_pk_fma_f32 v[26:27], v[50:51], v[86:87], v[26:27] op_sel_hi:[0,1,1]
	v_pk_fma_f32 v[64:65], v[2:3], v[24:25], v[26:27] op_sel_hi:[0,1,1]
	ds_read_b128 v[26:29], v67 offset:42800
	ds_read_b128 v[74:77], v67 offset:42528
	ds_read_b128 v[52:55], v67 offset:43056
	ds_read_b128 v[78:81], v67 offset:42784
	ds_read_b128 v[56:59], v67 offset:43312
	ds_read_b128 v[82:85], v67 offset:43040
	s_waitcnt lgkmcnt(6)
	v_pk_fma_f32 v[18:19], v[12:13], v[22:23], v[18:19] op_sel_hi:[0,1,1]
	ds_read_b128 v[60:63], v67 offset:43568
	ds_read_b128 v[86:89], v67 offset:43296
	s_waitcnt lgkmcnt(7)
	v_pk_fma_f32 v[18:19], v[10:11], v[28:29], v[18:19] op_sel_hi:[0,1,1]
	v_pk_fma_f32 v[38:39], v[2:3], v[38:39], v[98:99] op_sel_hi:[0,1,1]
	v_pk_fma_f32 v[40:41], v[2:3], v[40:41], v[100:101] op_sel_hi:[0,1,1]
	s_waitcnt lgkmcnt(5)
	v_pk_fma_f32 v[18:19], v[6:7], v[54:55], v[18:19] op_sel_hi:[0,1,1]
	ds_read_b128 v[90:93], v67 offset:43824
	ds_read_b128 v[94:97], v67 offset:44080
	ds_read_b128 v[98:101], v67 offset:43552
	v_pk_fma_f32 v[16:17], v[12:13], v[20:21], v[16:17] op_sel_hi:[0,1,1]
	s_waitcnt lgkmcnt(6)
	v_pk_fma_f32 v[18:19], v[6:7], v[58:59], v[18:19] op_sel:[1,0,0]
	v_pk_fma_f32 v[16:17], v[10:11], v[26:27], v[16:17] op_sel_hi:[0,1,1]
	s_waitcnt lgkmcnt(4)
	v_pk_fma_f32 v[18:19], v[8:9], v[62:63], v[18:19] op_sel_hi:[0,1,1]
	v_pk_fma_f32 v[16:17], v[6:7], v[52:53], v[16:17] op_sel_hi:[0,1,1]
	s_waitcnt lgkmcnt(2)
	v_pk_fma_f32 v[18:19], v[50:51], v[92:93], v[18:19] op_sel_hi:[0,1,1]
	v_pk_fma_f32 v[16:17], v[6:7], v[56:57], v[16:17] op_sel:[1,0,0]
	s_waitcnt lgkmcnt(1)
	v_pk_fma_f32 v[62:63], v[2:3], v[96:97], v[18:19] op_sel_hi:[0,1,1]
	v_pk_fma_f32 v[20:21], v[8:9], v[60:61], v[16:17] op_sel_hi:[0,1,1]
	ds_read_b128 v[16:19], v67 offset:44336
	ds_read_b128 v[102:105], v67 offset:43808
	ds_read_b128 v[22:25], v67 offset:44064
	v_pk_fma_f32 v[14:15], v[12:13], v[76:77], v[14:15] op_sel_hi:[0,1,1]
	v_pk_fma_f32 v[14:15], v[10:11], v[80:81], v[14:15] op_sel_hi:[0,1,1]
	v_pk_fma_f32 v[20:21], v[50:51], v[90:91], v[20:21] op_sel_hi:[0,1,1]
	ds_read_b128 v[52:55], v67 offset:44352
	ds_read_b128 v[26:29], v67 offset:44320
	v_pk_fma_f32 v[14:15], v[6:7], v[84:85], v[14:15] op_sel_hi:[0,1,1]
	v_pk_fma_f32 v[20:21], v[2:3], v[94:95], v[20:21] op_sel_hi:[0,1,1]
	v_pk_fma_f32 v[14:15], v[6:7], v[88:89], v[14:15] op_sel:[1,0,0]
	s_waitcnt lgkmcnt(4)
	v_pk_fma_f32 v[58:59], v[2:3], v[16:17], v[20:21] op_sel:[1,0,0]
	v_pk_fma_f32 v[60:61], v[2:3], v[18:19], v[62:63] op_sel:[1,0,0]
	ds_read_b128 v[16:19], v67 offset:44368
	v_pk_fma_f32 v[14:15], v[8:9], v[100:101], v[14:15] op_sel_hi:[0,1,1]
	s_waitcnt lgkmcnt(4)
	v_pk_fma_f32 v[14:15], v[50:51], v[104:105], v[14:15] op_sel_hi:[0,1,1]
	s_waitcnt lgkmcnt(3)
	v_pk_fma_f32 v[14:15], v[2:3], v[24:25], v[14:15] op_sel_hi:[0,1,1]
	s_waitcnt lgkmcnt(1)
	v_pk_fma_f32 v[62:63], v[2:3], v[28:29], v[14:15] op_sel:[1,0,0]
	v_pk_fma_f32 v[28:29], v[12:13], v[74:75], v[30:31] op_sel_hi:[0,1,1]
	v_pk_fma_f32 v[28:29], v[10:11], v[78:79], v[28:29] op_sel_hi:[0,1,1]
	v_lshlrev_b32_e32 v11, 3, v1
	s_waitcnt lgkmcnt(0)
	v_pk_fma_f32 v[56:57], v[2:3], v[16:17], v[106:107] op_sel:[1,0,0]
	v_pk_fma_f32 v[24:25], v[2:3], v[18:19], v[108:109] op_sel:[1,0,0]
	ds_read_b128 v[18:21], v67 offset:44384
	ds_read_b128 v[14:17], v67 offset:44400
	global_load_dwordx2 a[0:1], v11, s[6:7]
	v_pk_fma_f32 v[28:29], v[6:7], v[82:83], v[28:29] op_sel_hi:[0,1,1]
	v_pk_fma_f32 v[28:29], v[6:7], v[86:87], v[28:29] op_sel:[1,0,0]
	v_pk_fma_f32 v[52:53], v[2:3], v[52:53], v[64:65] op_sel:[1,0,0]
	v_pk_fma_f32 v[28:29], v[8:9], v[98:99], v[28:29] op_sel_hi:[0,1,1]
	v_pk_fma_f32 v[64:65], v[50:51], v[102:103], v[28:29] op_sel_hi:[0,1,1]
	ds_read_b128 v[28:31], v67 offset:42512
	ds_read_b128 v[74:77], v67 offset:42768
	ds_read_b128 v[78:81], v67 offset:42496
	ds_read_b128 v[82:85], v67 offset:43024
	ds_read_b128 v[86:89], v67 offset:42752
	v_pk_fma_f32 v[22:23], v[2:3], v[22:23], v[64:65] op_sel_hi:[0,1,1]
	ds_read_b128 v[90:93], v67 offset:43280
	ds_read_b128 v[94:97], v67 offset:43008
	v_pk_fma_f32 v[22:23], v[2:3], v[26:27], v[22:23] op_sel:[1,0,0]
	s_waitcnt lgkmcnt(6)
	v_pk_fma_f32 v[26:27], v[12:13], v[30:31], v[48:49] op_sel_hi:[0,1,1]
	ds_read_b128 v[98:101], v67 offset:43536
	ds_read_b128 v[102:105], v67 offset:43264
	v_pk_fma_f32 v[54:55], v[2:3], v[54:55], v[110:111] op_sel:[1,0,0]
	s_waitcnt lgkmcnt(7)
	v_pk_fma_f32 v[26:27], v[10:11], v[76:77], v[26:27] op_sel_hi:[0,1,1]
	ds_read_b128 v[106:109], v67 offset:43792
	ds_read_b128 v[110:113], v67 offset:43520
	s_waitcnt lgkmcnt(7)
	v_pk_fma_f32 v[26:27], v[6:7], v[84:85], v[26:27] op_sel_hi:[0,1,1]
	ds_read_b128 v[114:117], v67 offset:44048
	ds_read_b128 v[118:121], v67 offset:43776
	s_waitcnt lgkmcnt(7)
	v_pk_fma_f32 v[26:27], v[6:7], v[92:93], v[26:27] op_sel:[1,0,0]
	ds_read_b128 v[122:125], v67 offset:44304
	ds_read_b128 v[126:129], v67 offset:44032
	s_waitcnt lgkmcnt(7)
	v_pk_fma_f32 v[26:27], v[8:9], v[100:101], v[26:27] op_sel_hi:[0,1,1]
	s_waitcnt lgkmcnt(5)
	v_pk_fma_f32 v[26:27], v[50:51], v[108:109], v[26:27] op_sel_hi:[0,1,1]
	ds_read_b128 v[130:133], v67 offset:44560
	ds_read_b128 v[134:137], v67 offset:44576
	ds_read_b128 v[138:141], v67 offset:44288
	s_waitcnt lgkmcnt(6)
	v_pk_fma_f32 v[26:27], v[2:3], v[116:117], v[26:27] op_sel_hi:[0,1,1]
	s_waitcnt lgkmcnt(4)
	v_pk_fma_f32 v[26:27], v[2:3], v[124:125], v[26:27] op_sel:[1,0,0]
	ds_read_b128 v[142:145], v67 offset:44592
	ds_read_b128 v[146:149], v67 offset:44544
	s_waitcnt lgkmcnt(4)
	v_pk_fma_f32 v[30:31], v[4:5], v[132:133], v[26:27] op_sel_hi:[0,1,1]
	v_pk_fma_f32 v[26:27], v[12:13], v[28:29], v[42:43] op_sel_hi:[0,1,1]
	v_pk_fma_f32 v[26:27], v[10:11], v[74:75], v[26:27] op_sel_hi:[0,1,1]
	v_pk_fma_f32 v[26:27], v[6:7], v[82:83], v[26:27] op_sel_hi:[0,1,1]
	v_pk_fma_f32 v[26:27], v[6:7], v[90:91], v[26:27] op_sel:[1,0,0]
	s_waitcnt lgkmcnt(1)
	v_pk_fma_f32 v[76:77], v[4:5], v[142:143], v[58:59] op_sel_hi:[0,1,1]
	v_pk_fma_f32 v[26:27], v[8:9], v[98:99], v[26:27] op_sel_hi:[0,1,1]
	v_pk_fma_f32 v[26:27], v[50:51], v[106:107], v[26:27] op_sel_hi:[0,1,1]
	v_pk_fma_f32 v[26:27], v[2:3], v[114:115], v[26:27] op_sel_hi:[0,1,1]
	v_pk_fma_f32 v[26:27], v[2:3], v[122:123], v[26:27] op_sel:[1,0,0]
	v_pk_fma_f32 v[84:85], v[4:5], v[144:145], v[60:61] op_sel_hi:[0,1,1]
	v_pk_fma_f32 v[42:43], v[4:5], v[130:131], v[26:27] op_sel_hi:[0,1,1]
	v_pk_fma_f32 v[26:27], v[12:13], v[80:81], v[36:37] op_sel_hi:[0,1,1]
	v_pk_fma_f32 v[12:13], v[12:13], v[78:79], v[34:35] op_sel_hi:[0,1,1]
	v_pk_fma_f32 v[26:27], v[10:11], v[88:89], v[26:27] op_sel_hi:[0,1,1]
	v_pk_fma_f32 v[10:11], v[10:11], v[86:87], v[12:13] op_sel_hi:[0,1,1]
	v_pk_fma_f32 v[26:27], v[6:7], v[96:97], v[26:27] op_sel_hi:[0,1,1]
	v_pk_fma_f32 v[10:11], v[6:7], v[94:95], v[10:11] op_sel_hi:[0,1,1]
	v_pk_fma_f32 v[26:27], v[6:7], v[104:105], v[26:27] op_sel:[1,0,0]
	v_pk_fma_f32 v[6:7], v[6:7], v[102:103], v[10:11] op_sel:[1,0,0]
	v_pk_fma_f32 v[26:27], v[8:9], v[112:113], v[26:27] op_sel_hi:[0,1,1]
	v_pk_fma_f32 v[6:7], v[8:9], v[110:111], v[6:7] op_sel_hi:[0,1,1]
	v_pk_fma_f32 v[26:27], v[50:51], v[120:121], v[26:27] op_sel_hi:[0,1,1]
	v_pk_fma_f32 v[6:7], v[50:51], v[118:119], v[6:7] op_sel_hi:[0,1,1]
	v_pk_fma_f32 v[36:37], v[2:3], v[128:129], v[26:27] op_sel_hi:[0,1,1]
	ds_read_b128 v[26:29], v67 offset:44800
	ds_read_b128 v[58:61], v67 offset:44816
	v_pk_fma_f32 v[10:11], v[2:3], v[126:127], v[6:7] op_sel_hi:[0,1,1]
	ds_read_b128 v[6:9], v67 offset:45056
	v_pk_fma_f32 v[34:35], v[2:3], v[138:139], v[10:11] op_sel:[1,0,0]
	ds_read_b128 v[10:13], v67 offset:45072
	v_pk_fma_f32 v[36:37], v[2:3], v[140:141], v[36:37] op_sel:[1,0,0]
	v_mov_b32_e32 v32, v5
	s_waitcnt lgkmcnt(4)
	v_pk_fma_f32 v[36:37], v[4:5], v[148:149], v[36:37] op_sel_hi:[0,1,1]
	v_pk_fma_f32 v[34:35], v[4:5], v[146:147], v[34:35] op_sel_hi:[0,1,1]
	s_waitcnt lgkmcnt(3)
	v_pk_fma_f32 v[36:37], v[32:33], v[28:29], v[36:37] op_sel_hi:[0,1,1]
	s_waitcnt lgkmcnt(2)
	v_pk_fma_f32 v[42:43], v[32:33], v[58:59], v[42:43] op_sel_hi:[0,1,1]
	v_pk_fma_f32 v[58:59], v[32:33], v[60:61], v[30:31] op_sel_hi:[0,1,1]
	v_pk_fma_f32 v[26:27], v[32:33], v[26:27], v[34:35] op_sel_hi:[0,1,1]
	s_waitcnt lgkmcnt(1)
	v_pk_fma_f32 v[6:7], v[68:69], v[6:7], v[26:27] op_sel_hi:[0,1,1]
	v_pk_fma_f32 v[8:9], v[68:69], v[8:9], v[36:37] op_sel_hi:[0,1,1]
	s_waitcnt lgkmcnt(0)
	v_pk_fma_f32 v[10:11], v[68:69], v[10:11], v[42:43] op_sel_hi:[0,1,1]
	v_pk_fma_f32 v[12:13], v[68:69], v[12:13], v[58:59] op_sel_hi:[0,1,1]
	v_lshlrev_b32_e32 v33, 4, v72
	v_pk_fma_f32 v[48:49], v[4:5], v[136:137], v[62:63] op_sel_hi:[0,1,1]
	ds_read_b128 v[62:65], v67 offset:44832
	v_cvt_pk_f16_f32 v6, v6, v7
	v_cvt_pk_f16_f32 v7, v8, v9
	v_cvt_pk_f16_f32 v8, v10, v11
	v_cvt_pk_f16_f32 v9, v12, v13
	ds_read_b128 v[10:13], v33
	ds_read_b128 v[28:31], v67 offset:44848
	v_pk_fma_f32 v[22:23], v[4:5], v[134:135], v[22:23] op_sel_hi:[0,1,1]
	s_waitcnt lgkmcnt(2)
	v_pk_fma_f32 v[22:23], v[32:33], v[62:63], v[22:23] op_sel_hi:[0,1,1]
	s_waitcnt vmcnt(0)
	v_accvgpr_mov_b32 a16, a0
	v_accvgpr_mov_b32 a17, a0
	v_accvgpr_mov_b32 a18, a0
	v_accvgpr_mov_b32 a19, a0
	v_accvgpr_mov_b32 a20, a0
	v_accvgpr_mov_b32 a21, a0
	v_accvgpr_mov_b32 a22, a0
	v_accvgpr_mov_b32 a23, a0
	v_accvgpr_mov_b32 a24, a0
	v_accvgpr_mov_b32 a25, a0
	v_accvgpr_mov_b32 a26, a0
	v_accvgpr_mov_b32 a27, a0
	v_accvgpr_mov_b32 a28, a0
	v_accvgpr_mov_b32 a29, a0
	v_accvgpr_mov_b32 a30, a0
	v_accvgpr_mov_b32 a31, a0
	v_accvgpr_mov_b32 a0, a1
	v_accvgpr_mov_b32 a2, a1
	s_waitcnt lgkmcnt(1)
	v_mfma_f32_32x32x16_f16 a[16:31], v[6:9], v[10:13], a[16:31]
	ds_read_b128 v[10:13], v33 offset:4096
	v_accvgpr_mov_b32 a3, a1
	v_accvgpr_mov_b32 a4, a1
	v_accvgpr_mov_b32 a5, a1
	v_accvgpr_mov_b32 a6, a1
	v_accvgpr_mov_b32 a7, a1
	v_accvgpr_mov_b32 a8, a1
	v_accvgpr_mov_b32 a9, a1
	v_accvgpr_mov_b32 a10, a1
	v_accvgpr_mov_b32 a11, a1
	v_accvgpr_mov_b32 a12, a1
	v_accvgpr_mov_b32 a13, a1
	v_accvgpr_mov_b32 a14, a1
	v_accvgpr_mov_b32 a15, a1
	v_pk_fma_f32 v[42:43], v[32:33], v[64:65], v[48:49] op_sel_hi:[0,1,1]
	s_waitcnt lgkmcnt(1)
	v_pk_fma_f32 v[62:63], v[32:33], v[28:29], v[76:77] op_sel_hi:[0,1,1]
	s_waitcnt lgkmcnt(0)
	v_mfma_f32_32x32x16_f16 a[0:15], v[6:9], v[10:13], a[0:15]
	ds_read_b128 v[34:37], v33 offset:1024
	ds_read_b128 v[10:13], v33 offset:8192
	ds_read_b128 v[48:51], v67 offset:45088
	ds_read_b128 v[58:61], v33 offset:12288
	ds_read_b128 v[26:29], v67 offset:45104
	v_pk_fma_f32 v[38:39], v[2:3], v[14:15], v[38:39] op_sel:[1,0,0]
	s_load_dwordx4 s[4:7], s[0:1], 0x40
	v_lshlrev_b32_e32 v1, 2, v1
	s_waitcnt lgkmcnt(0)
	v_mfma_f32_32x32x16_f16 a[16:31], v[6:9], v[10:13], a[16:31]
	v_fma_f32 v10, v32, v30, v84
	v_fma_f32 v11, v32, v31, v85
	v_fma_f32 v12, v68, v48, v22
	v_fma_f32 v13, v68, v49, v23
	v_fma_f32 v22, v68, v50, v42
	v_fma_f32 v23, v68, v51, v43
	v_pk_fma_f32 v[26:27], v[68:69], v[26:27], v[62:63] op_sel_hi:[0,1,1]
	v_pk_fma_f32 v[28:29], v[68:69], v[28:29], v[10:11] op_sel_hi:[0,1,1]
	v_cvt_pk_f16_f32 v10, v12, v13
	v_cvt_pk_f16_f32 v11, v22, v23
	v_cvt_pk_f16_f32 v12, v26, v27
	v_cvt_pk_f16_f32 v13, v28, v29
	v_mfma_f32_32x32x16_f16 a[0:15], v[6:9], v[58:61], a[0:15]
	ds_read_b128 v[26:29], v33 offset:5120
	ds_read_b128 v[48:51], v33 offset:9216
	ds_read_b128 v[58:61], v33 offset:13312
	ds_read_b128 v[62:65], v67 offset:44608
	v_fma_f32 v30, v3, v18, v46
	v_fma_f32 v31, v3, v19, v47
	v_pk_fma_f32 v[42:43], v[2:3], v[20:21], v[44:45] op_sel:[1,0,0]
	ds_read_b128 v[18:21], v67 offset:44864
	v_pk_fma_f32 v[2:3], v[2:3], v[16:17], v[40:41] op_sel:[1,0,0]
	s_waitcnt lgkmcnt(1)
	v_pk_fma_f32 v[22:23], v[4:5], v[62:63], v[52:53] op_sel_hi:[0,1,1]
	v_pk_fma_f32 v[44:45], v[4:5], v[64:65], v[54:55] op_sel_hi:[0,1,1]
	v_mfma_f32_32x32x16_f16 a[16:31], v[10:13], v[34:37], a[16:31]
	ds_read_b128 v[34:37], v67 offset:44624
	s_waitcnt lgkmcnt(1)
	v_fma_f32 v46, v32, v18, v22
	v_fma_f32 v47, v32, v19, v23
	v_fma_f32 v44, v32, v20, v44
	v_fma_f32 v45, v32, v21, v45
	ds_read_b128 v[18:21], v67 offset:45120
	s_waitcnt lgkmcnt(1)
	v_pk_fma_f32 v[36:37], v[4:5], v[36:37], v[24:25] op_sel_hi:[0,1,1]
	ds_read_b128 v[22:25], v67 offset:45136
	v_mfma_f32_32x32x16_f16 a[0:15], v[10:13], v[26:29], a[0:15]
	ds_read_b128 v[26:29], v67 offset:44880
	v_fma_f32 v34, v4, v34, v56
	v_fma_f32 v35, v4, v35, v57
	s_waitcnt lgkmcnt(2)
	v_fma_f32 v18, v68, v18, v46
	v_fma_f32 v19, v68, v19, v47
	v_pk_fma_f32 v[20:21], v[68:69], v[20:21], v[44:45] op_sel_hi:[0,1,1]
	v_cvt_pk_f16_f32 v18, v18, v19
	s_waitcnt lgkmcnt(0)
	v_pk_fma_f32 v[26:27], v[32:33], v[26:27], v[34:35] op_sel_hi:[0,1,1]
	v_pk_fma_f32 v[28:29], v[32:33], v[28:29], v[36:37] op_sel_hi:[0,1,1]
	v_mfma_f32_32x32x16_f16 a[16:31], v[10:13], v[48:51], a[16:31]
	v_fma_f32 v22, v68, v22, v26
	v_fma_f32 v23, v68, v23, v27
	v_fma_f32 v24, v68, v24, v28
	v_fma_f32 v25, v68, v25, v29
	v_cvt_pk_f16_f32 v19, v20, v21
	v_cvt_pk_f16_f32 v20, v22, v23
	v_cvt_pk_f16_f32 v21, v24, v25
	ds_read_b128 v[22:25], v33 offset:2048
	ds_read_b128 v[26:29], v67 offset:44640
	ds_read_b128 v[14:17], v67 offset:44656
	v_mfma_f32_32x32x16_f16 a[0:15], v[10:13], v[58:61], a[0:15]
	s_waitcnt lgkmcnt(1)
	v_fma_f32 v30, v4, v26, v30
	v_fma_f32 v31, v4, v27, v31
	v_fma_f32 v40, v4, v28, v42
	v_fma_f32 v41, v4, v29, v43
	s_waitcnt lgkmcnt(0)
	v_pk_fma_f32 v[38:39], v[4:5], v[14:15], v[38:39] op_sel_hi:[0,1,1]
	v_pk_fma_f32 v[42:43], v[4:5], v[16:17], v[2:3] op_sel_hi:[0,1,1]
	v_mfma_f32_32x32x16_f16 a[16:31], v[18:21], v[22:25], a[16:31]
	ds_read_b128 v[22:25], v33 offset:6144
	ds_read_b128 v[26:29], v33 offset:3072
	ds_read_b128 v[34:37], v67 offset:44896
	ds_read_b128 v[2:5], v67 offset:44912
	ds_read_b128 v[14:17], v33 offset:10240
	s_waitcnt lgkmcnt(2)
	v_pk_fma_f32 v[30:31], v[32:33], v[34:35], v[30:31] op_sel_hi:[0,1,1]
	v_pk_fma_f32 v[40:41], v[32:33], v[36:37], v[40:41] op_sel_hi:[0,1,1]
	v_mfma_f32_32x32x16_f16 a[0:15], v[18:21], v[22:25], a[0:15]
	ds_read_b128 v[22:25], v67 offset:45152
	ds_read_b128 v[34:37], v67 offset:45168
	s_waitcnt lgkmcnt(3)
	v_fma_f32 v38, v32, v2, v38
	v_fma_f32 v39, v32, v3, v39
	s_waitcnt lgkmcnt(2)
	v_mfma_f32_32x32x16_f16 a[16:31], v[18:21], v[14:17], a[16:31]
	v_fma_f32 v14, v32, v4, v42
	v_fma_f32 v15, v32, v5, v43
	ds_read_b128 v[2:5], v33 offset:14336
	s_waitcnt lgkmcnt(2)
	v_fma_f32 v16, v68, v22, v30
	v_fma_f32 v17, v68, v23, v31
	v_pk_fma_f32 v[22:23], v[68:69], v[24:25], v[40:41] op_sel_hi:[0,1,1]
	s_waitcnt lgkmcnt(1)
	v_pk_fma_f32 v[24:25], v[68:69], v[34:35], v[38:39] op_sel_hi:[0,1,1]
	v_pk_fma_f32 v[30:31], v[68:69], v[36:37], v[14:15] op_sel_hi:[0,1,1]
	v_cvt_pk_f16_f32 v14, v16, v17
	s_waitcnt lgkmcnt(0)
	v_mfma_f32_32x32x16_f16 a[0:15], v[18:21], v[2:5], a[0:15]
	v_cvt_pk_f16_f32 v15, v22, v23
	v_cvt_pk_f16_f32 v16, v24, v25
	v_cvt_pk_f16_f32 v17, v30, v31
	ds_read_b128 v[2:5], v33 offset:7168
	ds_read_b128 v[22:25], v33 offset:31744
	v_ashrrev_i32_e32 v67, 31, v66
	v_mfma_f32_32x32x16_f16 a[16:31], v[14:17], v[26:29], a[16:31]
	v_lshlrev_b64 v[26:27], 7, v[66:67]
	v_lshl_add_u64 v[26:27], s[4:5], 0, v[26:27]
	s_waitcnt lgkmcnt(1)
	v_mfma_f32_32x32x16_f16 a[0:15], v[14:17], v[2:5], a[0:15]
	ds_read_b128 v[2:5], v33 offset:11264
	s_waitcnt lgkmcnt(0)
	v_mfma_f32_32x32x16_f16 a[16:31], v[14:17], v[2:5], a[16:31]
	ds_read_b128 v[2:5], v33 offset:15360
	s_waitcnt lgkmcnt(0)
	v_mfma_f32_32x32x16_f16 a[0:15], v[14:17], v[2:5], a[0:15]
	ds_read_b128 v[2:5], v33 offset:16384
	s_waitcnt lgkmcnt(0)
	v_mfma_f32_32x32x16_f16 a[32:47], v[6:9], v[2:5], 0
	ds_read_b128 v[2:5], v33 offset:20480
	s_waitcnt lgkmcnt(0)
	v_mfma_f32_32x32x16_f16 a[48:63], v[6:9], v[2:5], 0
	ds_read_b128 v[2:5], v33 offset:24576
	s_waitcnt lgkmcnt(0)
	v_mfma_f32_32x32x16_f16 a[32:47], v[6:9], v[2:5], a[32:47]
	ds_read_b128 v[2:5], v33 offset:28672
	s_waitcnt lgkmcnt(0)
	v_mfma_f32_32x32x16_f16 a[48:63], v[6:9], v[2:5], a[48:63]
	ds_read_b128 v[2:5], v33 offset:17408
	s_waitcnt lgkmcnt(0)
	v_mfma_f32_32x32x16_f16 a[32:47], v[10:13], v[2:5], a[32:47]
	ds_read_b128 v[2:5], v33 offset:21504
	s_waitcnt lgkmcnt(0)
	v_mfma_f32_32x32x16_f16 a[48:63], v[10:13], v[2:5], a[48:63]
	ds_read_b128 v[2:5], v33 offset:25600
	s_waitcnt lgkmcnt(0)
	v_mfma_f32_32x32x16_f16 a[32:47], v[10:13], v[2:5], a[32:47]
	ds_read_b128 v[2:5], v33 offset:29696
	s_waitcnt lgkmcnt(0)
	v_mfma_f32_32x32x16_f16 a[48:63], v[10:13], v[2:5], a[48:63]
	ds_read_b128 v[2:5], v33 offset:18432
	s_waitcnt lgkmcnt(0)
	v_mfma_f32_32x32x16_f16 a[32:47], v[18:21], v[2:5], a[32:47]
	ds_read_b128 v[2:5], v33 offset:22528
	s_waitcnt lgkmcnt(0)
	v_mfma_f32_32x32x16_f16 a[48:63], v[18:21], v[2:5], a[48:63]
	ds_read_b128 v[2:5], v33 offset:26624
	s_waitcnt lgkmcnt(0)
	v_mfma_f32_32x32x16_f16 a[32:47], v[18:21], v[2:5], a[32:47]
	ds_read_b128 v[2:5], v33 offset:30720
	s_waitcnt lgkmcnt(0)
	v_mfma_f32_32x32x16_f16 a[48:63], v[18:21], v[2:5], a[48:63]
	ds_read_b128 v[2:5], v33 offset:19456
	s_waitcnt lgkmcnt(0)
	v_mfma_f32_32x32x16_f16 a[32:47], v[14:17], v[2:5], a[32:47]
	ds_read_b128 v[2:5], v33 offset:23552
	s_waitcnt lgkmcnt(0)
	v_mfma_f32_32x32x16_f16 a[48:63], v[14:17], v[2:5], a[48:63]
	ds_read_b128 v[2:5], v33 offset:27648
	s_waitcnt lgkmcnt(0)
	v_mfma_f32_32x32x16_f16 a[32:47], v[14:17], v[2:5], a[32:47]
	v_lshlrev_b32_e32 v2, 1, v71
	v_mov_b32_e32 v3, 0
	v_lshl_add_u64 v[2:3], v[26:27], 0, v[2:3]
	global_store_dwordx4 v[2:3], v[6:9], off
	global_store_dwordx4 v[2:3], v[10:13], off offset:16
	global_store_dwordx4 v[2:3], v[18:21], off offset:32
	global_store_dwordx4 v[2:3], v[14:17], off offset:48
	v_lshrrev_b32_e32 v2, 3, v0
	v_and_or_b32 v2, v2, 4, v69
	v_ashrrev_i32_e32 v3, 31, v2
	v_mfma_f32_32x32x16_f16 a[48:63], v[14:17], v[22:25], a[48:63]
	v_accvgpr_read_b32 v4, a0
	v_accvgpr_read_b32 v5, a16
	v_cvt_pk_bf16_f32 v8, v5, v4
	v_lshlrev_b64 v[4:5], 7, v[2:3]
	v_or_b32_e32 v4, v4, v1
	v_lshl_add_u64 v[6:7], s[6:7], 0, v[4:5]
	global_store_dword v[6:7], v8, off
	v_accvgpr_read_b32 v6, a32
	v_lshl_add_u64 v[4:5], s[10:11], 0, v[4:5]
	s_nop 2
	v_accvgpr_read_b32 v3, a48
	v_cvt_pk_bf16_f32 v3, v6, v3
	global_store_dword v[4:5], v3, off
	v_or_b32_e32 v4, 1, v2
	v_ashrrev_i32_e32 v5, 31, v4
	v_lshlrev_b64 v[4:5], 7, v[4:5]
	v_accvgpr_read_b32 v3, a1
	v_accvgpr_read_b32 v6, a17
	v_or_b32_e32 v4, v4, v1
	v_cvt_pk_bf16_f32 v3, v6, v3
	v_lshl_add_u64 v[6:7], s[6:7], 0, v[4:5]
	global_store_dword v[6:7], v3, off
	v_accvgpr_read_b32 v3, a49
	v_accvgpr_read_b32 v6, a33
	v_cvt_pk_bf16_f32 v3, v6, v3
	v_lshl_add_u64 v[4:5], s[10:11], 0, v[4:5]
	global_store_dword v[4:5], v3, off
	v_or_b32_e32 v4, 2, v2
	v_ashrrev_i32_e32 v5, 31, v4
	v_lshlrev_b64 v[4:5], 7, v[4:5]
	v_accvgpr_read_b32 v3, a2
	v_accvgpr_read_b32 v6, a18
	v_or_b32_e32 v4, v4, v1
	v_cvt_pk_bf16_f32 v3, v6, v3
	v_lshl_add_u64 v[6:7], s[6:7], 0, v[4:5]
	global_store_dword v[6:7], v3, off
	v_accvgpr_read_b32 v3, a50
	v_accvgpr_read_b32 v6, a34
	v_cvt_pk_bf16_f32 v3, v6, v3
	v_lshl_add_u64 v[4:5], s[10:11], 0, v[4:5]
	global_store_dword v[4:5], v3, off
	v_or_b32_e32 v4, 3, v2
	v_ashrrev_i32_e32 v5, 31, v4
	v_lshlrev_b64 v[4:5], 7, v[4:5]
	v_accvgpr_read_b32 v3, a3
	v_accvgpr_read_b32 v6, a19
	v_or_b32_e32 v4, v4, v1
	v_cvt_pk_bf16_f32 v3, v6, v3
	v_lshl_add_u64 v[6:7], s[6:7], 0, v[4:5]
	global_store_dword v[6:7], v3, off
	v_accvgpr_read_b32 v3, a51
	v_accvgpr_read_b32 v6, a35
	v_cvt_pk_bf16_f32 v3, v6, v3
	v_lshl_add_u64 v[4:5], s[10:11], 0, v[4:5]
	global_store_dword v[4:5], v3, off
	v_or_b32_e32 v4, 8, v2
	v_ashrrev_i32_e32 v5, 31, v4
	v_lshlrev_b64 v[4:5], 7, v[4:5]
	v_accvgpr_read_b32 v3, a4
	v_accvgpr_read_b32 v6, a20
	v_or_b32_e32 v4, v4, v1
	v_cvt_pk_bf16_f32 v3, v6, v3
	v_lshl_add_u64 v[6:7], s[6:7], 0, v[4:5]
	global_store_dword v[6:7], v3, off
	v_accvgpr_read_b32 v3, a52
	v_accvgpr_read_b32 v6, a36
	v_cvt_pk_bf16_f32 v3, v6, v3
	v_lshl_add_u64 v[4:5], s[10:11], 0, v[4:5]
	global_store_dword v[4:5], v3, off
	v_or_b32_e32 v4, 9, v2
	v_ashrrev_i32_e32 v5, 31, v4
	v_lshlrev_b64 v[4:5], 7, v[4:5]
	v_accvgpr_read_b32 v3, a5
	v_accvgpr_read_b32 v6, a21
	v_or_b32_e32 v4, v4, v1
	v_cvt_pk_bf16_f32 v3, v6, v3
	v_lshl_add_u64 v[6:7], s[6:7], 0, v[4:5]
	global_store_dword v[6:7], v3, off
	v_accvgpr_read_b32 v3, a53
	v_accvgpr_read_b32 v6, a37
	v_cvt_pk_bf16_f32 v3, v6, v3
	v_lshl_add_u64 v[4:5], s[10:11], 0, v[4:5]
	global_store_dword v[4:5], v3, off
	v_or_b32_e32 v4, 10, v2
	v_ashrrev_i32_e32 v5, 31, v4
	v_lshlrev_b64 v[4:5], 7, v[4:5]
	v_accvgpr_read_b32 v3, a6
	v_accvgpr_read_b32 v6, a22
	v_or_b32_e32 v4, v4, v1
	v_cvt_pk_bf16_f32 v3, v6, v3
	v_lshl_add_u64 v[6:7], s[6:7], 0, v[4:5]
	global_store_dword v[6:7], v3, off
	v_accvgpr_read_b32 v3, a54
	v_accvgpr_read_b32 v6, a38
	v_cvt_pk_bf16_f32 v3, v6, v3
	v_lshl_add_u64 v[4:5], s[10:11], 0, v[4:5]
	global_store_dword v[4:5], v3, off
	v_or_b32_e32 v4, 11, v2
	v_ashrrev_i32_e32 v5, 31, v4
	v_lshlrev_b64 v[4:5], 7, v[4:5]
	v_accvgpr_read_b32 v3, a7
	v_accvgpr_read_b32 v6, a23
	v_or_b32_e32 v4, v4, v1
	v_cvt_pk_bf16_f32 v3, v6, v3
	v_lshl_add_u64 v[6:7], s[6:7], 0, v[4:5]
	global_store_dword v[6:7], v3, off
	v_accvgpr_read_b32 v3, a55
	v_accvgpr_read_b32 v6, a39
	v_cvt_pk_bf16_f32 v3, v6, v3
	v_lshl_add_u64 v[4:5], s[10:11], 0, v[4:5]
	global_store_dword v[4:5], v3, off
	v_or_b32_e32 v4, 16, v2
	v_ashrrev_i32_e32 v5, 31, v4
	v_lshlrev_b64 v[4:5], 7, v[4:5]
	v_accvgpr_read_b32 v3, a8
	v_accvgpr_read_b32 v6, a24
	v_or_b32_e32 v4, v4, v1
	v_cvt_pk_bf16_f32 v3, v6, v3
	v_lshl_add_u64 v[6:7], s[6:7], 0, v[4:5]
	global_store_dword v[6:7], v3, off
	v_accvgpr_read_b32 v3, a56
	v_accvgpr_read_b32 v6, a40
	v_cvt_pk_bf16_f32 v3, v6, v3
	v_lshl_add_u64 v[4:5], s[10:11], 0, v[4:5]
	global_store_dword v[4:5], v3, off
	v_or_b32_e32 v4, 17, v2
	v_ashrrev_i32_e32 v5, 31, v4
	v_lshlrev_b64 v[4:5], 7, v[4:5]
	v_accvgpr_read_b32 v3, a9
	v_accvgpr_read_b32 v6, a25
	v_or_b32_e32 v4, v4, v1
	v_cvt_pk_bf16_f32 v3, v6, v3
	v_lshl_add_u64 v[6:7], s[6:7], 0, v[4:5]
	global_store_dword v[6:7], v3, off
	v_accvgpr_read_b32 v3, a57
	v_accvgpr_read_b32 v6, a41
	v_cvt_pk_bf16_f32 v3, v6, v3
	v_lshl_add_u64 v[4:5], s[10:11], 0, v[4:5]
	global_store_dword v[4:5], v3, off
	v_or_b32_e32 v4, 18, v2
	v_ashrrev_i32_e32 v5, 31, v4
	v_lshlrev_b64 v[4:5], 7, v[4:5]
	v_accvgpr_read_b32 v3, a10
	v_accvgpr_read_b32 v6, a26
	v_or_b32_e32 v4, v4, v1
	v_cvt_pk_bf16_f32 v3, v6, v3
	v_lshl_add_u64 v[6:7], s[6:7], 0, v[4:5]
	global_store_dword v[6:7], v3, off
	v_accvgpr_read_b32 v3, a58
	v_accvgpr_read_b32 v6, a42
	v_cvt_pk_bf16_f32 v3, v6, v3
	v_lshl_add_u64 v[4:5], s[10:11], 0, v[4:5]
	global_store_dword v[4:5], v3, off
	v_or_b32_e32 v4, 19, v2
	v_ashrrev_i32_e32 v5, 31, v4
	v_lshlrev_b64 v[4:5], 7, v[4:5]
	v_accvgpr_read_b32 v3, a11
	v_accvgpr_read_b32 v6, a27
	v_or_b32_e32 v4, v4, v1
	v_cvt_pk_bf16_f32 v3, v6, v3
	v_lshl_add_u64 v[6:7], s[6:7], 0, v[4:5]
	global_store_dword v[6:7], v3, off
	v_accvgpr_read_b32 v3, a59
	v_accvgpr_read_b32 v6, a43
	v_cvt_pk_bf16_f32 v3, v6, v3
	v_lshl_add_u64 v[4:5], s[10:11], 0, v[4:5]
	global_store_dword v[4:5], v3, off
	v_or_b32_e32 v4, 24, v2
	v_ashrrev_i32_e32 v5, 31, v4
	v_lshlrev_b64 v[4:5], 7, v[4:5]
	v_accvgpr_read_b32 v3, a12
	v_accvgpr_read_b32 v6, a28
	v_or_b32_e32 v4, v4, v1
	v_cvt_pk_bf16_f32 v3, v6, v3
	v_lshl_add_u64 v[6:7], s[6:7], 0, v[4:5]
	global_store_dword v[6:7], v3, off
	v_accvgpr_read_b32 v3, a60
	v_accvgpr_read_b32 v6, a44
	v_cvt_pk_bf16_f32 v3, v6, v3
	v_lshl_add_u64 v[4:5], s[10:11], 0, v[4:5]
	global_store_dword v[4:5], v3, off
	v_or_b32_e32 v4, 25, v2
	v_ashrrev_i32_e32 v5, 31, v4
	v_lshlrev_b64 v[4:5], 7, v[4:5]
	v_accvgpr_read_b32 v3, a13
	v_accvgpr_read_b32 v6, a29
	v_or_b32_e32 v4, v4, v1
	v_cvt_pk_bf16_f32 v3, v6, v3
	v_lshl_add_u64 v[6:7], s[6:7], 0, v[4:5]
	global_store_dword v[6:7], v3, off
	v_accvgpr_read_b32 v3, a61
	v_accvgpr_read_b32 v6, a45
	v_cvt_pk_bf16_f32 v3, v6, v3
	v_lshl_add_u64 v[4:5], s[10:11], 0, v[4:5]
	global_store_dword v[4:5], v3, off
	v_or_b32_e32 v4, 26, v2
	v_ashrrev_i32_e32 v5, 31, v4
	v_lshlrev_b64 v[4:5], 7, v[4:5]
	v_accvgpr_read_b32 v3, a14
	v_accvgpr_read_b32 v6, a30
	v_or_b32_e32 v4, v4, v1
	v_cvt_pk_bf16_f32 v3, v6, v3
	v_lshl_add_u64 v[6:7], s[6:7], 0, v[4:5]
	global_store_dword v[6:7], v3, off
	v_accvgpr_read_b32 v3, a62
	v_accvgpr_read_b32 v6, a46
	v_cvt_pk_bf16_f32 v3, v6, v3
	v_lshl_add_u64 v[4:5], s[10:11], 0, v[4:5]
	v_or_b32_e32 v2, 27, v2
	global_store_dword v[4:5], v3, off
	v_ashrrev_i32_e32 v3, 31, v2
	v_lshlrev_b64 v[2:3], 7, v[2:3]
	v_accvgpr_read_b32 v4, a15
	v_accvgpr_read_b32 v5, a31
	v_or_b32_e32 v2, v2, v1
	v_cvt_pk_bf16_f32 v6, v5, v4
	v_lshl_add_u64 v[4:5], s[6:7], 0, v[2:3]
	global_store_dword v[4:5], v6, off
	v_accvgpr_read_b32 v1, a63
	v_accvgpr_read_b32 v4, a47
	v_cvt_pk_bf16_f32 v1, v4, v1
	v_lshl_add_u64 v[2:3], s[10:11], 0, v[2:3]
	global_store_dword v[2:3], v1, off

_Z4k_U3ILb0EtEvPKtPtPKdPKfS6_PK15HIP_vector_typeIjLj4EES6_PT0_SC_S6_Pd:
	s_cmpk_ge_u32 s2, 0x300
	s_cbranch_scc1 .LBB9_4
	s_load_dwordx2 s[4:5], s[0:1], 0x28
	s_load_dwordx4 s[20:23], s[0:1], 0x0
	v_mov_b32_e32 v3, 0
	v_lshlrev_b32_e32 v2, 4, v0
	v_or_b32_e32 v1, 0x4000, v2
	s_movk_i32 s3, 0x1000
	s_waitcnt lgkmcnt(0)
	v_lshrrev_b32_e32 v78, 6, v0
	v_lshl_add_u32 v78, s2, 2, v78
	v_and_b32_e32 v79, 31, v0
	v_lshl_or_b32 v78, v78, 5, v79
	v_and_b32_e32 v79, 32, v0
	v_lshlrev_b32_e32 v78, 7, v78
	v_lshl_add_u32 v78, v79, 1, v78
	global_load_dwordx4 v[44:47], v78, s[22:23] offset:48
	global_load_dwordx4 v[48:51], v78, s[22:23] offset:32
	global_load_dwordx4 v[52:55], v78, s[22:23] offset:16
	global_load_dwordx4 v[56:59], v78, s[22:23]
	global_load_dwordx4 v[60:63], v78, s[20:21] offset:48
	global_load_dwordx4 v[64:67], v78, s[20:21] offset:32
	global_load_dwordx4 v[68:71], v78, s[20:21] offset:16
	global_load_dwordx4 v[72:75], v78, s[20:21]
	v_lshl_add_u64 v[32:33], s[4:5], 0, v[2:3]
	v_add_co_u32_e32 v24, vcc, 0x1000, v32
	global_load_dwordx4 v[4:7], v2, s[4:5]
	s_nop 0
	v_addc_co_u32_e32 v25, vcc, 0, v33, vcc
	v_add_co_u32_e32 v26, vcc, 0x2000, v32
	s_nop 1
	v_addc_co_u32_e32 v27, vcc, 0, v33, vcc
	v_add_co_u32_e32 v28, vcc, 0x3000, v32
	s_nop 1
	v_addc_co_u32_e32 v29, vcc, 0, v33, vcc
	v_add_co_u32_e32 v34, vcc, 0x5000, v32
	global_load_dwordx4 v[8:11], v[26:27], off
	global_load_dwordx4 v[12:15], v[28:29], off
	global_load_dwordx4 v[16:19], v[24:25], off
	global_load_dwordx4 v[20:23], v1, s[4:5]
	v_addc_co_u32_e32 v35, vcc, 0, v33, vcc
	v_add_co_u32_e32 v36, vcc, 0x6000, v32
	s_nop 1
	v_addc_co_u32_e32 v37, vcc, 0, v33, vcc
	global_load_dwordx4 v[24:27], v[34:35], off
	global_load_dwordx4 v[28:31], v[36:37], off
	v_add_co_u32_e32 v32, vcc, 0x7000, v32
	s_nop 1
	v_addc_co_u32_e32 v33, vcc, 0, v33, vcc
	global_load_dwordx4 v[32:35], v[32:33], off
	v_cmp_gt_u32_e32 vcc, 64, v0
	s_waitcnt vmcnt(7)
	ds_write_b128 v2, v[4:7]
	s_waitcnt vmcnt(4)
	ds_write_b128 v2, v[16:19] offset:4096
	s_waitcnt vmcnt(3)
	ds_write_b128 v2, v[20:23] offset:16384
	ds_write_b128 v2, v[8:11] offset:8192
	ds_write_b128 v2, v[12:15] offset:12288
	s_waitcnt vmcnt(2)
	ds_write_b128 v2, v[24:27] offset:20480
	s_waitcnt vmcnt(1)
	ds_write_b128 v2, v[28:31] offset:24576
	s_waitcnt vmcnt(0)
	ds_write_b128 v2, v[32:35] offset:28672
	v_lshlrev_b32_e32 v10, 2, v0
	s_and_saveexec_b64 s[6:7], vcc
	s_cbranch_execz .LBB9_2
	s_load_dwordx4 s[8:11], s[0:1], 0x10
	s_load_dwordx2 s[4:5], s[0:1], 0x20
	v_lshlrev_b32_e32 v2, 3, v0
	s_mov_b32 s12, 0
	s_brev_b32 s13, 8
	s_waitcnt lgkmcnt(0)
	global_load_dwordx2 v[6:7], v2, s[8:9]
	global_load_dwordx2 v[8:9], v2, s[8:9] offset:512
	global_load_dwordx2 v[12:13], v2, s[8:9] offset:1024
	global_load_dwordx2 v[14:15], v2, s[8:9] offset:1536
	global_load_dwordx2 v[16:17], v2, s[8:9] offset:2048
	global_load_dwordx2 v[18:19], v2, s[8:9] offset:2560
	global_load_dwordx2 v[20:21], v2, s[8:9] offset:3072
	global_load_dwordx2 v[22:23], v2, s[8:9] offset:3584
	v_lshl_add_u64 v[4:5], s[8:9], 0, v[2:3]
	v_add_co_u32_e32 v2, vcc, s3, v4
	s_mov_b32 s8, 0x88e368f1
	s_nop 0
	v_addc_co_u32_e32 v3, vcc, 0, v5, vcc
	global_load_dwordx2 v[4:5], v[2:3], off
	global_load_dwordx2 v[24:25], v[2:3], off offset:512
	global_load_dwordx2 v[26:27], v[2:3], off offset:1024
	global_load_dwordx2 v[28:29], v[2:3], off offset:1536
	global_load_dwordx2 v[30:31], v[2:3], off offset:2048
	global_load_dwordx2 v[32:33], v[2:3], off offset:2560
	global_load_dwordx2 v[34:35], v[2:3], off offset:3072
	global_load_dwordx2 v[36:37], v[2:3], off offset:3584
	global_load_dword v1, v10, s[10:11]
	global_load_dword v11, v10, s[4:5]
	s_mov_b32 s10, 0
	s_mov_b32 s11, 0x40f86a00
	s_mov_b32 s9, 0x3ee4f8b5
	v_mov_b32_e32 v38, 0x100
	v_mov_b32_e32 v39, 0xffffff80
	v_mov_b32_e32 v40, 0x260
	s_waitcnt vmcnt(17)
	v_add_f64 v[2:3], v[6:7], 0
	s_waitcnt vmcnt(16)
	v_add_f64 v[6:7], v[8:9], 0
	s_waitcnt vmcnt(15)
	v_add_f64 v[2:3], v[2:3], v[12:13]
	s_waitcnt vmcnt(14)
	v_add_f64 v[6:7], v[6:7], v[14:15]
	s_waitcnt vmcnt(13)
	v_add_f64 v[2:3], v[2:3], v[16:17]
	s_waitcnt vmcnt(12)
	v_add_f64 v[6:7], v[6:7], v[18:19]
	s_waitcnt vmcnt(11)
	v_add_f64 v[2:3], v[2:3], v[20:21]
	s_waitcnt vmcnt(10)
	v_add_f64 v[6:7], v[6:7], v[22:23]
	s_waitcnt vmcnt(9)
	v_add_f64 v[2:3], v[2:3], v[4:5]
	s_waitcnt vmcnt(8)
	v_add_f64 v[4:5], v[6:7], v[24:25]
	s_waitcnt vmcnt(7)
	v_add_f64 v[2:3], v[2:3], v[26:27]
	s_waitcnt vmcnt(6)
	v_add_f64 v[4:5], v[4:5], v[28:29]
	s_waitcnt vmcnt(5)
	v_add_f64 v[2:3], v[2:3], v[30:31]
	s_waitcnt vmcnt(4)
	v_add_f64 v[4:5], v[4:5], v[32:33]
	s_waitcnt vmcnt(3)
	v_add_f64 v[2:3], v[2:3], v[34:35]
	s_waitcnt vmcnt(2)
	v_add_f64 v[4:5], v[4:5], v[36:37]
	v_div_scale_f64 v[6:7], s[4:5], s[10:11], s[10:11], v[2:3]
	v_div_scale_f64 v[12:13], s[4:5], s[10:11], s[10:11], v[4:5]
	v_rcp_f64_e32 v[14:15], v[6:7]
	v_rcp_f64_e32 v[16:17], v[12:13]
	v_div_scale_f64 v[8:9], vcc, v[2:3], s[10:11], v[2:3]
	v_fma_f64 v[20:21], -v[6:7], v[14:15], 1.0
	v_fma_f64 v[22:23], -v[12:13], v[16:17], 1.0
	v_fmac_f64_e32 v[14:15], v[14:15], v[20:21]
	v_fmac_f64_e32 v[16:17], v[16:17], v[22:23]
	v_fma_f64 v[20:21], -v[6:7], v[14:15], 1.0
	v_fma_f64 v[22:23], -v[12:13], v[16:17], 1.0
	v_fmac_f64_e32 v[14:15], v[14:15], v[20:21]
	v_div_scale_f64 v[18:19], s[4:5], v[4:5], s[10:11], v[4:5]
	v_fmac_f64_e32 v[16:17], v[16:17], v[22:23]
	v_mul_f64 v[20:21], v[8:9], v[14:15]
	v_mul_f64 v[22:23], v[18:19], v[16:17]
	v_fma_f64 v[6:7], -v[6:7], v[20:21], v[8:9]
	v_fma_f64 v[8:9], -v[12:13], v[22:23], v[18:19]
	v_div_fmas_f64 v[6:7], v[6:7], v[14:15], v[20:21]
	s_mov_b64 vcc, s[4:5]
	v_div_fixup_f64 v[2:3], v[6:7], s[10:11], v[2:3]
	v_div_fmas_f64 v[6:7], v[8:9], v[16:17], v[22:23]
	v_div_fixup_f64 v[4:5], v[6:7], s[10:11], v[4:5]
	v_fma_f64 v[4:5], -v[2:3], v[2:3], v[4:5]
	v_cmp_ngt_f64_e32 vcc, 0, v[4:5]
	s_waitcnt vmcnt(1)
	v_cvt_f64_f32_e32 v[8:9], v1
	s_waitcnt vmcnt(0)
	v_cvt_f64_f32_e32 v[12:13], v11
	v_cndmask_b32_e32 v5, 0, v5, vcc
	v_cndmask_b32_e32 v4, 0, v4, vcc
	v_add_f64 v[4:5], v[4:5], s[8:9]
	v_cmp_gt_f64_e32 vcc, s[12:13], v[4:5]
	v_add_f64 v[2:3], v[2:3], 0
	s_nop 0
	v_cndmask_b32_e32 v6, 0, v38, vcc
	v_ldexp_f64 v[4:5], v[4:5], v6
	v_rsq_f64_e32 v[6:7], v[4:5]
	v_cndmask_b32_e32 v1, 0, v39, vcc
	v_cmp_class_f64_e32 vcc, v[4:5], v40
	v_mul_f64 v[14:15], v[4:5], v[6:7]
	v_mul_f64 v[6:7], v[6:7], 0.5
	v_fma_f64 v[16:17], -v[6:7], v[14:15], 0.5
	v_fmac_f64_e32 v[14:15], v[14:15], v[16:17]
	v_fmac_f64_e32 v[6:7], v[6:7], v[16:17]
	v_fma_f64 v[16:17], -v[14:15], v[14:15], v[4:5]
	v_fmac_f64_e32 v[14:15], v[16:17], v[6:7]
	v_fma_f64 v[16:17], -v[14:15], v[14:15], v[4:5]
	v_fmac_f64_e32 v[14:15], v[16:17], v[6:7]
	v_ldexp_f64 v[6:7], v[14:15], v1
	v_cndmask_b32_e32 v5, v7, v5, vcc
	v_cndmask_b32_e32 v4, v6, v4, vcc
	v_div_scale_f64 v[6:7], s[4:5], v[4:5], v[4:5], v[8:9]
	v_rcp_f64_e32 v[14:15], v[6:7]
	v_div_scale_f64 v[16:17], vcc, v[8:9], v[4:5], v[8:9]
	v_fma_f64 v[18:19], -v[6:7], v[14:15], 1.0
	v_fmac_f64_e32 v[14:15], v[14:15], v[18:19]
	v_fma_f64 v[18:19], -v[6:7], v[14:15], 1.0
	v_fmac_f64_e32 v[14:15], v[14:15], v[18:19]
	v_mul_f64 v[18:19], v[16:17], v[14:15]
	v_fma_f64 v[6:7], -v[6:7], v[18:19], v[16:17]
	v_div_fmas_f64 v[6:7], v[6:7], v[14:15], v[18:19]
	v_div_fixup_f64 v[4:5], v[6:7], v[4:5], v[8:9]
	v_fma_f64 v[2:3], -v[2:3], v[4:5], v[12:13]
	v_cvt_f32_f64_e32 v1, v[4:5]
	v_cvt_f32_f64_e32 v2, v[2:3]
	ds_write2st64_b32 v10, v1, v2 offset0:128 offset1:129
.LBB9_2:
	s_or_b64 exec, exec, s[6:7]
	s_waitcnt lgkmcnt(0)
	s_barrier
	s_mov_b32 s30, s2
	v_mov_b32_e32 v77, v0
	v_mov_b32_e32 v79, v10
	s_mov_b32 s31, 0
.Lu3_again:
	s_load_dword s3, s[0:1], 0x58
	v_lshrrev_b32_e32 v1, 6, v0
	s_waitcnt lgkmcnt(0)
	v_lshl_add_u32 v1, s2, 2, v1
	v_add_u32_e32 v1, s31, v1
	s_movk_i32 s2, 0xc35
	v_cmp_gt_i32_e32 vcc, s2, v1
	s_and_saveexec_b64 s[2:3], vcc
	s_cbranch_execz .LBB9_4
	s_load_dwordx4 s[4:7], s[0:1], 0x30
	s_load_dwordx2 s[2:3], s[0:1], 0x40
	s_load_dwordx4 s[8:11], s[0:1], 0x0
	v_and_b32_e32 v22, 31, v0
	v_lshlrev_b32_e32 v1, 5, v1
	v_or_b32_e32 v2, v1, v22
	v_ashrrev_i32_e32 v3, 31, v2
	v_lshlrev_b64 v[16:17], 7, v[2:3]
	v_and_b32_e32 v4, 32, v0
	s_waitcnt lgkmcnt(0)
	v_lshl_add_u64 v[2:3], s[10:11], 0, v[16:17]
	v_lshlrev_b32_e32 v28, 1, v4
	v_mov_b32_e32 v29, 0
	v_lshl_add_u64 v[18:19], v[2:3], 0, v[28:29]
	s_waitcnt vmcnt(0)
	v_mov_b32_e32 v2, v44
	v_mov_b32_e32 v3, v45
	v_mov_b32_e32 v4, v46
	v_mov_b32_e32 v5, v47
	v_mov_b32_e32 v6, v48
	v_mov_b32_e32 v7, v49
	v_mov_b32_e32 v8, v50
	v_mov_b32_e32 v9, v51
	v_mov_b32_e32 v12, v52
	v_mov_b32_e32 v13, v53
	v_mov_b32_e32 v14, v54
	v_mov_b32_e32 v15, v55
	v_mov_b32_e32 v24, v56
	v_mov_b32_e32 v25, v57
	v_mov_b32_e32 v26, v58
	v_mov_b32_e32 v27, v59
	v_lshl_add_u64 v[16:17], s[8:9], 0, v[16:17]
	v_lshl_add_u64 v[16:17], v[16:17], 0, v[28:29]
	v_and_b32_e32 v76, 0x80, v10
	v_and_b32_e32 v20, 63, v0
	v_lshrrev_b32_e32 v0, 3, v0
	v_and_or_b32 v0, v0, 4, v1
	v_ashrrev_i32_e32 v1, 31, v0
	s_waitcnt vmcnt(0)
	v_mov_b32_e32 v28, v60
	v_mov_b32_e32 v29, v61
	v_mov_b32_e32 v30, v62
	v_mov_b32_e32 v31, v63
	v_mov_b32_e32 v32, v64
	v_mov_b32_e32 v33, v65
	v_mov_b32_e32 v34, v66
	v_mov_b32_e32 v35, v67
	v_mov_b32_e32 v36, v68
	v_mov_b32_e32 v37, v69
	v_mov_b32_e32 v38, v70
	v_mov_b32_e32 v39, v71
	v_mov_b32_e32 v40, v72
	v_mov_b32_e32 v41, v73
	v_mov_b32_e32 v42, v74
	v_mov_b32_e32 v43, v75
	v_cvt_f32_f16_sdwa v17, v24 dst_sel:DWORD dst_unused:UNUSED_PAD src0_sel:WORD_1
	s_waitcnt vmcnt(0)
	v_lshlrev_b32_e32 v11, 16, v40
	v_and_b32_e32 v16, 0xffff0000, v40
	v_lshlrev_b32_e32 v21, 16, v41
	v_and_b32_e32 v23, 0xffff0000, v41
	v_lshlrev_b32_e32 v48, 16, v42
	v_and_b32_e32 v49, 0xffff0000, v42
	v_lshlrev_b32_e32 v50, 16, v43
	v_and_b32_e32 v51, 0xffff0000, v43
	v_lshlrev_b32_e32 v52, 16, v36
	v_and_b32_e32 v53, 0xffff0000, v36
	v_lshlrev_b32_e32 v54, 16, v37
	v_and_b32_e32 v55, 0xffff0000, v37
	v_lshlrev_b32_e32 v56, 16, v38
	v_and_b32_e32 v57, 0xffff0000, v38
	v_lshlrev_b32_e32 v58, 16, v39
	v_and_b32_e32 v59, 0xffff0000, v39
	v_lshlrev_b32_e32 v60, 16, v32
	v_and_b32_e32 v61, 0xffff0000, v32
	v_lshlrev_b32_e32 v62, 16, v33
	v_and_b32_e32 v63, 0xffff0000, v33
	v_lshlrev_b32_e32 v64, 16, v34
	v_and_b32_e32 v65, 0xffff0000, v34
	v_lshlrev_b32_e32 v66, 16, v35
	v_and_b32_e32 v67, 0xffff0000, v35
	v_lshlrev_b32_e32 v68, 16, v28
	v_and_b32_e32 v69, 0xffff0000, v28
	v_lshlrev_b32_e32 v70, 16, v29
	v_and_b32_e32 v71, 0xffff0000, v29
	v_lshlrev_b32_e32 v72, 16, v30
	v_and_b32_e32 v73, 0xffff0000, v30
	v_lshlrev_b32_e32 v74, 16, v31
	v_and_b32_e32 v75, 0xffff0000, v31
	ds_read_b128 v[28:31], v76 offset:32768
	ds_read_b128 v[32:35], v76 offset:32784
	ds_read_b128 v[36:39], v76 offset:32800
	ds_read_b128 v[40:43], v76 offset:32816
	ds_read_b128 v[44:47], v76 offset:33024
	s_waitcnt lgkmcnt(0)
	v_fma_f32 v10, v28, v11, v44
	v_fma_f32 v11, v29, v16, v45
	v_cvt_f32_f16_e32 v16, v24
	v_max_f32_e32 v10, 0, v10
	v_max_f32_e32 v11, 0, v11
	v_fmac_f32_e32 v47, v31, v23
	v_pk_add_f32 v[44:45], v[10:11], v[16:17]
	v_cvt_f32_f16_e32 v16, v25
	v_cvt_f32_f16_sdwa v17, v25 dst_sel:DWORD dst_unused:UNUSED_PAD src0_sel:WORD_1
	v_fma_f32 v10, v30, v21, v46
	ds_read_b128 v[28:31], v76 offset:33040
	v_max_f32_e32 v10, 0, v10
	v_max_f32_e32 v11, 0, v47
	v_pk_add_f32 v[46:47], v[10:11], v[16:17]
	v_cvt_f32_f16_e32 v16, v26
	v_cvt_f32_f16_sdwa v17, v26 dst_sel:DWORD dst_unused:UNUSED_PAD src0_sel:WORD_1
	s_waitcnt lgkmcnt(0)
	v_fma_f32 v10, v32, v48, v28
	v_fma_f32 v11, v33, v49, v29
	v_max_f32_e32 v10, 0, v10
	v_max_f32_e32 v11, 0, v11
	v_pk_add_f32 v[28:29], v[10:11], v[16:17]
	v_cvt_f32_f16_e32 v16, v27
	v_cvt_f32_f16_sdwa v17, v27 dst_sel:DWORD dst_unused:UNUSED_PAD src0_sel:WORD_1
	ds_read_b128 v[24:27], v76 offset:33056
	v_fma_f32 v10, v34, v50, v30
	v_fmac_f32_e32 v31, v35, v51
	v_max_f32_e32 v10, 0, v10
	v_max_f32_e32 v11, 0, v31
	v_pk_add_f32 v[30:31], v[10:11], v[16:17]
	v_cvt_f32_f16_e32 v16, v12
	v_cvt_f32_f16_sdwa v17, v12 dst_sel:DWORD dst_unused:UNUSED_PAD src0_sel:WORD_1
	s_waitcnt lgkmcnt(0)
	v_fma_f32 v10, v36, v52, v24
	v_fma_f32 v11, v37, v53, v25
	v_cvt_f32_f16_e32 v12, v13
	v_cvt_f32_f16_sdwa v13, v13 dst_sel:DWORD dst_unused:UNUSED_PAD src0_sel:WORD_1
	v_max_f32_e32 v10, 0, v10
	v_max_f32_e32 v11, 0, v11
	v_pk_add_f32 v[24:25], v[10:11], v[16:17]
	v_fma_f32 v10, v38, v54, v26
	v_fmac_f32_e32 v27, v39, v55
	v_max_f32_e32 v10, 0, v10
	v_max_f32_e32 v11, 0, v27
	v_pk_add_f32 v[26:27], v[10:11], v[12:13]
	ds_read_b128 v[10:13], v76 offset:33072
	v_cvt_f32_f16_e32 v16, v14
	v_cvt_f32_f16_sdwa v17, v14 dst_sel:DWORD dst_unused:UNUSED_PAD src0_sel:WORD_1
	v_lshlrev_b32_e32 v23, 4, v20
	s_waitcnt lgkmcnt(0)
	v_fma_f32 v10, v40, v56, v10
	v_fma_f32 v11, v41, v57, v11
	v_max_f32_e32 v10, 0, v10
	v_max_f32_e32 v11, 0, v11
	v_fmac_f32_e32 v13, v43, v59
	v_pk_add_f32 v[32:33], v[10:11], v[16:17]
	v_fma_f32 v10, v42, v58, v12
	v_max_f32_e32 v11, 0, v13
	v_cvt_f32_f16_e32 v12, v15
	v_cvt_f32_f16_sdwa v13, v15 dst_sel:DWORD dst_unused:UNUSED_PAD src0_sel:WORD_1
	v_max_f32_e32 v10, 0, v10
	v_pk_add_f32 v[34:35], v[10:11], v[12:13]
	ds_read_b128 v[10:13], v76 offset:32832
	ds_read_b128 v[14:17], v76 offset:33088
	s_waitcnt lgkmcnt(0)
	v_fma_f32 v10, v10, v60, v14
	v_fma_f32 v11, v11, v61, v15
	v_cvt_f32_f16_e32 v14, v6
	v_cvt_f32_f16_sdwa v15, v6 dst_sel:DWORD dst_unused:UNUSED_PAD src0_sel:WORD_1
	v_max_f32_e32 v10, 0, v10
	v_max_f32_e32 v11, 0, v11
	v_fma_f32 v6, v12, v62, v16
	v_pk_add_f32 v[36:37], v[10:11], v[14:15]
	v_max_f32_e32 v10, 0, v6
	v_cvt_f32_f16_e32 v6, v7
	v_cvt_f32_f16_sdwa v7, v7 dst_sel:DWORD dst_unused:UNUSED_PAD src0_sel:WORD_1
	v_fmac_f32_e32 v17, v13, v63
	v_max_f32_e32 v11, 0, v17
	v_pk_add_f32 v[38:39], v[10:11], v[6:7]
	ds_read_b128 v[10:13], v76 offset:32848
	ds_read_b128 v[14:17], v76 offset:33104
	s_waitcnt lgkmcnt(0)
	v_fma_f32 v6, v10, v64, v14
	v_fma_f32 v7, v11, v65, v15
	v_cvt_f32_f16_e32 v10, v8
	v_cvt_f32_f16_sdwa v11, v8 dst_sel:DWORD dst_unused:UNUSED_PAD src0_sel:WORD_1
	v_cvt_f32_f16_e32 v8, v9
	v_cvt_f32_f16_sdwa v9, v9 dst_sel:DWORD dst_unused:UNUSED_PAD src0_sel:WORD_1
	v_max_f32_e32 v6, 0, v6
	v_max_f32_e32 v7, 0, v7
	v_pk_add_f32 v[40:41], v[6:7], v[10:11]
	v_fma_f32 v6, v12, v66, v16
	v_fmac_f32_e32 v17, v13, v67
	v_max_f32_e32 v6, 0, v6
	v_max_f32_e32 v7, 0, v17
	v_pk_add_f32 v[42:43], v[6:7], v[8:9]
	ds_read_b128 v[6:9], v76 offset:32864
	ds_read_b128 v[10:13], v76 offset:33120
	v_cvt_pk_f16_f32 v14, v44, v45
	v_cvt_pk_f16_f32 v15, v46, v47
	v_cvt_pk_f16_f32 v16, v28, v29
	v_cvt_pk_f16_f32 v17, v30, v31
	s_waitcnt lgkmcnt(0)
	v_fma_f32 v6, v6, v68, v10
	v_fma_f32 v7, v7, v69, v11
	v_cvt_f32_f16_e32 v10, v2
	v_cvt_f32_f16_sdwa v11, v2 dst_sel:DWORD dst_unused:UNUSED_PAD src0_sel:WORD_1
	v_max_f32_e32 v6, 0, v6
	v_max_f32_e32 v7, 0, v7
	v_fma_f32 v2, v8, v70, v12
	v_pk_add_f32 v[48:49], v[6:7], v[10:11]
	v_max_f32_e32 v6, 0, v2
	v_cvt_f32_f16_e32 v2, v3
	v_cvt_f32_f16_sdwa v3, v3 dst_sel:DWORD dst_unused:UNUSED_PAD src0_sel:WORD_1
	v_fmac_f32_e32 v13, v9, v71
	v_max_f32_e32 v7, 0, v13
	v_pk_add_f32 v[50:51], v[6:7], v[2:3]
	ds_read_b128 v[6:9], v76 offset:32880
	ds_read_b128 v[10:13], v76 offset:33136
	global_store_dwordx4 v[18:19], v[14:17], off
	s_waitcnt lgkmcnt(0)
	v_fma_f32 v2, v6, v72, v10
	v_fma_f32 v3, v7, v73, v11
	v_cvt_f32_f16_e32 v6, v4
	v_cvt_f32_f16_sdwa v7, v4 dst_sel:DWORD dst_unused:UNUSED_PAD src0_sel:WORD_1
	v_cvt_f32_f16_e32 v4, v5
	v_cvt_f32_f16_sdwa v5, v5 dst_sel:DWORD dst_unused:UNUSED_PAD src0_sel:WORD_1
	v_max_f32_e32 v2, 0, v2
	v_max_f32_e32 v3, 0, v3
	v_pk_add_f32 v[52:53], v[2:3], v[6:7]
	v_fma_f32 v2, v8, v74, v12
	v_fmac_f32_e32 v13, v9, v75
	v_max_f32_e32 v2, 0, v2
	v_max_f32_e32 v3, 0, v13
	v_pk_add_f32 v[54:55], v[2:3], v[4:5]
	v_cvt_pk_f16_f32 v10, v24, v25
	v_cvt_pk_f16_f32 v11, v26, v27
	v_cvt_pk_f16_f32 v12, v32, v33
	v_cvt_pk_f16_f32 v13, v34, v35
	v_cvt_pk_f16_f32 v6, v36, v37
	v_cvt_pk_f16_f32 v7, v38, v39
	v_cvt_pk_f16_f32 v8, v40, v41
	v_cvt_pk_f16_f32 v9, v42, v43
	v_cvt_pk_f16_f32 v2, v48, v49
	v_cvt_pk_f16_f32 v3, v50, v51
	v_cvt_pk_f16_f32 v4, v52, v53
	v_cvt_pk_f16_f32 v5, v54, v55
	global_store_dwordx4 v[18:19], v[10:13], off offset:16
	global_store_dwordx4 v[18:19], v[6:9], off offset:32
	global_store_dwordx4 v[18:19], v[2:5], off offset:48
	v_lshlrev_b32_e32 v18, 3, v22
	global_load_dwordx2 a[0:1], v18, s[4:5]
	ds_read_b128 v[18:21], v23
	ds_read_b128 v[24:27], v23 offset:8192
	ds_read_b128 v[28:31], v23 offset:4096
	ds_read_b128 v[32:35], v23 offset:12288
	s_waitcnt vmcnt(0)
	v_accvgpr_mov_b32 a16, a0
	v_accvgpr_mov_b32 a17, a0
	v_accvgpr_mov_b32 a18, a0
	v_accvgpr_mov_b32 a19, a0
	v_accvgpr_mov_b32 a20, a0
	v_accvgpr_mov_b32 a21, a0
	v_accvgpr_mov_b32 a22, a0
	v_accvgpr_mov_b32 a23, a0
	v_accvgpr_mov_b32 a24, a0
	v_accvgpr_mov_b32 a25, a0
	v_accvgpr_mov_b32 a26, a0
	v_accvgpr_mov_b32 a27, a0
	v_accvgpr_mov_b32 a28, a0
	v_accvgpr_mov_b32 a29, a0
	v_accvgpr_mov_b32 a30, a0
	v_accvgpr_mov_b32 a31, a0
	v_accvgpr_mov_b32 a0, a1
	v_accvgpr_mov_b32 a2, a1
	v_accvgpr_mov_b32 a3, a1
	v_accvgpr_mov_b32 a4, a1
	v_accvgpr_mov_b32 a5, a1
	v_accvgpr_mov_b32 a6, a1
	v_accvgpr_mov_b32 a7, a1
	v_accvgpr_mov_b32 a8, a1
	v_accvgpr_mov_b32 a9, a1
	v_accvgpr_mov_b32 a10, a1
	v_accvgpr_mov_b32 a11, a1
	v_accvgpr_mov_b32 a12, a1
	v_accvgpr_mov_b32 a13, a1
	v_accvgpr_mov_b32 a14, a1
	v_accvgpr_mov_b32 a15, a1
	s_waitcnt lgkmcnt(3)
	v_mfma_f32_32x32x16_f16 a[16:31], v[14:17], v[18:21], a[16:31]
	s_waitcnt lgkmcnt(1)
	v_mfma_f32_32x32x16_f16 a[0:15], v[14:17], v[28:31], a[0:15]
	v_mfma_f32_32x32x16_f16 a[16:31], v[14:17], v[24:27], a[16:31]
	s_waitcnt lgkmcnt(0)
	v_mfma_f32_32x32x16_f16 a[0:15], v[14:17], v[32:35], a[0:15]
	ds_read_b128 v[18:21], v23 offset:1024
	ds_read_b128 v[24:27], v23 offset:9216
	ds_read_b128 v[28:31], v23 offset:5120
	ds_read_b128 v[32:35], v23 offset:13312
	s_waitcnt lgkmcnt(3)
	v_mfma_f32_32x32x16_f16 a[16:31], v[10:13], v[18:21], a[16:31]
	s_waitcnt lgkmcnt(1)
	v_mfma_f32_32x32x16_f16 a[0:15], v[10:13], v[28:31], a[0:15]
	v_mfma_f32_32x32x16_f16 a[16:31], v[10:13], v[24:27], a[16:31]
	s_waitcnt lgkmcnt(0)
	v_mfma_f32_32x32x16_f16 a[0:15], v[10:13], v[32:35], a[0:15]
	ds_read_b128 v[18:21], v23 offset:2048
	ds_read_b128 v[24:27], v23 offset:10240
	ds_read_b128 v[28:31], v23 offset:6144
	ds_read_b128 v[32:35], v23 offset:14336
	s_waitcnt lgkmcnt(3)
	v_mfma_f32_32x32x16_f16 a[16:31], v[6:9], v[18:21], a[16:31]
	s_waitcnt lgkmcnt(1)
	v_mfma_f32_32x32x16_f16 a[0:15], v[6:9], v[28:31], a[0:15]
	v_mfma_f32_32x32x16_f16 a[16:31], v[6:9], v[24:27], a[16:31]
	s_waitcnt lgkmcnt(0)
	v_mfma_f32_32x32x16_f16 a[0:15], v[6:9], v[32:35], a[0:15]
	ds_read_b128 v[18:21], v23 offset:3072
	ds_read_b128 v[24:27], v23 offset:11264
	ds_read_b128 v[28:31], v23 offset:7168
	ds_read_b128 v[32:35], v23 offset:15360
	s_waitcnt lgkmcnt(3)
	v_mfma_f32_32x32x16_f16 a[16:31], v[2:5], v[18:21], a[16:31]
	s_waitcnt lgkmcnt(1)
	v_mfma_f32_32x32x16_f16 a[0:15], v[2:5], v[28:31], a[0:15]
	v_mfma_f32_32x32x16_f16 a[16:31], v[2:5], v[24:27], a[16:31]
	s_waitcnt lgkmcnt(0)
	v_mfma_f32_32x32x16_f16 a[0:15], v[2:5], v[32:35], a[0:15]
	ds_read_b128 v[18:21], v23 offset:16384
	ds_read_b128 v[24:27], v23 offset:24576
	ds_read_b128 v[28:31], v23 offset:20480
	ds_read_b128 v[32:35], v23 offset:28672
	s_waitcnt lgkmcnt(3)
	v_mfma_f32_32x32x16_f16 a[32:47], v[14:17], v[18:21], 0
	s_waitcnt lgkmcnt(1)
	v_mfma_f32_32x32x16_f16 a[48:63], v[14:17], v[28:31], 0
	v_mfma_f32_32x32x16_f16 a[32:47], v[14:17], v[24:27], a[32:47]
	s_waitcnt lgkmcnt(0)
	v_mfma_f32_32x32x16_f16 a[48:63], v[14:17], v[32:35], a[48:63]
	ds_read_b128 v[14:17], v23 offset:17408
	ds_read_b128 v[18:21], v23 offset:25600
	ds_read_b128 v[24:27], v23 offset:21504
	ds_read_b128 v[28:31], v23 offset:29696
	s_waitcnt lgkmcnt(3)
	v_mfma_f32_32x32x16_f16 a[32:47], v[10:13], v[14:17], a[32:47]
	s_waitcnt lgkmcnt(1)
	v_mfma_f32_32x32x16_f16 a[48:63], v[10:13], v[24:27], a[48:63]
	v_mfma_f32_32x32x16_f16 a[32:47], v[10:13], v[18:21], a[32:47]
	s_waitcnt lgkmcnt(0)
	v_mfma_f32_32x32x16_f16 a[48:63], v[10:13], v[28:31], a[48:63]
	ds_read_b128 v[10:13], v23 offset:18432
	ds_read_b128 v[14:17], v23 offset:26624
	ds_read_b128 v[18:21], v23 offset:22528
	ds_read_b128 v[24:27], v23 offset:30720
	s_waitcnt lgkmcnt(3)
	v_mfma_f32_32x32x16_f16 a[32:47], v[6:9], v[10:13], a[32:47]
	s_waitcnt lgkmcnt(1)
	v_mfma_f32_32x32x16_f16 a[48:63], v[6:9], v[18:21], a[48:63]
	v_mfma_f32_32x32x16_f16 a[32:47], v[6:9], v[14:17], a[32:47]
	s_waitcnt lgkmcnt(0)
	v_mfma_f32_32x32x16_f16 a[48:63], v[6:9], v[24:27], a[48:63]
	ds_read_b128 v[10:13], v23 offset:19456
	ds_read_b128 v[6:9], v23 offset:27648
	ds_read_b128 v[18:21], v23 offset:23552
	ds_read_b128 v[14:17], v23 offset:31744
	s_waitcnt lgkmcnt(3)
	v_mfma_f32_32x32x16_f16 a[32:47], v[2:5], v[10:13], a[32:47]
	s_waitcnt lgkmcnt(1)
	v_mfma_f32_32x32x16_f16 a[48:63], v[2:5], v[18:21], a[48:63]
	v_mfma_f32_32x32x16_f16 a[32:47], v[2:5], v[6:9], a[32:47]
	v_lshlrev_b32_e32 v7, 2, v22
	s_waitcnt lgkmcnt(0)
	v_mfma_f32_32x32x16_f16 a[48:63], v[2:5], v[14:17], a[48:63]
	v_accvgpr_read_b32 v2, a0
	v_accvgpr_read_b32 v3, a16
	v_cvt_pk_bf16_f32 v6, v3, v2
	v_lshlrev_b64 v[2:3], 7, v[0:1]
	v_or_b32_e32 v2, v2, v7
	v_lshl_add_u64 v[4:5], s[6:7], 0, v[2:3]
	global_store_dword v[4:5], v6, off
	s_nop 1
	v_accvgpr_read_b32 v4, a32
	v_lshl_add_u64 v[2:3], s[2:3], 0, v[2:3]
	s_nop 0
	v_accvgpr_read_b32 v1, a48
	v_cvt_pk_bf16_f32 v1, v4, v1
	global_store_dword v[2:3], v1, off
	v_or_b32_e32 v2, 1, v0
	v_ashrrev_i32_e32 v3, 31, v2
	v_lshlrev_b64 v[2:3], 7, v[2:3]
	v_accvgpr_read_b32 v1, a1
	v_accvgpr_read_b32 v4, a17
	v_or_b32_e32 v2, v2, v7
	v_cvt_pk_bf16_f32 v1, v4, v1
	v_lshl_add_u64 v[4:5], s[6:7], 0, v[2:3]
	global_store_dword v[4:5], v1, off
	v_accvgpr_read_b32 v1, a49
	v_accvgpr_read_b32 v4, a33
	v_cvt_pk_bf16_f32 v1, v4, v1
	v_lshl_add_u64 v[2:3], s[2:3], 0, v[2:3]
	global_store_dword v[2:3], v1, off
	v_or_b32_e32 v2, 2, v0
	v_ashrrev_i32_e32 v3, 31, v2
	v_lshlrev_b64 v[2:3], 7, v[2:3]
	v_accvgpr_read_b32 v1, a2
	v_accvgpr_read_b32 v4, a18
	v_or_b32_e32 v2, v2, v7
	v_cvt_pk_bf16_f32 v1, v4, v1
	v_lshl_add_u64 v[4:5], s[6:7], 0, v[2:3]
	global_store_dword v[4:5], v1, off
	v_accvgpr_read_b32 v1, a50
	v_accvgpr_read_b32 v4, a34
	v_cvt_pk_bf16_f32 v1, v4, v1
	v_lshl_add_u64 v[2:3], s[2:3], 0, v[2:3]
	global_store_dword v[2:3], v1, off
	v_or_b32_e32 v2, 3, v0
	v_ashrrev_i32_e32 v3, 31, v2
	v_lshlrev_b64 v[2:3], 7, v[2:3]
	v_accvgpr_read_b32 v1, a3
	v_accvgpr_read_b32 v4, a19
	v_or_b32_e32 v2, v2, v7
	v_cvt_pk_bf16_f32 v1, v4, v1
	v_lshl_add_u64 v[4:5], s[6:7], 0, v[2:3]
	global_store_dword v[4:5], v1, off
	v_accvgpr_read_b32 v1, a51
	v_accvgpr_read_b32 v4, a35
	v_cvt_pk_bf16_f32 v1, v4, v1
	v_lshl_add_u64 v[2:3], s[2:3], 0, v[2:3]
	global_store_dword v[2:3], v1, off
	v_or_b32_e32 v2, 8, v0
	v_ashrrev_i32_e32 v3, 31, v2
	v_lshlrev_b64 v[2:3], 7, v[2:3]
	v_accvgpr_read_b32 v1, a4
	v_accvgpr_read_b32 v4, a20
	v_or_b32_e32 v2, v2, v7
	v_cvt_pk_bf16_f32 v1, v4, v1
	v_lshl_add_u64 v[4:5], s[6:7], 0, v[2:3]
	global_store_dword v[4:5], v1, off
	v_accvgpr_read_b32 v1, a52
	v_accvgpr_read_b32 v4, a36
	v_cvt_pk_bf16_f32 v1, v4, v1
	v_lshl_add_u64 v[2:3], s[2:3], 0, v[2:3]
	global_store_dword v[2:3], v1, off
	v_or_b32_e32 v2, 9, v0
	v_ashrrev_i32_e32 v3, 31, v2
	v_lshlrev_b64 v[2:3], 7, v[2:3]
	v_accvgpr_read_b32 v1, a5
	v_accvgpr_read_b32 v4, a21
	v_or_b32_e32 v2, v2, v7
	v_cvt_pk_bf16_f32 v1, v4, v1
	v_lshl_add_u64 v[4:5], s[6:7], 0, v[2:3]
	global_store_dword v[4:5], v1, off
	v_accvgpr_read_b32 v1, a53
	v_accvgpr_read_b32 v4, a37
	v_cvt_pk_bf16_f32 v1, v4, v1
	v_lshl_add_u64 v[2:3], s[2:3], 0, v[2:3]
	global_store_dword v[2:3], v1, off
	v_or_b32_e32 v2, 10, v0
	v_ashrrev_i32_e32 v3, 31, v2
	v_lshlrev_b64 v[2:3], 7, v[2:3]
	v_accvgpr_read_b32 v1, a6
	v_accvgpr_read_b32 v4, a22
	v_or_b32_e32 v2, v2, v7
	v_cvt_pk_bf16_f32 v1, v4, v1
	v_lshl_add_u64 v[4:5], s[6:7], 0, v[2:3]
	global_store_dword v[4:5], v1, off
	v_accvgpr_read_b32 v1, a54
	v_accvgpr_read_b32 v4, a38
	v_cvt_pk_bf16_f32 v1, v4, v1
	v_lshl_add_u64 v[2:3], s[2:3], 0, v[2:3]
	global_store_dword v[2:3], v1, off
	v_or_b32_e32 v2, 11, v0
	v_ashrrev_i32_e32 v3, 31, v2
	v_lshlrev_b64 v[2:3], 7, v[2:3]
	v_accvgpr_read_b32 v1, a7
	v_accvgpr_read_b32 v4, a23
	v_or_b32_e32 v2, v2, v7
	v_cvt_pk_bf16_f32 v1, v4, v1
	v_lshl_add_u64 v[4:5], s[6:7], 0, v[2:3]
	global_store_dword v[4:5], v1, off
	v_accvgpr_read_b32 v1, a55
	v_accvgpr_read_b32 v4, a39
	v_cvt_pk_bf16_f32 v1, v4, v1
	v_lshl_add_u64 v[2:3], s[2:3], 0, v[2:3]
	global_store_dword v[2:3], v1, off
	v_or_b32_e32 v2, 16, v0
	v_ashrrev_i32_e32 v3, 31, v2
	v_lshlrev_b64 v[2:3], 7, v[2:3]
	v_accvgpr_read_b32 v1, a8
	v_accvgpr_read_b32 v4, a24
	v_or_b32_e32 v2, v2, v7
	v_cvt_pk_bf16_f32 v1, v4, v1
	v_lshl_add_u64 v[4:5], s[6:7], 0, v[2:3]
	global_store_dword v[4:5], v1, off
	v_accvgpr_read_b32 v1, a56
	v_accvgpr_read_b32 v4, a40
	v_cvt_pk_bf16_f32 v1, v4, v1
	v_lshl_add_u64 v[2:3], s[2:3], 0, v[2:3]
	global_store_dword v[2:3], v1, off
	v_or_b32_e32 v2, 17, v0
	v_ashrrev_i32_e32 v3, 31, v2
	v_lshlrev_b64 v[2:3], 7, v[2:3]
	v_accvgpr_read_b32 v1, a9
	v_accvgpr_read_b32 v4, a25
	v_or_b32_e32 v2, v2, v7
	v_cvt_pk_bf16_f32 v1, v4, v1
	v_lshl_add_u64 v[4:5], s[6:7], 0, v[2:3]
	global_store_dword v[4:5], v1, off
	v_accvgpr_read_b32 v1, a57
	v_accvgpr_read_b32 v4, a41
	v_cvt_pk_bf16_f32 v1, v4, v1
	v_lshl_add_u64 v[2:3], s[2:3], 0, v[2:3]
	global_store_dword v[2:3], v1, off
	v_or_b32_e32 v2, 18, v0
	v_ashrrev_i32_e32 v3, 31, v2
	v_lshlrev_b64 v[2:3], 7, v[2:3]
	v_accvgpr_read_b32 v1, a10
	v_accvgpr_read_b32 v4, a26
	v_or_b32_e32 v2, v2, v7
	v_cvt_pk_bf16_f32 v1, v4, v1
	v_lshl_add_u64 v[4:5], s[6:7], 0, v[2:3]
	global_store_dword v[4:5], v1, off
	v_accvgpr_read_b32 v1, a58
	v_accvgpr_read_b32 v4, a42
	v_cvt_pk_bf16_f32 v1, v4, v1
	v_lshl_add_u64 v[2:3], s[2:3], 0, v[2:3]
	global_store_dword v[2:3], v1, off
	v_or_b32_e32 v2, 19, v0
	v_ashrrev_i32_e32 v3, 31, v2
	v_lshlrev_b64 v[2:3], 7, v[2:3]
	v_accvgpr_read_b32 v1, a11
	v_accvgpr_read_b32 v4, a27
	v_or_b32_e32 v2, v2, v7
	v_cvt_pk_bf16_f32 v1, v4, v1
	v_lshl_add_u64 v[4:5], s[6:7], 0, v[2:3]
	global_store_dword v[4:5], v1, off
	v_accvgpr_read_b32 v1, a59
	v_accvgpr_read_b32 v4, a43
	v_cvt_pk_bf16_f32 v1, v4, v1
	v_lshl_add_u64 v[2:3], s[2:3], 0, v[2:3]
	global_store_dword v[2:3], v1, off
	v_or_b32_e32 v2, 24, v0
	v_ashrrev_i32_e32 v3, 31, v2
	v_lshlrev_b64 v[2:3], 7, v[2:3]
	v_accvgpr_read_b32 v1, a12
	v_accvgpr_read_b32 v4, a28
	v_or_b32_e32 v2, v2, v7
	v_cvt_pk_bf16_f32 v1, v4, v1
	v_lshl_add_u64 v[4:5], s[6:7], 0, v[2:3]
	global_store_dword v[4:5], v1, off
	v_accvgpr_read_b32 v1, a60
	v_accvgpr_read_b32 v4, a44
	v_cvt_pk_bf16_f32 v1, v4, v1
	v_lshl_add_u64 v[2:3], s[2:3], 0, v[2:3]
	global_store_dword v[2:3], v1, off
	v_or_b32_e32 v2, 25, v0
	v_ashrrev_i32_e32 v3, 31, v2
	v_lshlrev_b64 v[2:3], 7, v[2:3]
	v_accvgpr_read_b32 v1, a13
	v_accvgpr_read_b32 v4, a29
	v_or_b32_e32 v2, v2, v7
	v_cvt_pk_bf16_f32 v1, v4, v1
	v_lshl_add_u64 v[4:5], s[6:7], 0, v[2:3]
	global_store_dword v[4:5], v1, off
	v_accvgpr_read_b32 v1, a61
	v_accvgpr_read_b32 v4, a45
	v_cvt_pk_bf16_f32 v1, v4, v1
	v_lshl_add_u64 v[2:3], s[2:3], 0, v[2:3]
	global_store_dword v[2:3], v1, off
	v_or_b32_e32 v2, 26, v0
	v_ashrrev_i32_e32 v3, 31, v2
	v_lshlrev_b64 v[2:3], 7, v[2:3]
	v_accvgpr_read_b32 v1, a14
	v_accvgpr_read_b32 v4, a30
	v_or_b32_e32 v2, v2, v7
	v_cvt_pk_bf16_f32 v1, v4, v1
	v_lshl_add_u64 v[4:5], s[6:7], 0, v[2:3]
	global_store_dword v[4:5], v1, off
	v_accvgpr_read_b32 v1, a62
	v_accvgpr_read_b32 v4, a46
	v_cvt_pk_bf16_f32 v1, v4, v1
	v_lshl_add_u64 v[2:3], s[2:3], 0, v[2:3]
	v_or_b32_e32 v0, 27, v0
	global_store_dword v[2:3], v1, off
	v_ashrrev_i32_e32 v1, 31, v0
	v_lshlrev_b64 v[0:1], 7, v[0:1]
	v_accvgpr_read_b32 v2, a15
	v_accvgpr_read_b32 v3, a31
	v_or_b32_e32 v0, v0, v7
	v_cvt_pk_bf16_f32 v4, v3, v2
	v_lshl_add_u64 v[2:3], s[6:7], 0, v[0:1]
	global_store_dword v[2:3], v4, off
	v_accvgpr_read_b32 v2, a63
	v_accvgpr_read_b32 v3, a47
	v_cvt_pk_bf16_f32 v2, v3, v2
	v_lshl_add_u64 v[0:1], s[2:3], 0, v[0:1]
	global_store_dword v[0:1], v2, off
	s_cmp_lg_u32 s31, 0
	s_cbranch_scc1 .LBB9_4
	s_mov_b64 exec, -1
	v_lshrrev_b32_e32 v78, 6, v77
	s_lshl_b32 s33, s30, 2
	v_readfirstlane_b32 s32, v78
	s_add_i32 s32, s32, s33
	s_cmp_ge_u32 s32, 53
	s_cbranch_scc1 .LBB9_4
	s_movk_i32 s31, 0xc00
	s_mov_b32 s2, s30
	v_mov_b32_e32 v0, v77
	v_mov_b32_e32 v10, v79
	s_add_i32 s32, s32, 0xc00
	s_lshl_b32 s32, s32, 5
	v_and_b32_e32 v78, 31, v0
	v_or_b32_e32 v78, s32, v78
	v_lshlrev_b32_e32 v78, 7, v78
	v_and_b32_e32 v1, 32, v0
	v_lshl_add_u32 v78, v1, 1, v78
	global_load_dwordx4 v[44:47], v78, s[22:23] offset:48
	global_load_dwordx4 v[48:51], v78, s[22:23] offset:32
	global_load_dwordx4 v[52:55], v78, s[22:23] offset:16
	global_load_dwordx4 v[56:59], v78, s[22:23]
	global_load_dwordx4 v[60:63], v78, s[20:21] offset:48
	global_load_dwordx4 v[64:67], v78, s[20:21] offset:32
	global_load_dwordx4 v[68:71], v78, s[20:21] offset:16
	global_load_dwordx4 v[72:75], v78, s[20:21]
	s_waitcnt vmcnt(0)
	s_branch .Lu3_again
